# v5 + GEMM K-loops: first iteration peeled with C=0 on each accumulator's first MFMA, the 127 accumulator-zeroing v_mov per unit removed (8 loops)
# speedup vs baseline: 1.0132x; 1.0006x over previous
.LBB0_243:
	s_ashr_i32 s17, s16, 31
	s_lshl_b64 s[18:19], s[16:17], 19
	s_add_u32 s18, s72, s18
	s_addc_u32 s19, s73, s19
	s_and_b64 s[20:21], s[0:1], exec
	s_cselect_b32 s17, s19, s25
	s_cselect_b32 s47, s18, s24
	s_ashr_i32 s15, s14, 31
	s_lshl_b64 s[20:21], s[14:15], 19
	s_add_u32 s20, s30, s20
	s_addc_u32 s21, s31, s21
	s_and_b64 s[28:29], s[0:1], exec
	s_cselect_b32 s15, s21, s27
	s_cselect_b32 s48, s20, s26
	s_add_u32 s24, s24, 0x40080
	s_addc_u32 s25, s25, 0
	s_add_u32 s49, s26, 0x100
	v_mov_b32_e32 v2, 0
	s_addc_u32 s50, s27, 0
	s_mov_b32 s51, -2
	ds_read_b128 v[158:161], v192
	ds_read_b128 v[154:157], v192 offset:1024
	ds_read_b128 v[150:153], v192 offset:2048
	ds_read_b128 v[146:149], v192 offset:3072
	ds_read_b128 v[142:145], v193
	ds_read_b128 v[138:141], v193 offset:1024
	ds_read_b128 v[134:137], v193 offset:2048
	ds_read_b128 v[130:133], v193 offset:3072
	s_add_u32 s26, s24, 0xfffc0080
	s_addc_u32 s27, s25, -1
	s_cmp_eq_u32 s51, 12
	s_cselect_b32 s29, s17, s27
	s_cselect_b32 s28, s47, s26
	s_cselect_b32 s27, s15, s50
	s_cselect_b32 s26, s48, s49
	v_lshl_add_u64 v[222:223], s[24:25], 0, v[170:171]
	s_add_i32 m0, s23, 0xc000
	ds_read_b128 v[182:185], v194
	ds_read_b128 v[186:189], v194 offset:1024
	ds_read_b128 v[198:201], v194 offset:2048
	ds_read_b128 v[202:205], v194 offset:3072
	ds_read_b128 v[206:209], v194 offset:4096
	ds_read_b128 v[210:213], v194 offset:5120
	ds_read_b128 v[214:217], v194 offset:6144
	ds_read_b128 v[218:221], v194 offset:7168
	global_load_lds_dwordx4 v[222:223], off
	v_lshl_add_u64 v[222:223], s[24:25], 0, v[172:173]
	s_add_i32 m0, s23, 0xe000
	s_nop 0
	global_load_lds_dwordx4 v[222:223], off
	s_waitcnt vmcnt(8)
	s_waitcnt lgkmcnt(0)
	s_barrier
	s_setprio 1
	s_waitcnt lgkmcnt(0)
	v_mfma_i32_16x16x64_i8 v[126:129], v[158:161], v[182:185], 0
	s_nop 0
	v_mfma_i32_16x16x64_i8 v[126:129], v[154:157], v[186:189], v[126:129]
	v_mfma_i32_16x16x64_i8 v[122:125], v[150:153], v[182:185], 0
	s_nop 0
	v_mfma_i32_16x16x64_i8 v[122:125], v[146:149], v[186:189], v[122:125]
	v_mfma_i32_16x16x64_i8 v[118:121], v[158:161], v[198:201], 0
	s_nop 0
	v_mfma_i32_16x16x64_i8 v[118:121], v[154:157], v[202:205], v[118:121]
	v_mfma_i32_16x16x64_i8 v[114:117], v[150:153], v[198:201], 0
	s_nop 0
	v_mfma_i32_16x16x64_i8 v[114:117], v[146:149], v[202:205], v[114:117]
	v_mfma_i32_16x16x64_i8 v[98:101], v[158:161], v[206:209], 0
	s_nop 0
	v_mfma_i32_16x16x64_i8 v[98:101], v[154:157], v[210:213], v[98:101]
	v_mfma_i32_16x16x64_i8 v[94:97], v[150:153], v[206:209], 0
	s_nop 0
	v_mfma_i32_16x16x64_i8 v[94:97], v[146:149], v[210:213], v[94:97]
	v_mfma_i32_16x16x64_i8 v[86:89], v[158:161], v[214:217], 0
	s_nop 0
	v_mfma_i32_16x16x64_i8 v[86:89], v[154:157], v[218:221], v[86:89]
	v_mfma_i32_16x16x64_i8 v[78:81], v[150:153], v[214:217], 0
	s_nop 0
	v_mfma_i32_16x16x64_i8 v[78:81], v[146:149], v[218:221], v[78:81]
	s_setprio 0
	s_setprio 1
	v_mfma_i32_16x16x64_i8 v[110:113], v[142:145], v[182:185], 0
	s_nop 0
	v_mfma_i32_16x16x64_i8 v[110:113], v[138:141], v[186:189], v[110:113]
	v_mfma_i32_16x16x64_i8 v[106:109], v[134:137], v[182:185], 0
	s_nop 0
	v_mfma_i32_16x16x64_i8 v[106:109], v[130:133], v[186:189], v[106:109]
	v_mfma_i32_16x16x64_i8 v[102:105], v[142:145], v[198:201], 0
	s_nop 0
	v_mfma_i32_16x16x64_i8 v[102:105], v[138:141], v[202:205], v[102:105]
	v_mfma_i32_16x16x64_i8 v[90:93], v[134:137], v[198:201], 0
	s_nop 0
	v_mfma_i32_16x16x64_i8 v[90:93], v[130:133], v[202:205], v[90:93]
	v_mfma_i32_16x16x64_i8 v[82:85], v[142:145], v[206:209], 0
	s_nop 0
	v_mfma_i32_16x16x64_i8 v[82:85], v[138:141], v[210:213], v[82:85]
	v_mfma_i32_16x16x64_i8 v[74:77], v[134:137], v[206:209], 0
	s_nop 0
	v_mfma_i32_16x16x64_i8 v[74:77], v[130:133], v[210:213], v[74:77]
	v_mfma_i32_16x16x64_i8 v[70:73], v[142:145], v[214:217], 0
	s_nop 0
	v_mfma_i32_16x16x64_i8 v[70:73], v[138:141], v[218:221], v[70:73]
	v_mfma_i32_16x16x64_i8 v[66:69], v[134:137], v[214:217], 0
	s_nop 0
	v_mfma_i32_16x16x64_i8 v[66:69], v[130:133], v[218:221], v[66:69]
	s_setprio 0
	s_barrier
	s_add_i32 s52, s43, s33
	v_lshl_add_u64 v[182:183], s[26:27], 0, v[166:167]
	s_mov_b32 m0, s52
	ds_read_b128 v[198:201], v194 offset:16384
	ds_read_b128 v[202:205], v194 offset:17408
	ds_read_b128 v[206:209], v194 offset:18432
	ds_read_b128 v[210:213], v194 offset:19456
	ds_read_b128 v[214:217], v194 offset:20480
	ds_read_b128 v[218:221], v194 offset:21504
	ds_read_b128 v[222:225], v194 offset:22528
	ds_read_b128 v[226:229], v194 offset:23552
	global_load_lds_dwordx4 v[182:183], off
	s_add_i32 m0, s52, 0x2000
	s_add_u32 s52, s26, 0x40000
	v_lshl_add_u64 v[184:185], s[26:27], 0, v[162:163]
	s_addc_u32 s53, s27, 0
	s_add_i32 s54, s44, s33
	global_load_lds_dwordx4 v[184:185], off
	v_lshl_add_u64 v[186:187], s[52:53], 0, v[166:167]
	s_mov_b32 m0, s54
	v_lshl_add_u64 v[188:189], s[28:29], 0, v[164:165]
	global_load_lds_dwordx4 v[186:187], off
	v_lshl_add_u64 v[186:187], s[52:53], 0, v[162:163]
	s_add_i32 m0, s54, 0x2000
	s_nop 0
	global_load_lds_dwordx4 v[186:187], off
	v_lshl_add_u64 v[186:187], s[28:29], 0, v[168:169]
	s_mov_b32 m0, s23
	s_nop 0
	global_load_lds_dwordx4 v[186:187], off
	s_mov_b32 m0, s36
	s_nop 0
	global_load_lds_dwordx4 v[188:189], off
	s_waitcnt vmcnt(8)
	s_waitcnt lgkmcnt(0)
	s_barrier
	s_setprio 1
	s_waitcnt lgkmcnt(0)
	v_mfma_i32_16x16x64_i8 v[62:65], v[158:161], v[198:201], 0
	s_nop 0
	v_mfma_i32_16x16x64_i8 v[62:65], v[154:157], v[202:205], v[62:65]
	v_mfma_i32_16x16x64_i8 v[58:61], v[150:153], v[198:201], 0
	s_nop 0
	v_mfma_i32_16x16x64_i8 v[58:61], v[146:149], v[202:205], v[58:61]
	v_mfma_i32_16x16x64_i8 v[54:57], v[158:161], v[206:209], 0
	s_nop 0
	v_mfma_i32_16x16x64_i8 v[54:57], v[154:157], v[210:213], v[54:57]
	v_mfma_i32_16x16x64_i8 v[46:49], v[150:153], v[206:209], 0
	s_nop 0
	v_mfma_i32_16x16x64_i8 v[46:49], v[146:149], v[210:213], v[46:49]
	v_mfma_i32_16x16x64_i8 v[38:41], v[158:161], v[214:217], 0
	s_nop 0
	v_mfma_i32_16x16x64_i8 v[38:41], v[154:157], v[218:221], v[38:41]
	v_mfma_i32_16x16x64_i8 v[30:33], v[150:153], v[214:217], 0
	s_nop 0
	v_mfma_i32_16x16x64_i8 v[30:33], v[146:149], v[218:221], v[30:33]
	v_mfma_i32_16x16x64_i8 v[22:25], v[158:161], v[222:225], 0
	s_nop 0
	v_mfma_i32_16x16x64_i8 v[22:25], v[154:157], v[226:229], v[22:25]
	v_mfma_i32_16x16x64_i8 v[14:17], v[150:153], v[222:225], 0
	s_nop 0
	v_mfma_i32_16x16x64_i8 v[14:17], v[146:149], v[226:229], v[14:17]
	s_setprio 0
	s_setprio 1
	v_mfma_i32_16x16x64_i8 v[50:53], v[142:145], v[198:201], 0
	s_nop 0
	v_mfma_i32_16x16x64_i8 v[50:53], v[138:141], v[202:205], v[50:53]
	v_mfma_i32_16x16x64_i8 v[42:45], v[134:137], v[198:201], 0
	s_nop 0
	v_mfma_i32_16x16x64_i8 v[42:45], v[130:133], v[202:205], v[42:45]
	v_mfma_i32_16x16x64_i8 v[34:37], v[142:145], v[206:209], 0
	s_nop 0
	v_mfma_i32_16x16x64_i8 v[34:37], v[138:141], v[210:213], v[34:37]
	v_mfma_i32_16x16x64_i8 v[26:29], v[134:137], v[206:209], 0
	s_nop 0
	v_mfma_i32_16x16x64_i8 v[26:29], v[130:133], v[210:213], v[26:29]
	v_mfma_i32_16x16x64_i8 v[18:21], v[142:145], v[214:217], 0
	s_nop 0
	v_mfma_i32_16x16x64_i8 v[18:21], v[138:141], v[218:221], v[18:21]
	v_mfma_i32_16x16x64_i8 v[10:13], v[134:137], v[214:217], 0
	s_nop 0
	v_mfma_i32_16x16x64_i8 v[10:13], v[130:133], v[218:221], v[10:13]
	v_mfma_i32_16x16x64_i8 v[6:9], v[142:145], v[222:225], 0
	s_nop 0
	v_mfma_i32_16x16x64_i8 v[6:9], v[138:141], v[226:229], v[6:9]
	v_mfma_i32_16x16x64_i8 v[2:5], v[134:137], v[222:225], 0
	s_nop 0
	v_mfma_i32_16x16x64_i8 v[2:5], v[130:133], v[226:229], v[2:5]
	s_setprio 0
	s_barrier
	s_add_i32 s52, 0, 0x18000
	s_add_i32 s53, 0, 0x1c000
	v_add_u32_e32 v142, s52, v190
	v_add_u32_e32 v158, s53, v190
	ds_read_b128 v[130:133], v142
	ds_read_b128 v[134:137], v142 offset:1024
	ds_read_b128 v[138:141], v142 offset:2048
	ds_read_b128 v[142:145], v142 offset:3072
	ds_read_b128 v[146:149], v158
	ds_read_b128 v[150:153], v158 offset:1024
	ds_read_b128 v[154:157], v158 offset:2048
	ds_read_b128 v[158:161], v158 offset:3072
	s_add_u32 s28, s28, 0x40000
	s_addc_u32 s29, s29, 0
	s_mov_b32 m0, s37
	v_lshl_add_u64 v[230:231], s[28:29], 0, v[168:169]
	ds_read_b128 v[198:201], v194 offset:32768
	ds_read_b128 v[202:205], v194 offset:33792
	ds_read_b128 v[206:209], v194 offset:34816
	ds_read_b128 v[210:213], v194 offset:35840
	ds_read_b128 v[214:217], v194 offset:36864
	ds_read_b128 v[218:221], v194 offset:37888
	ds_read_b128 v[222:225], v194 offset:38912
	ds_read_b128 v[226:229], v194 offset:39936
	global_load_lds_dwordx4 v[230:231], off
	v_lshl_add_u64 v[230:231], s[28:29], 0, v[164:165]
	s_mov_b32 m0, s38
	s_nop 0
	global_load_lds_dwordx4 v[230:231], off
	s_waitcnt vmcnt(8)
	s_waitcnt lgkmcnt(0)
	s_barrier
	s_setprio 1
	s_waitcnt lgkmcnt(0)
	v_mfma_i32_16x16x64_i8 v[126:129], v[130:133], v[198:201], v[126:129]
	s_nop 0
	v_mfma_i32_16x16x64_i8 v[126:129], v[134:137], v[202:205], v[126:129]
	v_mfma_i32_16x16x64_i8 v[122:125], v[138:141], v[198:201], v[122:125]
	s_nop 0
	v_mfma_i32_16x16x64_i8 v[122:125], v[142:145], v[202:205], v[122:125]
	v_mfma_i32_16x16x64_i8 v[118:121], v[130:133], v[206:209], v[118:121]
	s_nop 0
	v_mfma_i32_16x16x64_i8 v[118:121], v[134:137], v[210:213], v[118:121]
	v_mfma_i32_16x16x64_i8 v[114:117], v[138:141], v[206:209], v[114:117]
	s_nop 0
	v_mfma_i32_16x16x64_i8 v[114:117], v[142:145], v[210:213], v[114:117]
	v_mfma_i32_16x16x64_i8 v[98:101], v[130:133], v[214:217], v[98:101]
	s_nop 0
	v_mfma_i32_16x16x64_i8 v[98:101], v[134:137], v[218:221], v[98:101]
	v_mfma_i32_16x16x64_i8 v[94:97], v[138:141], v[214:217], v[94:97]
	s_nop 0
	v_mfma_i32_16x16x64_i8 v[94:97], v[142:145], v[218:221], v[94:97]
	v_mfma_i32_16x16x64_i8 v[86:89], v[130:133], v[222:225], v[86:89]
	s_nop 0
	v_mfma_i32_16x16x64_i8 v[86:89], v[134:137], v[226:229], v[86:89]
	v_mfma_i32_16x16x64_i8 v[78:81], v[138:141], v[222:225], v[78:81]
	s_nop 0
	v_mfma_i32_16x16x64_i8 v[78:81], v[142:145], v[226:229], v[78:81]
	s_setprio 0
	s_setprio 1
	v_mfma_i32_16x16x64_i8 v[110:113], v[146:149], v[198:201], v[110:113]
	s_nop 0
	v_mfma_i32_16x16x64_i8 v[110:113], v[150:153], v[202:205], v[110:113]
	v_mfma_i32_16x16x64_i8 v[106:109], v[154:157], v[198:201], v[106:109]
	s_nop 0
	v_mfma_i32_16x16x64_i8 v[106:109], v[158:161], v[202:205], v[106:109]
	v_mfma_i32_16x16x64_i8 v[102:105], v[146:149], v[206:209], v[102:105]
	s_nop 0
	v_mfma_i32_16x16x64_i8 v[102:105], v[150:153], v[210:213], v[102:105]
	v_mfma_i32_16x16x64_i8 v[90:93], v[154:157], v[206:209], v[90:93]
	s_nop 0
	v_mfma_i32_16x16x64_i8 v[90:93], v[158:161], v[210:213], v[90:93]
	v_mfma_i32_16x16x64_i8 v[82:85], v[146:149], v[214:217], v[82:85]
	s_nop 0
	v_mfma_i32_16x16x64_i8 v[82:85], v[150:153], v[218:221], v[82:85]
	v_mfma_i32_16x16x64_i8 v[74:77], v[154:157], v[214:217], v[74:77]
	s_nop 0
	v_mfma_i32_16x16x64_i8 v[74:77], v[158:161], v[218:221], v[74:77]
	v_mfma_i32_16x16x64_i8 v[70:73], v[146:149], v[222:225], v[70:73]
	s_nop 0
	v_mfma_i32_16x16x64_i8 v[70:73], v[150:153], v[226:229], v[70:73]
	v_mfma_i32_16x16x64_i8 v[66:69], v[154:157], v[222:225], v[66:69]
	s_nop 0
	v_mfma_i32_16x16x64_i8 v[66:69], v[158:161], v[226:229], v[66:69]
	s_setprio 0
	s_barrier
	s_add_i32 s28, s52, s33
	v_lshl_add_u64 v[182:183], v[182:183], 0, s[10:11]
	s_mov_b32 m0, s28
	ds_read_b128 v[198:201], v194 offset:49152
	ds_read_b128 v[202:205], v194 offset:50176
	ds_read_b128 v[206:209], v194 offset:51200
	ds_read_b128 v[210:213], v194 offset:52224
	ds_read_b128 v[214:217], v194 offset:53248
	ds_read_b128 v[218:221], v194 offset:54272
	ds_read_b128 v[222:225], v194 offset:55296
	ds_read_b128 v[226:229], v194 offset:56320
	global_load_lds_dwordx4 v[182:183], off
	s_add_i32 m0, s28, 0x2000
	s_add_u32 s26, s26, 0x40080
	v_lshl_add_u64 v[182:183], v[184:185], 0, s[10:11]
	s_addc_u32 s27, s27, 0
	s_add_i32 s28, s53, s33
	global_load_lds_dwordx4 v[182:183], off
	v_lshl_add_u64 v[182:183], s[26:27], 0, v[166:167]
	s_mov_b32 m0, s28
	s_nop 0
	global_load_lds_dwordx4 v[182:183], off
	v_lshl_add_u64 v[182:183], s[26:27], 0, v[162:163]
	s_add_i32 m0, s28, 0x2000
	s_nop 0
	global_load_lds_dwordx4 v[182:183], off
	v_lshl_add_u64 v[182:183], v[186:187], 0, s[10:11]
	s_mov_b32 m0, s40
	s_nop 0
	global_load_lds_dwordx4 v[182:183], off
	v_lshl_add_u64 v[182:183], v[188:189], 0, s[10:11]
	s_mov_b32 m0, s41
	s_nop 0
	global_load_lds_dwordx4 v[182:183], off
	s_waitcnt vmcnt(8)
	s_waitcnt lgkmcnt(0)
	s_barrier
	s_setprio 1
	s_waitcnt lgkmcnt(0)
	v_mfma_i32_16x16x64_i8 v[62:65], v[130:133], v[198:201], v[62:65]
	s_nop 0
	v_mfma_i32_16x16x64_i8 v[62:65], v[134:137], v[202:205], v[62:65]
	v_mfma_i32_16x16x64_i8 v[58:61], v[138:141], v[198:201], v[58:61]
	s_nop 0
	v_mfma_i32_16x16x64_i8 v[58:61], v[142:145], v[202:205], v[58:61]
	v_mfma_i32_16x16x64_i8 v[54:57], v[130:133], v[206:209], v[54:57]
	s_nop 0
	v_mfma_i32_16x16x64_i8 v[54:57], v[134:137], v[210:213], v[54:57]
	v_mfma_i32_16x16x64_i8 v[46:49], v[138:141], v[206:209], v[46:49]
	s_nop 0
	v_mfma_i32_16x16x64_i8 v[46:49], v[142:145], v[210:213], v[46:49]
	v_mfma_i32_16x16x64_i8 v[38:41], v[130:133], v[214:217], v[38:41]
	s_nop 0
	v_mfma_i32_16x16x64_i8 v[38:41], v[134:137], v[218:221], v[38:41]
	v_mfma_i32_16x16x64_i8 v[30:33], v[138:141], v[214:217], v[30:33]
	s_nop 0
	v_mfma_i32_16x16x64_i8 v[30:33], v[142:145], v[218:221], v[30:33]
	v_mfma_i32_16x16x64_i8 v[22:25], v[130:133], v[222:225], v[22:25]
	s_nop 0
	v_mfma_i32_16x16x64_i8 v[22:25], v[134:137], v[226:229], v[22:25]
	v_mfma_i32_16x16x64_i8 v[14:17], v[138:141], v[222:225], v[14:17]
	s_nop 0
	v_mfma_i32_16x16x64_i8 v[14:17], v[142:145], v[226:229], v[14:17]
	s_setprio 0
	s_setprio 1
	v_mfma_i32_16x16x64_i8 v[50:53], v[146:149], v[198:201], v[50:53]
	s_nop 0
	v_mfma_i32_16x16x64_i8 v[50:53], v[150:153], v[202:205], v[50:53]
	v_mfma_i32_16x16x64_i8 v[42:45], v[154:157], v[198:201], v[42:45]
	s_nop 0
	v_mfma_i32_16x16x64_i8 v[42:45], v[158:161], v[202:205], v[42:45]
	v_mfma_i32_16x16x64_i8 v[34:37], v[146:149], v[206:209], v[34:37]
	s_nop 0
	v_mfma_i32_16x16x64_i8 v[34:37], v[150:153], v[210:213], v[34:37]
	v_mfma_i32_16x16x64_i8 v[26:29], v[154:157], v[206:209], v[26:29]
	s_nop 0
	v_mfma_i32_16x16x64_i8 v[26:29], v[158:161], v[210:213], v[26:29]
	v_mfma_i32_16x16x64_i8 v[18:21], v[146:149], v[214:217], v[18:21]
	s_nop 0
	v_mfma_i32_16x16x64_i8 v[18:21], v[150:153], v[218:221], v[18:21]
	v_mfma_i32_16x16x64_i8 v[10:13], v[154:157], v[214:217], v[10:13]
	s_nop 0
	v_mfma_i32_16x16x64_i8 v[10:13], v[158:161], v[218:221], v[10:13]
	v_mfma_i32_16x16x64_i8 v[6:9], v[146:149], v[222:225], v[6:9]
	s_nop 0
	v_mfma_i32_16x16x64_i8 v[6:9], v[150:153], v[226:229], v[6:9]
	v_mfma_i32_16x16x64_i8 v[2:5], v[154:157], v[222:225], v[2:5]
	s_nop 0
	v_mfma_i32_16x16x64_i8 v[2:5], v[158:161], v[226:229], v[2:5]
	s_setprio 0
	s_barrier
	s_add_i32 s51, s51, 2
	s_add_u32 s24, s24, 0x100
	s_addc_u32 s25, s25, 0
	s_add_u32 s49, s49, 0x100
	s_addc_u32 s50, s50, 0
	s_cmp_gt_u32 s51, 13
	s_cbranch_scc1 .Lpeel_exit_244

.Lpeel_exit_244:
	s_and_b64 vcc, exec, s[12:13]
	s_cbranch_vccz .LBB0_247
	s_barrier

.LBB0_625:
	s_ashr_i32 s13, s12, 31
	v_cmp_lt_i64_e32 vcc, s[14:15], v[170:171]
	s_lshl_b64 s[14:15], s[12:13], 19
	s_add_u32 s14, s30, s14
	s_addc_u32 s15, s31, s15
	s_and_b64 s[16:17], vcc, exec
	s_cselect_b32 s13, s15, s21
	s_cselect_b32 s46, s14, s20
	s_ashr_i32 s11, s10, 31
	s_lshl_b64 s[16:17], s[10:11], 19
	s_add_u32 s16, s28, s16
	s_addc_u32 s17, s29, s17
	s_and_b64 s[24:25], vcc, exec
	s_cselect_b32 s11, s17, s23
	s_cselect_b32 s47, s16, s22
	s_add_u32 s20, s20, 0x40080
	s_addc_u32 s21, s21, 0
	s_add_u32 s48, s22, 0x100
	s_waitcnt vmcnt(0)
	v_mov_b32_e32 v34, 0
	s_addc_u32 s49, s23, 0
	s_mov_b32 s50, -2
	ds_read_b128 v[18:21], v188
	ds_read_b128 v[22:25], v188 offset:1024
	ds_read_b128 v[26:29], v188 offset:2048
	ds_read_b128 v[30:33], v188 offset:3072
	ds_read_b128 v[2:5], v189
	ds_read_b128 v[6:9], v189 offset:1024
	ds_read_b128 v[10:13], v189 offset:2048
	ds_read_b128 v[14:17], v189 offset:3072
	s_add_u32 s22, s20, 0xfffc0080
	s_addc_u32 s23, s21, -1
	s_cmp_eq_u32 s50, 12
	s_cselect_b32 s25, s13, s23
	s_cselect_b32 s24, s46, s22
	s_cselect_b32 s23, s11, s49
	s_cselect_b32 s22, s47, s48
	v_lshl_add_u64 v[174:175], s[20:21], 0, v[166:167]
	s_add_i32 m0, s19, 0xc000
	ds_read_b128 v[200:203], v190
	ds_read_b128 v[204:207], v190 offset:1024
	ds_read_b128 v[208:211], v190 offset:2048
	ds_read_b128 v[212:215], v190 offset:3072
	ds_read_b128 v[216:219], v190 offset:4096
	ds_read_b128 v[220:223], v190 offset:5120
	ds_read_b128 v[224:227], v190 offset:6144
	ds_read_b128 v[228:231], v190 offset:7168
	global_load_lds_dwordx4 v[174:175], off
	v_lshl_add_u64 v[174:175], s[20:21], 0, v[168:169]
	s_add_i32 m0, s19, 0xe000
	s_nop 0
	global_load_lds_dwordx4 v[174:175], off
	s_waitcnt vmcnt(8)
	s_waitcnt lgkmcnt(0)
	s_barrier
	s_setprio 1
	s_waitcnt lgkmcnt(0)
	v_mfma_scale_f32_16x16x128_f8f6f4 v[158:161], v[18:25], v[200:207], 0, v191, v192 op_sel_hi:[0,0,0]
	v_mfma_scale_f32_16x16x128_f8f6f4 v[154:157], v[26:33], v[200:207], 0, v191, v192 op_sel_hi:[0,0,0]
	v_mfma_scale_f32_16x16x128_f8f6f4 v[146:149], v[18:25], v[208:215], 0, v191, v192 op_sel_hi:[0,0,0]
	v_mfma_scale_f32_16x16x128_f8f6f4 v[142:145], v[26:33], v[208:215], 0, v191, v192 op_sel_hi:[0,0,0]
	v_mfma_scale_f32_16x16x128_f8f6f4 v[130:133], v[18:25], v[216:223], 0, v191, v192 op_sel_hi:[0,0,0]
	v_mfma_scale_f32_16x16x128_f8f6f4 v[126:129], v[26:33], v[216:223], 0, v191, v192 op_sel_hi:[0,0,0]
	v_mfma_scale_f32_16x16x128_f8f6f4 v[114:117], v[18:25], v[224:231], 0, v191, v192 op_sel_hi:[0,0,0]
	v_mfma_scale_f32_16x16x128_f8f6f4 v[110:113], v[26:33], v[224:231], 0, v191, v192 op_sel_hi:[0,0,0]
	s_setprio 0
	s_setprio 1
	v_mfma_scale_f32_16x16x128_f8f6f4 v[150:153], v[2:9], v[200:207], 0, v191, v192 op_sel_hi:[0,0,0]
	v_mfma_scale_f32_16x16x128_f8f6f4 v[138:141], v[10:17], v[200:207], 0, v191, v192 op_sel_hi:[0,0,0]
	v_mfma_scale_f32_16x16x128_f8f6f4 v[134:137], v[2:9], v[208:215], 0, v191, v192 op_sel_hi:[0,0,0]
	v_mfma_scale_f32_16x16x128_f8f6f4 v[122:125], v[10:17], v[208:215], 0, v191, v192 op_sel_hi:[0,0,0]
	v_mfma_scale_f32_16x16x128_f8f6f4 v[118:121], v[2:9], v[216:223], 0, v191, v192 op_sel_hi:[0,0,0]
	v_mfma_scale_f32_16x16x128_f8f6f4 v[106:109], v[10:17], v[216:223], 0, v191, v192 op_sel_hi:[0,0,0]
	v_mfma_scale_f32_16x16x128_f8f6f4 v[102:105], v[2:9], v[224:231], 0, v191, v192 op_sel_hi:[0,0,0]
	v_mfma_scale_f32_16x16x128_f8f6f4 v[98:101], v[10:17], v[224:231], 0, v191, v192 op_sel_hi:[0,0,0]
	s_setprio 0
	s_barrier
	s_add_i32 s51, s43, s33
	v_lshl_add_u64 v[174:175], s[22:23], 0, v[162:163]
	s_mov_b32 m0, s51
	ds_read_b128 v[200:203], v190 offset:16384
	ds_read_b128 v[204:207], v190 offset:17408
	ds_read_b128 v[208:211], v190 offset:18432
	ds_read_b128 v[212:215], v190 offset:19456
	ds_read_b128 v[216:219], v190 offset:20480
	ds_read_b128 v[220:223], v190 offset:21504
	ds_read_b128 v[224:227], v190 offset:22528
	ds_read_b128 v[228:231], v190 offset:23552
	global_load_lds_dwordx4 v[174:175], off
	s_add_i32 m0, s51, 0x2000
	s_add_u32 s52, s22, 0x40000
	v_lshl_add_u64 v[176:177], s[22:23], 0, v[164:165]
	s_addc_u32 s53, s23, 0
	s_add_i32 s51, s44, s33
	global_load_lds_dwordx4 v[176:177], off
	v_lshl_add_u64 v[184:185], s[52:53], 0, v[162:163]
	s_mov_b32 m0, s51
	v_lshl_add_u64 v[186:187], s[24:25], 0, v[164:165]
	global_load_lds_dwordx4 v[184:185], off
	v_lshl_add_u64 v[184:185], s[52:53], 0, v[164:165]
	s_add_i32 m0, s51, 0x2000
	s_nop 0
	global_load_lds_dwordx4 v[184:185], off
	v_lshl_add_u64 v[184:185], s[24:25], 0, v[162:163]
	s_mov_b32 m0, s19
	s_nop 0
	global_load_lds_dwordx4 v[184:185], off
	s_mov_b32 m0, s34
	s_nop 0
	global_load_lds_dwordx4 v[186:187], off
	s_waitcnt vmcnt(8)
	s_waitcnt lgkmcnt(0)
	s_barrier
	s_setprio 1
	s_waitcnt lgkmcnt(0)
	v_mfma_scale_f32_16x16x128_f8f6f4 v[94:97], v[18:25], v[200:207], 0, v191, v192 op_sel_hi:[0,0,0]
	v_mfma_scale_f32_16x16x128_f8f6f4 v[90:93], v[26:33], v[200:207], 0, v191, v192 op_sel_hi:[0,0,0]
	v_mfma_scale_f32_16x16x128_f8f6f4 v[82:85], v[18:25], v[208:215], 0, v191, v192 op_sel_hi:[0,0,0]
	v_mfma_scale_f32_16x16x128_f8f6f4 v[78:81], v[26:33], v[208:215], 0, v191, v192 op_sel_hi:[0,0,0]
	v_mfma_scale_f32_16x16x128_f8f6f4 v[66:69], v[18:25], v[216:223], 0, v191, v192 op_sel_hi:[0,0,0]
	v_mfma_scale_f32_16x16x128_f8f6f4 v[62:65], v[26:33], v[216:223], 0, v191, v192 op_sel_hi:[0,0,0]
	v_mfma_scale_f32_16x16x128_f8f6f4 v[50:53], v[18:25], v[224:231], 0, v191, v192 op_sel_hi:[0,0,0]
	v_mfma_scale_f32_16x16x128_f8f6f4 v[46:49], v[26:33], v[224:231], 0, v191, v192 op_sel_hi:[0,0,0]
	s_setprio 0
	s_setprio 1
	v_mfma_scale_f32_16x16x128_f8f6f4 v[86:89], v[2:9], v[200:207], 0, v191, v192 op_sel_hi:[0,0,0]
	v_mfma_scale_f32_16x16x128_f8f6f4 v[74:77], v[10:17], v[200:207], 0, v191, v192 op_sel_hi:[0,0,0]
	v_mfma_scale_f32_16x16x128_f8f6f4 v[70:73], v[2:9], v[208:215], 0, v191, v192 op_sel_hi:[0,0,0]
	v_mfma_scale_f32_16x16x128_f8f6f4 v[58:61], v[10:17], v[208:215], 0, v191, v192 op_sel_hi:[0,0,0]
	v_mfma_scale_f32_16x16x128_f8f6f4 v[54:57], v[2:9], v[216:223], 0, v191, v192 op_sel_hi:[0,0,0]
	v_mfma_scale_f32_16x16x128_f8f6f4 v[42:45], v[10:17], v[216:223], 0, v191, v192 op_sel_hi:[0,0,0]
	v_mfma_scale_f32_16x16x128_f8f6f4 v[38:41], v[2:9], v[224:231], 0, v191, v192 op_sel_hi:[0,0,0]
	v_mfma_scale_f32_16x16x128_f8f6f4 v[34:37], v[10:17], v[224:231], 0, v191, v192 op_sel_hi:[0,0,0]
	s_setprio 0
	s_barrier
	s_add_i32 s51, 0, 0x18000
	s_add_i32 s52, 0, 0x1c000
	v_add_u32_e32 v14, s51, v181
	v_add_u32_e32 v30, s52, v181
	ds_read_b128 v[2:5], v14
	ds_read_b128 v[6:9], v14 offset:1024
	ds_read_b128 v[10:13], v14 offset:2048
	ds_read_b128 v[14:17], v14 offset:3072
	ds_read_b128 v[18:21], v30
	ds_read_b128 v[22:25], v30 offset:1024
	ds_read_b128 v[26:29], v30 offset:2048
	ds_read_b128 v[30:33], v30 offset:3072
	s_add_u32 s24, s24, 0x40000
	s_addc_u32 s25, s25, 0
	s_mov_b32 m0, s35
	v_lshl_add_u64 v[232:233], s[24:25], 0, v[162:163]
	ds_read_b128 v[200:203], v190 offset:32768
	ds_read_b128 v[204:207], v190 offset:33792
	ds_read_b128 v[208:211], v190 offset:34816
	ds_read_b128 v[212:215], v190 offset:35840
	ds_read_b128 v[216:219], v190 offset:36864
	ds_read_b128 v[220:223], v190 offset:37888
	ds_read_b128 v[224:227], v190 offset:38912
	ds_read_b128 v[228:231], v190 offset:39936
	global_load_lds_dwordx4 v[232:233], off
	v_lshl_add_u64 v[232:233], s[24:25], 0, v[164:165]
	s_mov_b32 m0, s36
	s_nop 0
	global_load_lds_dwordx4 v[232:233], off
	s_waitcnt vmcnt(8)
	s_waitcnt lgkmcnt(0)
	s_barrier
	s_setprio 1
	s_waitcnt lgkmcnt(0)
	v_mfma_scale_f32_16x16x128_f8f6f4 v[158:161], v[2:9], v[200:207], v[158:161], v191, v192 op_sel_hi:[0,0,0]
	v_mfma_scale_f32_16x16x128_f8f6f4 v[154:157], v[10:17], v[200:207], v[154:157], v191, v192 op_sel_hi:[0,0,0]
	v_mfma_scale_f32_16x16x128_f8f6f4 v[146:149], v[2:9], v[208:215], v[146:149], v191, v192 op_sel_hi:[0,0,0]
	v_mfma_scale_f32_16x16x128_f8f6f4 v[142:145], v[10:17], v[208:215], v[142:145], v191, v192 op_sel_hi:[0,0,0]
	v_mfma_scale_f32_16x16x128_f8f6f4 v[130:133], v[2:9], v[216:223], v[130:133], v191, v192 op_sel_hi:[0,0,0]
	v_mfma_scale_f32_16x16x128_f8f6f4 v[126:129], v[10:17], v[216:223], v[126:129], v191, v192 op_sel_hi:[0,0,0]
	v_mfma_scale_f32_16x16x128_f8f6f4 v[114:117], v[2:9], v[224:231], v[114:117], v191, v192 op_sel_hi:[0,0,0]
	v_mfma_scale_f32_16x16x128_f8f6f4 v[110:113], v[10:17], v[224:231], v[110:113], v191, v192 op_sel_hi:[0,0,0]
	s_setprio 0
	s_setprio 1
	v_mfma_scale_f32_16x16x128_f8f6f4 v[150:153], v[18:25], v[200:207], v[150:153], v191, v192 op_sel_hi:[0,0,0]
	v_mfma_scale_f32_16x16x128_f8f6f4 v[138:141], v[26:33], v[200:207], v[138:141], v191, v192 op_sel_hi:[0,0,0]
	v_mfma_scale_f32_16x16x128_f8f6f4 v[134:137], v[18:25], v[208:215], v[134:137], v191, v192 op_sel_hi:[0,0,0]
	v_mfma_scale_f32_16x16x128_f8f6f4 v[122:125], v[26:33], v[208:215], v[122:125], v191, v192 op_sel_hi:[0,0,0]
	v_mfma_scale_f32_16x16x128_f8f6f4 v[118:121], v[18:25], v[216:223], v[118:121], v191, v192 op_sel_hi:[0,0,0]
	v_mfma_scale_f32_16x16x128_f8f6f4 v[106:109], v[26:33], v[216:223], v[106:109], v191, v192 op_sel_hi:[0,0,0]
	v_mfma_scale_f32_16x16x128_f8f6f4 v[102:105], v[18:25], v[224:231], v[102:105], v191, v192 op_sel_hi:[0,0,0]
	v_mfma_scale_f32_16x16x128_f8f6f4 v[98:101], v[26:33], v[224:231], v[98:101], v191, v192 op_sel_hi:[0,0,0]
	s_setprio 0
	s_barrier
	s_add_i32 s24, s51, s33
	v_lshl_add_u64 v[174:175], v[174:175], 0, s[4:5]
	s_mov_b32 m0, s24
	ds_read_b128 v[200:203], v190 offset:49152
	ds_read_b128 v[204:207], v190 offset:50176
	ds_read_b128 v[208:211], v190 offset:51200
	ds_read_b128 v[212:215], v190 offset:52224
	ds_read_b128 v[216:219], v190 offset:53248
	ds_read_b128 v[220:223], v190 offset:54272
	ds_read_b128 v[224:227], v190 offset:55296
	ds_read_b128 v[228:231], v190 offset:56320
	global_load_lds_dwordx4 v[174:175], off
	s_add_i32 m0, s24, 0x2000
	s_add_u32 s22, s22, 0x40080
	v_lshl_add_u64 v[174:175], v[176:177], 0, s[4:5]
	s_addc_u32 s23, s23, 0
	s_add_i32 s24, s52, s33
	global_load_lds_dwordx4 v[174:175], off
	v_lshl_add_u64 v[174:175], s[22:23], 0, v[162:163]
	s_mov_b32 m0, s24
	s_nop 0
	global_load_lds_dwordx4 v[174:175], off
	v_lshl_add_u64 v[174:175], s[22:23], 0, v[164:165]
	s_add_i32 m0, s24, 0x2000
	s_nop 0
	global_load_lds_dwordx4 v[174:175], off
	v_lshl_add_u64 v[174:175], v[184:185], 0, s[4:5]
	s_mov_b32 m0, s40
	s_nop 0
	global_load_lds_dwordx4 v[174:175], off
	v_lshl_add_u64 v[174:175], v[186:187], 0, s[4:5]
	s_mov_b32 m0, s41
	s_nop 0
	global_load_lds_dwordx4 v[174:175], off
	s_waitcnt vmcnt(8)
	s_waitcnt lgkmcnt(0)
	s_barrier
	s_setprio 1
	s_waitcnt lgkmcnt(0)
	v_mfma_scale_f32_16x16x128_f8f6f4 v[94:97], v[2:9], v[200:207], v[94:97], v191, v192 op_sel_hi:[0,0,0]
	v_mfma_scale_f32_16x16x128_f8f6f4 v[90:93], v[10:17], v[200:207], v[90:93], v191, v192 op_sel_hi:[0,0,0]
	v_mfma_scale_f32_16x16x128_f8f6f4 v[82:85], v[2:9], v[208:215], v[82:85], v191, v192 op_sel_hi:[0,0,0]
	v_mfma_scale_f32_16x16x128_f8f6f4 v[78:81], v[10:17], v[208:215], v[78:81], v191, v192 op_sel_hi:[0,0,0]
	v_mfma_scale_f32_16x16x128_f8f6f4 v[66:69], v[2:9], v[216:223], v[66:69], v191, v192 op_sel_hi:[0,0,0]
	v_mfma_scale_f32_16x16x128_f8f6f4 v[62:65], v[10:17], v[216:223], v[62:65], v191, v192 op_sel_hi:[0,0,0]
	v_mfma_scale_f32_16x16x128_f8f6f4 v[50:53], v[2:9], v[224:231], v[50:53], v191, v192 op_sel_hi:[0,0,0]
	v_mfma_scale_f32_16x16x128_f8f6f4 v[46:49], v[10:17], v[224:231], v[46:49], v191, v192 op_sel_hi:[0,0,0]
	s_setprio 0
	s_setprio 1
	v_mfma_scale_f32_16x16x128_f8f6f4 v[86:89], v[18:25], v[200:207], v[86:89], v191, v192 op_sel_hi:[0,0,0]
	v_mfma_scale_f32_16x16x128_f8f6f4 v[74:77], v[26:33], v[200:207], v[74:77], v191, v192 op_sel_hi:[0,0,0]
	v_mfma_scale_f32_16x16x128_f8f6f4 v[70:73], v[18:25], v[208:215], v[70:73], v191, v192 op_sel_hi:[0,0,0]
	v_mfma_scale_f32_16x16x128_f8f6f4 v[58:61], v[26:33], v[208:215], v[58:61], v191, v192 op_sel_hi:[0,0,0]
	v_mfma_scale_f32_16x16x128_f8f6f4 v[54:57], v[18:25], v[216:223], v[54:57], v191, v192 op_sel_hi:[0,0,0]
	v_mfma_scale_f32_16x16x128_f8f6f4 v[42:45], v[26:33], v[216:223], v[42:45], v191, v192 op_sel_hi:[0,0,0]
	v_mfma_scale_f32_16x16x128_f8f6f4 v[38:41], v[18:25], v[224:231], v[38:41], v191, v192 op_sel_hi:[0,0,0]
	v_mfma_scale_f32_16x16x128_f8f6f4 v[34:37], v[26:33], v[224:231], v[34:37], v191, v192 op_sel_hi:[0,0,0]
	s_setprio 0
	s_barrier
	s_add_i32 s50, s50, 2
	s_add_u32 s20, s20, 0x100
	s_addc_u32 s21, s21, 0
	s_add_u32 s48, s48, 0x100
	s_addc_u32 s49, s49, 0
	s_cmp_gt_u32 s50, 13
	s_cbranch_scc1 .Lpeel_exit_626

.Lpeel_exit_626:
	v_lshl_add_u32 v26, s18, 8, v1
	v_lshl_or_b32 v24, s45, 8, v183
	s_ashr_i32 s11, s18, 3
	v_ashrrev_i32_e32 v27, 31, v26
	s_mul_hi_i32 s13, s11, 0x1c000
	s_mul_i32 s11, s11, 0x1c000
	v_ashrrev_i32_e32 v25, 31, v24
	v_lshlrev_b64 v[4:5], 11, v[26:27]
	s_add_u32 s20, s38, s11
	v_lshl_add_u64 v[4:5], v[4:5], 0, v[24:25]
	v_readlane_b32 s48, v250, 56
	s_addc_u32 s21, s39, s13
	v_lshlrev_b64 v[18:19], 2, v[4:5]
	v_readlane_b32 s49, v250, 57
	s_nop 15
	s_nop 15
	v_lshl_add_u64 v[2:3], v[24:25], 2, s[20:21]
	v_lshl_add_u64 v[30:31], s[76:77], 0, v[18:19]
	v_lshl_add_u64 v[28:29], s[48:49], 0, v[18:19]
	global_load_dwordx4 v[20:23], v[28:29], off
	global_load_dwordx4 v[14:17], v[2:3], off
	global_load_dwordx4 v[10:13], v[2:3], off offset:64
	global_load_dwordx4 v[6:9], v[2:3], off offset:512
	s_nop 0
	global_load_dwordx4 v[2:5], v[2:3], off offset:576
	s_mov_b64 s[20:21], 0x100000
	v_readlane_b32 s60, v251, 4
	v_readlane_b32 s61, v251, 5
	v_readlane_b32 s62, v251, 6
	v_readlane_b32 s63, v251, 7
	s_mov_b32 s45, s10
	s_mov_b32 s18, s12
	s_and_b64 vcc, exec, s[0:1]
	s_mov_b64 s[22:23], s[16:17]
	v_readlane_b32 s50, v250, 58
	v_readlane_b32 s51, v250, 59
	v_readlane_b32 s52, v250, 60
	v_readlane_b32 s53, v250, 61
	v_readlane_b32 s54, v250, 62
	v_readlane_b32 s55, v250, 63
	v_readlane_b32 s56, v251, 0
	v_readlane_b32 s57, v251, 1
	v_readlane_b32 s58, v251, 2
	v_readlane_b32 s59, v251, 3
	s_waitcnt vmcnt(0)
	v_pk_fma_f32 v[22:23], v[160:161], v[16:17], v[22:23]
	v_pk_fma_f32 v[20:21], v[158:159], v[14:15], v[20:21]
	global_store_dwordx4 v[30:31], v[20:23], off
	global_load_dwordx4 v[20:23], v[28:29], off offset:64
	s_waitcnt vmcnt(0)
	v_pk_fma_f32 v[22:23], v[156:157], v[12:13], v[22:23]
	v_pk_fma_f32 v[20:21], v[154:155], v[10:11], v[20:21]
	global_store_dwordx4 v[30:31], v[20:23], off offset:64
	global_load_dwordx4 v[20:23], v[28:29], off offset:512
	s_waitcnt vmcnt(0)
	v_pk_fma_f32 v[22:23], v[152:153], v[8:9], v[22:23]
	v_pk_fma_f32 v[20:21], v[150:151], v[6:7], v[20:21]
	global_store_dwordx4 v[30:31], v[20:23], off offset:512
	global_load_dwordx4 v[20:23], v[28:29], off offset:576
	v_or_b32_e32 v28, 16, v26
	v_ashrrev_i32_e32 v29, 31, v28
	v_lshlrev_b64 v[28:29], 11, v[28:29]
	v_lshl_add_u64 v[28:29], v[28:29], 0, v[24:25]
	v_lshlrev_b64 v[28:29], 2, v[28:29]
	v_lshl_add_u64 v[32:33], s[48:49], 0, v[28:29]
	v_lshl_add_u64 v[28:29], s[76:77], 0, v[28:29]
	s_waitcnt vmcnt(0)
	v_pk_fma_f32 v[22:23], v[140:141], v[4:5], v[22:23]
	v_pk_fma_f32 v[20:21], v[138:139], v[2:3], v[20:21]
	global_store_dwordx4 v[30:31], v[20:23], off offset:576
	global_load_dwordx4 v[20:23], v[32:33], off
	v_or_b32_e32 v30, 32, v26
	v_ashrrev_i32_e32 v31, 31, v30
	v_lshlrev_b64 v[30:31], 11, v[30:31]
	v_lshl_add_u64 v[30:31], v[30:31], 0, v[24:25]
	v_lshlrev_b64 v[30:31], 2, v[30:31]
	v_or_b32_e32 v26, 48, v26
	v_ashrrev_i32_e32 v27, 31, v26
	v_lshlrev_b64 v[26:27], 11, v[26:27]
	v_lshl_add_u64 v[24:25], v[26:27], 0, v[24:25]
	v_lshlrev_b64 v[24:25], 2, v[24:25]
	v_lshl_add_u64 v[26:27], s[48:49], 0, v[24:25]
	v_lshl_add_u64 v[24:25], s[76:77], 0, v[24:25]
	s_waitcnt vmcnt(0)
	v_pk_fma_f32 v[22:23], v[148:149], v[16:17], v[22:23]
	v_pk_fma_f32 v[20:21], v[146:147], v[14:15], v[20:21]
	global_store_dwordx4 v[28:29], v[20:23], off
	global_load_dwordx4 v[20:23], v[32:33], off offset:64
	s_waitcnt vmcnt(0)
	v_pk_fma_f32 v[22:23], v[144:145], v[12:13], v[22:23]
	v_pk_fma_f32 v[20:21], v[142:143], v[10:11], v[20:21]
	global_store_dwordx4 v[28:29], v[20:23], off offset:64
	global_load_dwordx4 v[20:23], v[32:33], off offset:512
	s_waitcnt vmcnt(0)
	v_pk_fma_f32 v[22:23], v[136:137], v[8:9], v[22:23]
	v_pk_fma_f32 v[20:21], v[134:135], v[6:7], v[20:21]
	global_store_dwordx4 v[28:29], v[20:23], off offset:512
	global_load_dwordx4 v[20:23], v[32:33], off offset:576
	v_lshl_add_u64 v[32:33], s[48:49], 0, v[30:31]
	s_waitcnt vmcnt(0)
	v_pk_fma_f32 v[22:23], v[124:125], v[4:5], v[22:23]
	v_pk_fma_f32 v[20:21], v[122:123], v[2:3], v[20:21]
	global_store_dwordx4 v[28:29], v[20:23], off offset:576
	global_load_dwordx4 v[20:23], v[32:33], off
	v_lshl_add_u64 v[28:29], s[76:77], 0, v[30:31]
	s_waitcnt vmcnt(0)
	v_pk_fma_f32 v[22:23], v[132:133], v[16:17], v[22:23]
	v_pk_fma_f32 v[20:21], v[130:131], v[14:15], v[20:21]
	global_store_dwordx4 v[28:29], v[20:23], off
	global_load_dwordx4 v[20:23], v[32:33], off offset:64
	s_waitcnt vmcnt(0)
	v_pk_fma_f32 v[22:23], v[128:129], v[12:13], v[22:23]
	v_pk_fma_f32 v[20:21], v[126:127], v[10:11], v[20:21]
	global_store_dwordx4 v[28:29], v[20:23], off offset:64
	global_load_dwordx4 v[20:23], v[32:33], off offset:512
	s_waitcnt vmcnt(0)
	v_pk_fma_f32 v[22:23], v[120:121], v[8:9], v[22:23]
	v_pk_fma_f32 v[20:21], v[118:119], v[6:7], v[20:21]
	global_store_dwordx4 v[28:29], v[20:23], off offset:512
	global_load_dwordx4 v[20:23], v[32:33], off offset:576
	s_waitcnt vmcnt(0)
	v_pk_fma_f32 v[22:23], v[108:109], v[4:5], v[22:23]
	v_pk_fma_f32 v[20:21], v[106:107], v[2:3], v[20:21]
	global_store_dwordx4 v[28:29], v[20:23], off offset:576
	global_load_dwordx4 v[20:23], v[26:27], off
	s_waitcnt vmcnt(0)
	v_pk_fma_f32 v[22:23], v[116:117], v[16:17], v[22:23]
	v_pk_fma_f32 v[20:21], v[114:115], v[14:15], v[20:21]
	global_store_dwordx4 v[24:25], v[20:23], off
	global_load_dwordx4 v[20:23], v[26:27], off offset:64
	s_waitcnt vmcnt(0)
	v_pk_fma_f32 v[22:23], v[112:113], v[12:13], v[22:23]
	v_pk_fma_f32 v[20:21], v[110:111], v[10:11], v[20:21]
	global_store_dwordx4 v[24:25], v[20:23], off offset:64
	global_load_dwordx4 v[20:23], v[26:27], off offset:512
	s_waitcnt vmcnt(0)
	v_pk_fma_f32 v[22:23], v[104:105], v[8:9], v[22:23]
	v_pk_fma_f32 v[20:21], v[102:103], v[6:7], v[20:21]
	global_store_dwordx4 v[24:25], v[20:23], off offset:512
	global_load_dwordx4 v[20:23], v[26:27], off offset:576
	v_lshl_add_u64 v[26:27], v[18:19], 0, s[20:21]
	v_lshl_add_u64 v[28:29], s[48:49], 0, v[26:27]
	s_mov_b64 s[20:21], 0x120000
	s_waitcnt vmcnt(0)
	v_pk_fma_f32 v[22:23], v[100:101], v[4:5], v[22:23]
	v_pk_fma_f32 v[20:21], v[98:99], v[2:3], v[20:21]
	global_store_dwordx4 v[24:25], v[20:23], off offset:576
	global_load_dwordx4 v[20:23], v[28:29], off
	v_lshl_add_u64 v[24:25], s[76:77], 0, v[26:27]
	v_lshl_add_u64 v[26:27], v[18:19], 0, s[20:21]
	s_mov_b64 s[20:21], s[14:15]
	s_waitcnt vmcnt(0)
	v_pk_fma_f32 v[22:23], v[96:97], v[16:17], v[22:23]
	v_pk_fma_f32 v[20:21], v[94:95], v[14:15], v[20:21]
	global_store_dwordx4 v[24:25], v[20:23], off
	global_load_dwordx4 v[20:23], v[28:29], off offset:64
	s_waitcnt vmcnt(0)
	v_pk_fma_f32 v[22:23], v[92:93], v[12:13], v[22:23]
	v_pk_fma_f32 v[20:21], v[90:91], v[10:11], v[20:21]
	global_store_dwordx4 v[24:25], v[20:23], off offset:64
	global_load_dwordx4 v[20:23], v[28:29], off offset:512
	s_waitcnt vmcnt(0)
	v_pk_fma_f32 v[22:23], v[88:89], v[8:9], v[22:23]
	v_pk_fma_f32 v[20:21], v[86:87], v[6:7], v[20:21]
	global_store_dwordx4 v[24:25], v[20:23], off offset:512
	global_load_dwordx4 v[20:23], v[28:29], off offset:576
	v_lshl_add_u64 v[28:29], s[48:49], 0, v[26:27]
	s_waitcnt vmcnt(0)
	v_pk_fma_f32 v[22:23], v[76:77], v[4:5], v[22:23]
	v_pk_fma_f32 v[20:21], v[74:75], v[2:3], v[20:21]
	global_store_dwordx4 v[24:25], v[20:23], off offset:576
	global_load_dwordx4 v[20:23], v[28:29], off
	v_lshl_add_u64 v[24:25], s[76:77], 0, v[26:27]
	v_lshl_add_u64 v[26:27], v[18:19], 0, s[6:7]
	s_waitcnt vmcnt(0)
	v_pk_fma_f32 v[22:23], v[84:85], v[16:17], v[22:23]
	v_pk_fma_f32 v[20:21], v[82:83], v[14:15], v[20:21]
	global_store_dwordx4 v[24:25], v[20:23], off
	global_load_dwordx4 v[20:23], v[28:29], off offset:64
	s_waitcnt vmcnt(0)
	v_pk_fma_f32 v[22:23], v[80:81], v[12:13], v[22:23]
	v_pk_fma_f32 v[20:21], v[78:79], v[10:11], v[20:21]
	global_store_dwordx4 v[24:25], v[20:23], off offset:64
	global_load_dwordx4 v[20:23], v[28:29], off offset:512
	s_waitcnt vmcnt(0)
	v_pk_fma_f32 v[22:23], v[72:73], v[8:9], v[22:23]
	v_pk_fma_f32 v[20:21], v[70:71], v[6:7], v[20:21]
	global_store_dwordx4 v[24:25], v[20:23], off offset:512
	global_load_dwordx4 v[20:23], v[28:29], off offset:576
	v_lshl_add_u64 v[28:29], s[48:49], 0, v[26:27]
	s_waitcnt vmcnt(0)
	v_pk_fma_f32 v[22:23], v[60:61], v[4:5], v[22:23]
	v_pk_fma_f32 v[20:21], v[58:59], v[2:3], v[20:21]
	global_store_dwordx4 v[24:25], v[20:23], off offset:576
	global_load_dwordx4 v[20:23], v[28:29], off
	v_lshl_add_u64 v[24:25], s[76:77], 0, v[26:27]
	v_lshl_add_u64 v[26:27], v[18:19], 0, s[8:9]
	s_waitcnt vmcnt(0)
	v_pk_fma_f32 v[22:23], v[68:69], v[16:17], v[22:23]
	v_pk_fma_f32 v[20:21], v[66:67], v[14:15], v[20:21]
	global_store_dwordx4 v[24:25], v[20:23], off
	global_load_dwordx4 v[20:23], v[28:29], off offset:64
	s_waitcnt vmcnt(0)
	v_pk_fma_f32 v[22:23], v[64:65], v[12:13], v[22:23]
	v_pk_fma_f32 v[20:21], v[62:63], v[10:11], v[20:21]
	global_store_dwordx4 v[24:25], v[20:23], off offset:64
	global_load_dwordx4 v[20:23], v[28:29], off offset:512
	s_waitcnt vmcnt(0)
	v_pk_fma_f32 v[22:23], v[56:57], v[8:9], v[22:23]
	v_pk_fma_f32 v[20:21], v[54:55], v[6:7], v[20:21]
	global_store_dwordx4 v[24:25], v[20:23], off offset:512
	global_load_dwordx4 v[20:23], v[28:29], off offset:576
	v_lshl_add_u64 v[28:29], s[48:49], 0, v[26:27]
	s_waitcnt vmcnt(0)
	v_pk_fma_f32 v[22:23], v[44:45], v[4:5], v[22:23]
	v_pk_fma_f32 v[20:21], v[42:43], v[2:3], v[20:21]
	global_store_dwordx4 v[24:25], v[20:23], off offset:576
	global_load_dwordx4 v[18:21], v[28:29], off
	s_waitcnt vmcnt(0)
	v_pk_fma_f32 v[16:17], v[52:53], v[16:17], v[20:21]
	v_lshl_add_u64 v[22:23], s[76:77], 0, v[26:27]
	v_pk_fma_f32 v[14:15], v[50:51], v[14:15], v[18:19]
	global_store_dwordx4 v[22:23], v[14:17], off
	global_load_dwordx4 v[14:17], v[28:29], off offset:64
	s_waitcnt vmcnt(0)
	v_pk_fma_f32 v[12:13], v[48:49], v[12:13], v[16:17]
	v_pk_fma_f32 v[10:11], v[46:47], v[10:11], v[14:15]
	global_store_dwordx4 v[22:23], v[10:13], off offset:64
	global_load_dwordx4 v[10:13], v[28:29], off offset:512
	s_waitcnt vmcnt(0)
	v_pk_fma_f32 v[8:9], v[40:41], v[8:9], v[12:13]
	v_pk_fma_f32 v[6:7], v[38:39], v[6:7], v[10:11]
	global_store_dwordx4 v[22:23], v[6:9], off offset:512
	global_load_dwordx4 v[6:9], v[28:29], off offset:576
	s_waitcnt vmcnt(0)
	v_pk_fma_f32 v[4:5], v[36:37], v[4:5], v[8:9]
	v_pk_fma_f32 v[2:3], v[34:35], v[2:3], v[6:7]
	global_store_dwordx4 v[22:23], v[2:5], off offset:576
	s_cbranch_vccz .LBB0_619
	s_waitcnt vmcnt(0)
	s_cmpk_gt_u32 s26, 0xff
	s_cbranch_scc1 .LBB0_630
	s_barrier

.LBB0_763:
	s_ashr_i32 s17, s16, 31
	s_lshl_b64 s[18:19], s[16:17], 19
	s_add_u32 s18, s72, s18
	s_addc_u32 s19, s73, s19
	s_and_b64 s[20:21], s[0:1], exec
	s_cselect_b32 s17, s19, s25
	s_cselect_b32 s47, s18, s24
	s_ashr_i32 s15, s14, 31
	s_lshl_b64 s[20:21], s[14:15], 19
	s_add_u32 s20, s30, s20
	s_addc_u32 s21, s31, s21
	s_and_b64 s[28:29], s[0:1], exec
	s_cselect_b32 s15, s21, s27
	s_cselect_b32 s48, s20, s26
	s_add_u32 s24, s24, 0x40080
	s_addc_u32 s25, s25, 0
	s_add_u32 s49, s26, 0x100
	v_mov_b32_e32 v2, 0
	s_addc_u32 s50, s27, 0
	s_mov_b32 s51, -2
	v_mov_b32_e32 v3, v2
	v_mov_b32_e32 v4, v2
	v_mov_b32_e32 v5, v2
	v_mov_b32_e32 v6, v2
	v_mov_b32_e32 v7, v2
	v_mov_b32_e32 v8, v2
	v_mov_b32_e32 v9, v2
	v_mov_b32_e32 v14, v2
	v_mov_b32_e32 v15, v2
	v_mov_b32_e32 v16, v2
	v_mov_b32_e32 v17, v2
	s_waitcnt vmcnt(0)
	ds_read_b128 v[158:161], v193
	ds_read_b128 v[154:157], v193 offset:1024
	ds_read_b128 v[150:153], v193 offset:2048
	ds_read_b128 v[146:149], v193 offset:3072
	ds_read_b128 v[142:145], v194
	ds_read_b128 v[138:141], v194 offset:1024
	ds_read_b128 v[134:137], v194 offset:2048
	ds_read_b128 v[130:133], v194 offset:3072
	s_add_u32 s26, s24, 0xfffc0080
	s_addc_u32 s27, s25, -1
	s_cmp_eq_u32 s51, 12
	s_cselect_b32 s29, s17, s27
	s_cselect_b32 s28, s47, s26
	s_cselect_b32 s27, s15, s50
	s_cselect_b32 s26, s48, s49
	v_lshl_add_u64 v[224:225], s[24:25], 0, v[170:171]
	s_add_i32 m0, s23, 0xc000
	ds_read_b128 v[184:187], v196
	ds_read_b128 v[188:191], v196 offset:1024
	ds_read_b128 v[200:203], v196 offset:2048
	ds_read_b128 v[204:207], v196 offset:3072
	ds_read_b128 v[208:211], v196 offset:4096
	ds_read_b128 v[212:215], v196 offset:5120
	ds_read_b128 v[216:219], v196 offset:6144
	ds_read_b128 v[220:223], v196 offset:7168
	global_load_lds_dwordx4 v[224:225], off
	v_lshl_add_u64 v[224:225], s[24:25], 0, v[172:173]
	s_add_i32 m0, s23, 0xe000
	s_nop 0
	global_load_lds_dwordx4 v[224:225], off
	s_waitcnt vmcnt(8)
	s_waitcnt lgkmcnt(0)
	s_barrier
	s_setprio 1
	s_waitcnt lgkmcnt(0)
	v_mfma_i32_16x16x64_i8 v[126:129], v[158:161], v[184:187], 0
	s_nop 0
	v_mfma_i32_16x16x64_i8 v[126:129], v[154:157], v[188:191], v[126:129]
	v_mfma_i32_16x16x64_i8 v[118:121], v[150:153], v[184:187], 0
	s_nop 0
	v_mfma_i32_16x16x64_i8 v[118:121], v[146:149], v[188:191], v[118:121]
	v_mfma_i32_16x16x64_i8 v[114:117], v[158:161], v[200:203], 0
	s_nop 0
	v_mfma_i32_16x16x64_i8 v[114:117], v[154:157], v[204:207], v[114:117]
	v_mfma_i32_16x16x64_i8 v[110:113], v[150:153], v[200:203], 0
	s_nop 0
	v_mfma_i32_16x16x64_i8 v[110:113], v[146:149], v[204:207], v[110:113]
	v_mfma_i32_16x16x64_i8 v[94:97], v[158:161], v[208:211], 0
	s_nop 0
	v_mfma_i32_16x16x64_i8 v[94:97], v[154:157], v[212:215], v[94:97]
	v_mfma_i32_16x16x64_i8 v[86:89], v[150:153], v[208:211], 0
	s_nop 0
	v_mfma_i32_16x16x64_i8 v[86:89], v[146:149], v[212:215], v[86:89]
	v_mfma_i32_16x16x64_i8 v[82:85], v[158:161], v[216:219], 0
	s_nop 0
	v_mfma_i32_16x16x64_i8 v[82:85], v[154:157], v[220:223], v[82:85]
	v_mfma_i32_16x16x64_i8 v[74:77], v[150:153], v[216:219], 0
	s_nop 0
	v_mfma_i32_16x16x64_i8 v[74:77], v[146:149], v[220:223], v[74:77]
	s_setprio 0
	s_setprio 1
	v_mfma_i32_16x16x64_i8 v[122:125], v[142:145], v[184:187], 0
	s_nop 0
	v_mfma_i32_16x16x64_i8 v[122:125], v[138:141], v[188:191], v[122:125]
	v_mfma_i32_16x16x64_i8 v[106:109], v[134:137], v[184:187], 0
	s_nop 0
	v_mfma_i32_16x16x64_i8 v[106:109], v[130:133], v[188:191], v[106:109]
	v_mfma_i32_16x16x64_i8 v[102:105], v[142:145], v[200:203], 0
	s_nop 0
	v_mfma_i32_16x16x64_i8 v[102:105], v[138:141], v[204:207], v[102:105]
	v_mfma_i32_16x16x64_i8 v[98:101], v[134:137], v[200:203], 0
	s_nop 0
	v_mfma_i32_16x16x64_i8 v[98:101], v[130:133], v[204:207], v[98:101]
	v_mfma_i32_16x16x64_i8 v[90:93], v[142:145], v[208:211], 0
	s_nop 0
	v_mfma_i32_16x16x64_i8 v[90:93], v[138:141], v[212:215], v[90:93]
	v_mfma_i32_16x16x64_i8 v[78:81], v[134:137], v[208:211], 0
	s_nop 0
	v_mfma_i32_16x16x64_i8 v[78:81], v[130:133], v[212:215], v[78:81]
	v_mfma_i32_16x16x64_i8 v[70:73], v[142:145], v[216:219], 0
	s_nop 0
	v_mfma_i32_16x16x64_i8 v[70:73], v[138:141], v[220:223], v[70:73]
	v_mfma_i32_16x16x64_i8 v[66:69], v[134:137], v[216:219], 0
	s_nop 0
	v_mfma_i32_16x16x64_i8 v[66:69], v[130:133], v[220:223], v[66:69]
	s_setprio 0
	s_barrier
	s_add_i32 s52, s43, s33
	v_lshl_add_u64 v[184:185], s[26:27], 0, v[166:167]
	s_mov_b32 m0, s52
	ds_read_b128 v[200:203], v196 offset:16384
	ds_read_b128 v[204:207], v196 offset:17408
	ds_read_b128 v[208:211], v196 offset:18432
	ds_read_b128 v[212:215], v196 offset:19456
	ds_read_b128 v[216:219], v196 offset:20480
	ds_read_b128 v[220:223], v196 offset:21504
	ds_read_b128 v[224:227], v196 offset:22528
	ds_read_b128 v[228:231], v196 offset:23552
	global_load_lds_dwordx4 v[184:185], off
	s_add_i32 m0, s52, 0x2000
	s_add_u32 s52, s26, 0x40000
	v_lshl_add_u64 v[186:187], s[26:27], 0, v[162:163]
	s_addc_u32 s53, s27, 0
	s_add_i32 s54, s44, s33
	global_load_lds_dwordx4 v[186:187], off
	v_lshl_add_u64 v[188:189], s[52:53], 0, v[166:167]
	s_mov_b32 m0, s54
	v_lshl_add_u64 v[190:191], s[28:29], 0, v[164:165]
	global_load_lds_dwordx4 v[188:189], off
	v_lshl_add_u64 v[188:189], s[52:53], 0, v[162:163]
	s_add_i32 m0, s54, 0x2000
	s_nop 0
	global_load_lds_dwordx4 v[188:189], off
	v_lshl_add_u64 v[188:189], s[28:29], 0, v[168:169]
	s_mov_b32 m0, s23
	s_nop 0
	global_load_lds_dwordx4 v[188:189], off
	s_mov_b32 m0, s36
	s_nop 0
	global_load_lds_dwordx4 v[190:191], off
	s_waitcnt vmcnt(8)
	s_waitcnt lgkmcnt(0)
	s_barrier
	s_setprio 1
	s_waitcnt lgkmcnt(0)
	v_mfma_i32_16x16x64_i8 v[62:65], v[158:161], v[200:203], 0
	s_nop 0
	v_mfma_i32_16x16x64_i8 v[62:65], v[154:157], v[204:207], v[62:65]
	v_mfma_i32_16x16x64_i8 v[58:61], v[150:153], v[200:203], 0
	s_nop 0
	v_mfma_i32_16x16x64_i8 v[58:61], v[146:149], v[204:207], v[58:61]
	v_mfma_i32_16x16x64_i8 v[50:53], v[158:161], v[208:211], 0
	s_nop 0
	v_mfma_i32_16x16x64_i8 v[50:53], v[154:157], v[212:215], v[50:53]
	v_mfma_i32_16x16x64_i8 v[42:45], v[150:153], v[208:211], 0
	s_nop 0
	v_mfma_i32_16x16x64_i8 v[42:45], v[146:149], v[212:215], v[42:45]
	v_mfma_i32_16x16x64_i8 v[34:37], v[158:161], v[216:219], 0
	s_nop 0
	v_mfma_i32_16x16x64_i8 v[34:37], v[154:157], v[220:223], v[34:37]
	v_mfma_i32_16x16x64_i8 v[26:29], v[150:153], v[216:219], 0
	s_nop 0
	v_mfma_i32_16x16x64_i8 v[26:29], v[146:149], v[220:223], v[26:29]
	v_mfma_i32_16x16x64_i8 v[18:21], v[158:161], v[224:227], 0
	s_nop 0
	v_mfma_i32_16x16x64_i8 v[18:21], v[154:157], v[228:231], v[18:21]
	v_mfma_i32_16x16x64_i8 v[10:13], v[150:153], v[224:227], 0
	s_nop 0
	v_mfma_i32_16x16x64_i8 v[10:13], v[146:149], v[228:231], v[10:13]
	s_setprio 0
	s_setprio 1
	v_mfma_i32_16x16x64_i8 v[54:57], v[142:145], v[200:203], 0
	s_nop 0
	v_mfma_i32_16x16x64_i8 v[54:57], v[138:141], v[204:207], v[54:57]
	v_mfma_i32_16x16x64_i8 v[46:49], v[134:137], v[200:203], 0
	s_nop 0
	v_mfma_i32_16x16x64_i8 v[46:49], v[130:133], v[204:207], v[46:49]
	v_mfma_i32_16x16x64_i8 v[38:41], v[142:145], v[208:211], 0
	s_nop 0
	v_mfma_i32_16x16x64_i8 v[38:41], v[138:141], v[212:215], v[38:41]
	v_mfma_i32_16x16x64_i8 v[30:33], v[134:137], v[208:211], 0
	s_nop 0
	v_mfma_i32_16x16x64_i8 v[30:33], v[130:133], v[212:215], v[30:33]
	v_mfma_i32_16x16x64_i8 v[22:25], v[142:145], v[216:219], 0
	s_nop 0
	v_mfma_i32_16x16x64_i8 v[22:25], v[138:141], v[220:223], v[22:25]
	v_mfma_i32_16x16x64_i8 v[14:17], v[134:137], v[216:219], 0
	s_nop 0
	v_mfma_i32_16x16x64_i8 v[14:17], v[130:133], v[220:223], v[14:17]
	v_mfma_i32_16x16x64_i8 v[6:9], v[142:145], v[224:227], 0
	s_nop 0
	v_mfma_i32_16x16x64_i8 v[6:9], v[138:141], v[228:231], v[6:9]
	v_mfma_i32_16x16x64_i8 v[2:5], v[134:137], v[224:227], 0
	s_nop 0
	v_mfma_i32_16x16x64_i8 v[2:5], v[130:133], v[228:231], v[2:5]
	s_setprio 0
	s_barrier
	s_add_i32 s52, 0, 0x18000
	s_add_i32 s53, 0, 0x1c000
	v_add_u32_e32 v142, s52, v183
	v_add_u32_e32 v158, s53, v183
	ds_read_b128 v[130:133], v142
	ds_read_b128 v[134:137], v142 offset:1024
	ds_read_b128 v[138:141], v142 offset:2048
	ds_read_b128 v[142:145], v142 offset:3072
	ds_read_b128 v[146:149], v158
	ds_read_b128 v[150:153], v158 offset:1024
	ds_read_b128 v[154:157], v158 offset:2048
	ds_read_b128 v[158:161], v158 offset:3072
	s_add_u32 s28, s28, 0x40000
	s_addc_u32 s29, s29, 0
	s_mov_b32 m0, s37
	v_lshl_add_u64 v[232:233], s[28:29], 0, v[168:169]
	ds_read_b128 v[200:203], v196 offset:32768
	ds_read_b128 v[204:207], v196 offset:33792
	ds_read_b128 v[208:211], v196 offset:34816
	ds_read_b128 v[212:215], v196 offset:35840
	ds_read_b128 v[216:219], v196 offset:36864
	ds_read_b128 v[220:223], v196 offset:37888
	ds_read_b128 v[224:227], v196 offset:38912
	ds_read_b128 v[228:231], v196 offset:39936
	global_load_lds_dwordx4 v[232:233], off
	v_lshl_add_u64 v[232:233], s[28:29], 0, v[164:165]
	s_mov_b32 m0, s38
	s_nop 0
	global_load_lds_dwordx4 v[232:233], off
	s_waitcnt vmcnt(8)
	s_waitcnt lgkmcnt(0)
	s_barrier
	s_setprio 1
	s_waitcnt lgkmcnt(0)
	v_mfma_i32_16x16x64_i8 v[126:129], v[130:133], v[200:203], v[126:129]
	s_nop 0
	v_mfma_i32_16x16x64_i8 v[126:129], v[134:137], v[204:207], v[126:129]
	v_mfma_i32_16x16x64_i8 v[118:121], v[138:141], v[200:203], v[118:121]
	s_nop 0
	v_mfma_i32_16x16x64_i8 v[118:121], v[142:145], v[204:207], v[118:121]
	v_mfma_i32_16x16x64_i8 v[114:117], v[130:133], v[208:211], v[114:117]
	s_nop 0
	v_mfma_i32_16x16x64_i8 v[114:117], v[134:137], v[212:215], v[114:117]
	v_mfma_i32_16x16x64_i8 v[110:113], v[138:141], v[208:211], v[110:113]
	s_nop 0
	v_mfma_i32_16x16x64_i8 v[110:113], v[142:145], v[212:215], v[110:113]
	v_mfma_i32_16x16x64_i8 v[94:97], v[130:133], v[216:219], v[94:97]
	s_nop 0
	v_mfma_i32_16x16x64_i8 v[94:97], v[134:137], v[220:223], v[94:97]
	v_mfma_i32_16x16x64_i8 v[86:89], v[138:141], v[216:219], v[86:89]
	s_nop 0
	v_mfma_i32_16x16x64_i8 v[86:89], v[142:145], v[220:223], v[86:89]
	v_mfma_i32_16x16x64_i8 v[82:85], v[130:133], v[224:227], v[82:85]
	s_nop 0
	v_mfma_i32_16x16x64_i8 v[82:85], v[134:137], v[228:231], v[82:85]
	v_mfma_i32_16x16x64_i8 v[74:77], v[138:141], v[224:227], v[74:77]
	s_nop 0
	v_mfma_i32_16x16x64_i8 v[74:77], v[142:145], v[228:231], v[74:77]
	s_setprio 0
	s_setprio 1
	v_mfma_i32_16x16x64_i8 v[122:125], v[146:149], v[200:203], v[122:125]
	s_nop 0
	v_mfma_i32_16x16x64_i8 v[122:125], v[150:153], v[204:207], v[122:125]
	v_mfma_i32_16x16x64_i8 v[106:109], v[154:157], v[200:203], v[106:109]
	s_nop 0
	v_mfma_i32_16x16x64_i8 v[106:109], v[158:161], v[204:207], v[106:109]
	v_mfma_i32_16x16x64_i8 v[102:105], v[146:149], v[208:211], v[102:105]
	s_nop 0
	v_mfma_i32_16x16x64_i8 v[102:105], v[150:153], v[212:215], v[102:105]
	v_mfma_i32_16x16x64_i8 v[98:101], v[154:157], v[208:211], v[98:101]
	s_nop 0
	v_mfma_i32_16x16x64_i8 v[98:101], v[158:161], v[212:215], v[98:101]
	v_mfma_i32_16x16x64_i8 v[90:93], v[146:149], v[216:219], v[90:93]
	s_nop 0
	v_mfma_i32_16x16x64_i8 v[90:93], v[150:153], v[220:223], v[90:93]
	v_mfma_i32_16x16x64_i8 v[78:81], v[154:157], v[216:219], v[78:81]
	s_nop 0
	v_mfma_i32_16x16x64_i8 v[78:81], v[158:161], v[220:223], v[78:81]
	v_mfma_i32_16x16x64_i8 v[70:73], v[146:149], v[224:227], v[70:73]
	s_nop 0
	v_mfma_i32_16x16x64_i8 v[70:73], v[150:153], v[228:231], v[70:73]
	v_mfma_i32_16x16x64_i8 v[66:69], v[154:157], v[224:227], v[66:69]
	s_nop 0
	v_mfma_i32_16x16x64_i8 v[66:69], v[158:161], v[228:231], v[66:69]
	s_setprio 0
	s_barrier
	s_add_i32 s28, s52, s33
	v_lshl_add_u64 v[184:185], v[184:185], 0, s[10:11]
	s_mov_b32 m0, s28
	ds_read_b128 v[200:203], v196 offset:49152
	ds_read_b128 v[204:207], v196 offset:50176
	ds_read_b128 v[208:211], v196 offset:51200
	ds_read_b128 v[212:215], v196 offset:52224
	ds_read_b128 v[216:219], v196 offset:53248
	ds_read_b128 v[220:223], v196 offset:54272
	ds_read_b128 v[224:227], v196 offset:55296
	ds_read_b128 v[228:231], v196 offset:56320
	global_load_lds_dwordx4 v[184:185], off
	s_add_i32 m0, s28, 0x2000
	s_add_u32 s26, s26, 0x40080
	v_lshl_add_u64 v[184:185], v[186:187], 0, s[10:11]
	s_addc_u32 s27, s27, 0
	s_add_i32 s28, s53, s33
	global_load_lds_dwordx4 v[184:185], off
	v_lshl_add_u64 v[184:185], s[26:27], 0, v[166:167]
	s_mov_b32 m0, s28
	s_nop 0
	global_load_lds_dwordx4 v[184:185], off
	v_lshl_add_u64 v[184:185], s[26:27], 0, v[162:163]
	s_add_i32 m0, s28, 0x2000
	s_nop 0
	global_load_lds_dwordx4 v[184:185], off
	v_lshl_add_u64 v[184:185], v[188:189], 0, s[10:11]
	s_mov_b32 m0, s40
	s_nop 0
	global_load_lds_dwordx4 v[184:185], off
	v_lshl_add_u64 v[184:185], v[190:191], 0, s[10:11]
	s_mov_b32 m0, s41
	s_nop 0
	global_load_lds_dwordx4 v[184:185], off
	s_waitcnt vmcnt(8)
	s_waitcnt lgkmcnt(0)
	s_barrier
	s_setprio 1
	s_waitcnt lgkmcnt(0)
	v_mfma_i32_16x16x64_i8 v[62:65], v[130:133], v[200:203], v[62:65]
	s_nop 0
	v_mfma_i32_16x16x64_i8 v[62:65], v[134:137], v[204:207], v[62:65]
	v_mfma_i32_16x16x64_i8 v[58:61], v[138:141], v[200:203], v[58:61]
	s_nop 0
	v_mfma_i32_16x16x64_i8 v[58:61], v[142:145], v[204:207], v[58:61]
	v_mfma_i32_16x16x64_i8 v[50:53], v[130:133], v[208:211], v[50:53]
	s_nop 0
	v_mfma_i32_16x16x64_i8 v[50:53], v[134:137], v[212:215], v[50:53]
	v_mfma_i32_16x16x64_i8 v[42:45], v[138:141], v[208:211], v[42:45]
	s_nop 0
	v_mfma_i32_16x16x64_i8 v[42:45], v[142:145], v[212:215], v[42:45]
	v_mfma_i32_16x16x64_i8 v[34:37], v[130:133], v[216:219], v[34:37]
	s_nop 0
	v_mfma_i32_16x16x64_i8 v[34:37], v[134:137], v[220:223], v[34:37]
	v_mfma_i32_16x16x64_i8 v[26:29], v[138:141], v[216:219], v[26:29]
	s_nop 0
	v_mfma_i32_16x16x64_i8 v[26:29], v[142:145], v[220:223], v[26:29]
	v_mfma_i32_16x16x64_i8 v[18:21], v[130:133], v[224:227], v[18:21]
	s_nop 0
	v_mfma_i32_16x16x64_i8 v[18:21], v[134:137], v[228:231], v[18:21]
	v_mfma_i32_16x16x64_i8 v[10:13], v[138:141], v[224:227], v[10:13]
	s_nop 0
	v_mfma_i32_16x16x64_i8 v[10:13], v[142:145], v[228:231], v[10:13]
	s_setprio 0
	s_setprio 1
	v_mfma_i32_16x16x64_i8 v[54:57], v[146:149], v[200:203], v[54:57]
	s_nop 0
	v_mfma_i32_16x16x64_i8 v[54:57], v[150:153], v[204:207], v[54:57]
	v_mfma_i32_16x16x64_i8 v[46:49], v[154:157], v[200:203], v[46:49]
	s_nop 0
	v_mfma_i32_16x16x64_i8 v[46:49], v[158:161], v[204:207], v[46:49]
	v_mfma_i32_16x16x64_i8 v[38:41], v[146:149], v[208:211], v[38:41]
	s_nop 0
	v_mfma_i32_16x16x64_i8 v[38:41], v[150:153], v[212:215], v[38:41]
	v_mfma_i32_16x16x64_i8 v[30:33], v[154:157], v[208:211], v[30:33]
	s_nop 0
	v_mfma_i32_16x16x64_i8 v[30:33], v[158:161], v[212:215], v[30:33]
	v_mfma_i32_16x16x64_i8 v[22:25], v[146:149], v[216:219], v[22:25]
	s_nop 0
	v_mfma_i32_16x16x64_i8 v[22:25], v[150:153], v[220:223], v[22:25]
	v_mfma_i32_16x16x64_i8 v[14:17], v[154:157], v[216:219], v[14:17]
	s_nop 0
	v_mfma_i32_16x16x64_i8 v[14:17], v[158:161], v[220:223], v[14:17]
	v_mfma_i32_16x16x64_i8 v[6:9], v[146:149], v[224:227], v[6:9]
	s_nop 0
	v_mfma_i32_16x16x64_i8 v[6:9], v[150:153], v[228:231], v[6:9]
	v_mfma_i32_16x16x64_i8 v[2:5], v[154:157], v[224:227], v[2:5]
	s_nop 0
	v_mfma_i32_16x16x64_i8 v[2:5], v[158:161], v[228:231], v[2:5]
	s_setprio 0
	s_barrier
	s_add_i32 s51, s51, 2
	s_add_u32 s24, s24, 0x100
	s_addc_u32 s25, s25, 0
	s_add_u32 s49, s49, 0x100
	s_addc_u32 s50, s50, 0
	s_cmp_gt_u32 s51, 13
	s_cbranch_scc1 .Lpeel_exit_764

.LBB0_875:
	s_add_u32 s16, s16, 0xb0080
	s_addc_u32 s17, s17, 0
	s_add_u32 s50, s18, 0x100
	s_waitcnt vmcnt(0)
	v_mov_b32_e32 v34, 0
	s_addc_u32 s51, s19, 0
	s_mov_b32 s52, -2
	ds_read_b128 v[18:21], v188
	ds_read_b128 v[22:25], v188 offset:1024
	ds_read_b128 v[26:29], v188 offset:2048
	ds_read_b128 v[30:33], v188 offset:3072
	ds_read_b128 v[2:5], v189
	ds_read_b128 v[6:9], v189 offset:1024
	ds_read_b128 v[10:13], v189 offset:2048
	ds_read_b128 v[14:17], v189 offset:3072
	s_add_u32 s18, s16, 0xfff50080
	s_addc_u32 s19, s17, -1
	s_cmp_eq_u32 s52, 40
	s_cselect_b32 s23, s3, s19
	s_cselect_b32 s22, s2, s18
	s_cselect_b32 s19, s5, s51
	s_cselect_b32 s18, s4, s50
	v_lshl_add_u64 v[174:175], s[16:17], 0, v[166:167]
	s_add_i32 m0, s27, 0xc000
	ds_read_b128 v[200:203], v190
	ds_read_b128 v[204:207], v190 offset:1024
	ds_read_b128 v[208:211], v190 offset:2048
	ds_read_b128 v[212:215], v190 offset:3072
	ds_read_b128 v[216:219], v190 offset:4096
	ds_read_b128 v[220:223], v190 offset:5120
	ds_read_b128 v[224:227], v190 offset:6144
	ds_read_b128 v[228:231], v190 offset:7168
	global_load_lds_dwordx4 v[174:175], off
	v_lshl_add_u64 v[174:175], s[16:17], 0, v[168:169]
	s_add_i32 m0, s27, 0xe000
	s_nop 0
	global_load_lds_dwordx4 v[174:175], off
	s_waitcnt vmcnt(8)
	s_waitcnt lgkmcnt(0)
	s_barrier
	s_setprio 1
	s_waitcnt lgkmcnt(0)
	v_mfma_scale_f32_16x16x128_f8f6f4 v[158:161], v[18:25], v[200:207], 0, v191, v192 op_sel_hi:[0,0,0]
	v_mfma_scale_f32_16x16x128_f8f6f4 v[154:157], v[26:33], v[200:207], 0, v191, v192 op_sel_hi:[0,0,0]
	v_mfma_scale_f32_16x16x128_f8f6f4 v[142:145], v[18:25], v[208:215], 0, v191, v192 op_sel_hi:[0,0,0]
	v_mfma_scale_f32_16x16x128_f8f6f4 v[138:141], v[26:33], v[208:215], 0, v191, v192 op_sel_hi:[0,0,0]
	v_mfma_scale_f32_16x16x128_f8f6f4 v[126:129], v[18:25], v[216:223], 0, v191, v192 op_sel_hi:[0,0,0]
	v_mfma_scale_f32_16x16x128_f8f6f4 v[122:125], v[26:33], v[216:223], 0, v191, v192 op_sel_hi:[0,0,0]
	v_mfma_scale_f32_16x16x128_f8f6f4 v[110:113], v[18:25], v[224:231], 0, v191, v192 op_sel_hi:[0,0,0]
	v_mfma_scale_f32_16x16x128_f8f6f4 v[106:109], v[26:33], v[224:231], 0, v191, v192 op_sel_hi:[0,0,0]
	s_setprio 0
	s_setprio 1
	v_mfma_scale_f32_16x16x128_f8f6f4 v[150:153], v[2:9], v[200:207], 0, v191, v192 op_sel_hi:[0,0,0]
	v_mfma_scale_f32_16x16x128_f8f6f4 v[146:149], v[10:17], v[200:207], 0, v191, v192 op_sel_hi:[0,0,0]
	v_mfma_scale_f32_16x16x128_f8f6f4 v[134:137], v[2:9], v[208:215], 0, v191, v192 op_sel_hi:[0,0,0]
	v_mfma_scale_f32_16x16x128_f8f6f4 v[130:133], v[10:17], v[208:215], 0, v191, v192 op_sel_hi:[0,0,0]
	v_mfma_scale_f32_16x16x128_f8f6f4 v[118:121], v[2:9], v[216:223], 0, v191, v192 op_sel_hi:[0,0,0]
	v_mfma_scale_f32_16x16x128_f8f6f4 v[114:117], v[10:17], v[216:223], 0, v191, v192 op_sel_hi:[0,0,0]
	v_mfma_scale_f32_16x16x128_f8f6f4 v[102:105], v[2:9], v[224:231], 0, v191, v192 op_sel_hi:[0,0,0]
	v_mfma_scale_f32_16x16x128_f8f6f4 v[98:101], v[10:17], v[224:231], 0, v191, v192 op_sel_hi:[0,0,0]
	s_setprio 0
	s_barrier
	s_add_i32 s53, s42, s26
	v_lshl_add_u64 v[174:175], s[18:19], 0, v[162:163]
	s_mov_b32 m0, s53
	ds_read_b128 v[200:203], v190 offset:16384
	ds_read_b128 v[204:207], v190 offset:17408
	ds_read_b128 v[208:211], v190 offset:18432
	ds_read_b128 v[212:215], v190 offset:19456
	ds_read_b128 v[216:219], v190 offset:20480
	ds_read_b128 v[220:223], v190 offset:21504
	ds_read_b128 v[224:227], v190 offset:22528
	ds_read_b128 v[228:231], v190 offset:23552
	global_load_lds_dwordx4 v[174:175], off
	s_add_i32 m0, s53, 0x2000
	s_add_u32 s54, s18, 0xb0000
	v_lshl_add_u64 v[176:177], s[18:19], 0, v[164:165]
	s_addc_u32 s55, s19, 0
	s_add_i32 s53, s43, s26
	global_load_lds_dwordx4 v[176:177], off
	v_lshl_add_u64 v[184:185], s[54:55], 0, v[162:163]
	s_mov_b32 m0, s53
	v_lshl_add_u64 v[186:187], s[22:23], 0, v[164:165]
	global_load_lds_dwordx4 v[184:185], off
	v_lshl_add_u64 v[184:185], s[54:55], 0, v[164:165]
	s_add_i32 m0, s53, 0x2000
	s_nop 0
	global_load_lds_dwordx4 v[184:185], off
	v_lshl_add_u64 v[184:185], s[22:23], 0, v[162:163]
	s_mov_b32 m0, s27
	s_nop 0
	global_load_lds_dwordx4 v[184:185], off
	s_mov_b32 m0, s33
	s_nop 0
	global_load_lds_dwordx4 v[186:187], off
	s_waitcnt vmcnt(8)
	s_waitcnt lgkmcnt(0)
	s_barrier
	s_setprio 1
	s_waitcnt lgkmcnt(0)
	v_mfma_scale_f32_16x16x128_f8f6f4 v[94:97], v[18:25], v[200:207], 0, v191, v192 op_sel_hi:[0,0,0]
	v_mfma_scale_f32_16x16x128_f8f6f4 v[90:93], v[26:33], v[200:207], 0, v191, v192 op_sel_hi:[0,0,0]
	v_mfma_scale_f32_16x16x128_f8f6f4 v[78:81], v[18:25], v[208:215], 0, v191, v192 op_sel_hi:[0,0,0]
	v_mfma_scale_f32_16x16x128_f8f6f4 v[74:77], v[26:33], v[208:215], 0, v191, v192 op_sel_hi:[0,0,0]
	v_mfma_scale_f32_16x16x128_f8f6f4 v[62:65], v[18:25], v[216:223], 0, v191, v192 op_sel_hi:[0,0,0]
	v_mfma_scale_f32_16x16x128_f8f6f4 v[58:61], v[26:33], v[216:223], 0, v191, v192 op_sel_hi:[0,0,0]
	v_mfma_scale_f32_16x16x128_f8f6f4 v[46:49], v[18:25], v[224:231], 0, v191, v192 op_sel_hi:[0,0,0]
	v_mfma_scale_f32_16x16x128_f8f6f4 v[42:45], v[26:33], v[224:231], 0, v191, v192 op_sel_hi:[0,0,0]
	s_setprio 0
	s_setprio 1
	v_mfma_scale_f32_16x16x128_f8f6f4 v[86:89], v[2:9], v[200:207], 0, v191, v192 op_sel_hi:[0,0,0]
	v_mfma_scale_f32_16x16x128_f8f6f4 v[82:85], v[10:17], v[200:207], 0, v191, v192 op_sel_hi:[0,0,0]
	v_mfma_scale_f32_16x16x128_f8f6f4 v[70:73], v[2:9], v[208:215], 0, v191, v192 op_sel_hi:[0,0,0]
	v_mfma_scale_f32_16x16x128_f8f6f4 v[66:69], v[10:17], v[208:215], 0, v191, v192 op_sel_hi:[0,0,0]
	v_mfma_scale_f32_16x16x128_f8f6f4 v[54:57], v[2:9], v[216:223], 0, v191, v192 op_sel_hi:[0,0,0]
	v_mfma_scale_f32_16x16x128_f8f6f4 v[50:53], v[10:17], v[216:223], 0, v191, v192 op_sel_hi:[0,0,0]
	v_mfma_scale_f32_16x16x128_f8f6f4 v[38:41], v[2:9], v[224:231], 0, v191, v192 op_sel_hi:[0,0,0]
	v_mfma_scale_f32_16x16x128_f8f6f4 v[34:37], v[10:17], v[224:231], 0, v191, v192 op_sel_hi:[0,0,0]
	s_setprio 0
	s_barrier
	s_add_i32 s53, 0, 0x18000
	s_add_i32 s54, 0, 0x1c000
	v_add_u32_e32 v14, s53, v181
	v_add_u32_e32 v30, s54, v181
	ds_read_b128 v[2:5], v14
	ds_read_b128 v[6:9], v14 offset:1024
	ds_read_b128 v[10:13], v14 offset:2048
	ds_read_b128 v[14:17], v14 offset:3072
	ds_read_b128 v[18:21], v30
	ds_read_b128 v[22:25], v30 offset:1024
	ds_read_b128 v[26:29], v30 offset:2048
	ds_read_b128 v[30:33], v30 offset:3072
	s_add_u32 s22, s22, 0xb0000
	s_addc_u32 s23, s23, 0
	s_mov_b32 m0, s34
	v_lshl_add_u64 v[232:233], s[22:23], 0, v[162:163]
	ds_read_b128 v[200:203], v190 offset:32768
	ds_read_b128 v[204:207], v190 offset:33792
	ds_read_b128 v[208:211], v190 offset:34816
	ds_read_b128 v[212:215], v190 offset:35840
	ds_read_b128 v[216:219], v190 offset:36864
	ds_read_b128 v[220:223], v190 offset:37888
	ds_read_b128 v[224:227], v190 offset:38912
	ds_read_b128 v[228:231], v190 offset:39936
	global_load_lds_dwordx4 v[232:233], off
	v_lshl_add_u64 v[232:233], s[22:23], 0, v[164:165]
	s_mov_b32 m0, s35
	s_nop 0
	global_load_lds_dwordx4 v[232:233], off
	s_waitcnt vmcnt(8)
	s_waitcnt lgkmcnt(0)
	s_barrier
	s_setprio 1
	s_waitcnt lgkmcnt(0)
	v_mfma_scale_f32_16x16x128_f8f6f4 v[158:161], v[2:9], v[200:207], v[158:161], v191, v192 op_sel_hi:[0,0,0]
	v_mfma_scale_f32_16x16x128_f8f6f4 v[154:157], v[10:17], v[200:207], v[154:157], v191, v192 op_sel_hi:[0,0,0]
	v_mfma_scale_f32_16x16x128_f8f6f4 v[142:145], v[2:9], v[208:215], v[142:145], v191, v192 op_sel_hi:[0,0,0]
	v_mfma_scale_f32_16x16x128_f8f6f4 v[138:141], v[10:17], v[208:215], v[138:141], v191, v192 op_sel_hi:[0,0,0]
	v_mfma_scale_f32_16x16x128_f8f6f4 v[126:129], v[2:9], v[216:223], v[126:129], v191, v192 op_sel_hi:[0,0,0]
	v_mfma_scale_f32_16x16x128_f8f6f4 v[122:125], v[10:17], v[216:223], v[122:125], v191, v192 op_sel_hi:[0,0,0]
	v_mfma_scale_f32_16x16x128_f8f6f4 v[110:113], v[2:9], v[224:231], v[110:113], v191, v192 op_sel_hi:[0,0,0]
	v_mfma_scale_f32_16x16x128_f8f6f4 v[106:109], v[10:17], v[224:231], v[106:109], v191, v192 op_sel_hi:[0,0,0]
	s_setprio 0
	s_setprio 1
	v_mfma_scale_f32_16x16x128_f8f6f4 v[150:153], v[18:25], v[200:207], v[150:153], v191, v192 op_sel_hi:[0,0,0]
	v_mfma_scale_f32_16x16x128_f8f6f4 v[146:149], v[26:33], v[200:207], v[146:149], v191, v192 op_sel_hi:[0,0,0]
	v_mfma_scale_f32_16x16x128_f8f6f4 v[134:137], v[18:25], v[208:215], v[134:137], v191, v192 op_sel_hi:[0,0,0]
	v_mfma_scale_f32_16x16x128_f8f6f4 v[130:133], v[26:33], v[208:215], v[130:133], v191, v192 op_sel_hi:[0,0,0]
	v_mfma_scale_f32_16x16x128_f8f6f4 v[118:121], v[18:25], v[216:223], v[118:121], v191, v192 op_sel_hi:[0,0,0]
	v_mfma_scale_f32_16x16x128_f8f6f4 v[114:117], v[26:33], v[216:223], v[114:117], v191, v192 op_sel_hi:[0,0,0]
	v_mfma_scale_f32_16x16x128_f8f6f4 v[102:105], v[18:25], v[224:231], v[102:105], v191, v192 op_sel_hi:[0,0,0]
	v_mfma_scale_f32_16x16x128_f8f6f4 v[98:101], v[26:33], v[224:231], v[98:101], v191, v192 op_sel_hi:[0,0,0]
	s_setprio 0
	s_barrier
	s_add_i32 s22, s53, s26
	v_lshl_add_u64 v[174:175], v[174:175], 0, s[10:11]
	s_mov_b32 m0, s22
	ds_read_b128 v[200:203], v190 offset:49152
	ds_read_b128 v[204:207], v190 offset:50176
	ds_read_b128 v[208:211], v190 offset:51200
	ds_read_b128 v[212:215], v190 offset:52224
	ds_read_b128 v[216:219], v190 offset:53248
	ds_read_b128 v[220:223], v190 offset:54272
	ds_read_b128 v[224:227], v190 offset:55296
	ds_read_b128 v[228:231], v190 offset:56320
	global_load_lds_dwordx4 v[174:175], off
	s_add_i32 m0, s22, 0x2000
	s_add_u32 s18, s18, 0xb0080
	v_lshl_add_u64 v[174:175], v[176:177], 0, s[10:11]
	s_addc_u32 s19, s19, 0
	s_add_i32 s22, s54, s26
	global_load_lds_dwordx4 v[174:175], off
	v_lshl_add_u64 v[174:175], s[18:19], 0, v[162:163]
	s_mov_b32 m0, s22
	s_nop 0
	global_load_lds_dwordx4 v[174:175], off
	v_lshl_add_u64 v[174:175], s[18:19], 0, v[164:165]
	s_add_i32 m0, s22, 0x2000
	s_nop 0
	global_load_lds_dwordx4 v[174:175], off
	v_lshl_add_u64 v[174:175], v[184:185], 0, s[10:11]
	s_mov_b32 m0, s39
	s_nop 0
	global_load_lds_dwordx4 v[174:175], off
	v_lshl_add_u64 v[174:175], v[186:187], 0, s[10:11]
	s_mov_b32 m0, s40
	s_nop 0
	global_load_lds_dwordx4 v[174:175], off
	s_waitcnt vmcnt(8)
	s_waitcnt lgkmcnt(0)
	s_barrier
	s_setprio 1
	s_waitcnt lgkmcnt(0)
	v_mfma_scale_f32_16x16x128_f8f6f4 v[94:97], v[2:9], v[200:207], v[94:97], v191, v192 op_sel_hi:[0,0,0]
	v_mfma_scale_f32_16x16x128_f8f6f4 v[90:93], v[10:17], v[200:207], v[90:93], v191, v192 op_sel_hi:[0,0,0]
	v_mfma_scale_f32_16x16x128_f8f6f4 v[78:81], v[2:9], v[208:215], v[78:81], v191, v192 op_sel_hi:[0,0,0]
	v_mfma_scale_f32_16x16x128_f8f6f4 v[74:77], v[10:17], v[208:215], v[74:77], v191, v192 op_sel_hi:[0,0,0]
	v_mfma_scale_f32_16x16x128_f8f6f4 v[62:65], v[2:9], v[216:223], v[62:65], v191, v192 op_sel_hi:[0,0,0]
	v_mfma_scale_f32_16x16x128_f8f6f4 v[58:61], v[10:17], v[216:223], v[58:61], v191, v192 op_sel_hi:[0,0,0]
	v_mfma_scale_f32_16x16x128_f8f6f4 v[46:49], v[2:9], v[224:231], v[46:49], v191, v192 op_sel_hi:[0,0,0]
	v_mfma_scale_f32_16x16x128_f8f6f4 v[42:45], v[10:17], v[224:231], v[42:45], v191, v192 op_sel_hi:[0,0,0]
	s_setprio 0
	s_setprio 1
	v_mfma_scale_f32_16x16x128_f8f6f4 v[86:89], v[18:25], v[200:207], v[86:89], v191, v192 op_sel_hi:[0,0,0]
	v_mfma_scale_f32_16x16x128_f8f6f4 v[82:85], v[26:33], v[200:207], v[82:85], v191, v192 op_sel_hi:[0,0,0]
	v_mfma_scale_f32_16x16x128_f8f6f4 v[70:73], v[18:25], v[208:215], v[70:73], v191, v192 op_sel_hi:[0,0,0]
	v_mfma_scale_f32_16x16x128_f8f6f4 v[66:69], v[26:33], v[208:215], v[66:69], v191, v192 op_sel_hi:[0,0,0]
	v_mfma_scale_f32_16x16x128_f8f6f4 v[54:57], v[18:25], v[216:223], v[54:57], v191, v192 op_sel_hi:[0,0,0]
	v_mfma_scale_f32_16x16x128_f8f6f4 v[50:53], v[26:33], v[216:223], v[50:53], v191, v192 op_sel_hi:[0,0,0]
	v_mfma_scale_f32_16x16x128_f8f6f4 v[38:41], v[18:25], v[224:231], v[38:41], v191, v192 op_sel_hi:[0,0,0]
	v_mfma_scale_f32_16x16x128_f8f6f4 v[34:37], v[26:33], v[224:231], v[34:37], v191, v192 op_sel_hi:[0,0,0]
	s_setprio 0
	s_barrier
	s_add_i32 s52, s52, 2
	s_add_u32 s16, s16, 0x100
	s_addc_u32 s17, s17, 0
	s_add_u32 s50, s50, 0x100
	s_addc_u32 s51, s51, 0
	s_cmp_gt_u32 s52, 41
	s_cbranch_scc1 .Lpeel_exit_876

.Lpeel_exit_876:
	v_lshl_or_b32 v2, s49, 8, v183
	s_ashr_i32 s16, s48, 3
	v_lshl_add_u32 v184, s48, 8, v1
	s_mul_hi_i32 s17, s16, 0x1c000
	s_mul_i32 s16, s16, 0x1c000
	v_ashrrev_i32_e32 v3, 31, v2
	v_ashrrev_i32_e32 v185, 31, v184
	s_add_u32 s16, s37, s16
	v_lshlrev_b64 v[32:33], 2, v[2:3]
	v_lshlrev_b64 v[2:3], 13, v[184:185]
	s_addc_u32 s17, s38, s17
	v_lshl_add_u64 v[2:3], s[76:77], 0, v[2:3]
	s_nop 15
	s_nop 15
	v_lshl_add_u64 v[10:11], s[16:17], 0, v[32:33]
	v_lshl_add_u64 v[18:19], v[2:3], 0, v[32:33]
	global_load_dwordx4 v[20:23], v[18:19], off
	global_load_dwordx4 v[6:9], v[10:11], off
	global_load_dwordx4 v[2:5], v[10:11], off offset:64
	global_load_dwordx4 v[24:27], v[18:19], off offset:64
	global_load_dwordx4 v[28:31], v[18:19], off offset:512
	global_load_dwordx4 v[14:17], v[10:11], off offset:512
	s_nop 0
	global_load_dwordx4 v[10:13], v[10:11], off offset:576
	s_nop 0
	global_load_dwordx4 v[174:177], v[18:19], off offset:576
	v_or_b32_e32 v186, 16, v184
	v_ashrrev_i32_e32 v187, 31, v186
	v_lshlrev_b64 v[186:187], 13, v[186:187]
	v_lshl_add_u64 v[186:187], s[76:77], 0, v[186:187]
	v_lshl_add_u64 v[186:187], v[186:187], 0, v[32:33]
	s_mov_b32 s18, 0x100000
	s_mov_b64 s[16:17], 0x100000
	v_readlane_b32 s52, v250, 56
	s_mov_b32 s49, s46
	s_mov_b32 s48, s47
	v_readlane_b32 s64, v251, 4
	v_readlane_b32 s65, v251, 5
	v_readlane_b32 s66, v251, 6
	v_readlane_b32 s67, v251, 7
	v_readlane_b32 s53, v250, 57
	v_readlane_b32 s54, v250, 58
	v_readlane_b32 s55, v250, 59
	v_readlane_b32 s56, v250, 60
	v_readlane_b32 s57, v250, 61
	v_readlane_b32 s58, v250, 62
	v_readlane_b32 s59, v250, 63
	v_readlane_b32 s60, v251, 0
	v_readlane_b32 s61, v251, 1
	v_readlane_b32 s62, v251, 2
	v_readlane_b32 s63, v251, 3
	s_waitcnt vmcnt(0)
	v_pk_fma_f32 v[22:23], v[160:161], v[8:9], v[22:23]
	v_pk_fma_f32 v[20:21], v[158:159], v[6:7], v[20:21]
	v_pk_fma_f32 v[26:27], v[156:157], v[4:5], v[26:27]
	v_pk_fma_f32 v[24:25], v[154:155], v[2:3], v[24:25]
	v_pk_fma_f32 v[30:31], v[152:153], v[16:17], v[30:31]
	v_pk_fma_f32 v[28:29], v[150:151], v[14:15], v[28:29]
	v_pk_fma_f32 v[148:149], v[148:149], v[12:13], v[176:177]
	v_pk_fma_f32 v[146:147], v[146:147], v[10:11], v[174:175]
	global_store_dwordx4 v[18:19], v[20:23], off
	global_store_dwordx4 v[18:19], v[24:27], off offset:64
	global_store_dwordx4 v[18:19], v[28:31], off offset:512
	global_store_dwordx4 v[18:19], v[146:149], off offset:576
	global_load_dwordx4 v[20:23], v[186:187], off
	global_load_dwordx4 v[24:27], v[186:187], off offset:64
	global_load_dwordx4 v[28:31], v[186:187], off offset:512
	global_load_dwordx4 v[146:149], v[186:187], off offset:576
	v_or_b32_e32 v150, 32, v184
	v_ashrrev_i32_e32 v151, 31, v150
	v_lshlrev_b64 v[150:151], 13, v[150:151]
	v_lshl_add_u64 v[150:151], s[76:77], 0, v[150:151]
	v_lshl_add_u64 v[150:151], v[150:151], 0, v[32:33]
	s_waitcnt vmcnt(3)
	v_pk_fma_f32 v[22:23], v[144:145], v[8:9], v[22:23]
	v_pk_fma_f32 v[20:21], v[142:143], v[6:7], v[20:21]
	s_waitcnt vmcnt(2)
	v_pk_fma_f32 v[26:27], v[140:141], v[4:5], v[26:27]
	v_pk_fma_f32 v[24:25], v[138:139], v[2:3], v[24:25]
	s_waitcnt vmcnt(1)
	v_pk_fma_f32 v[30:31], v[136:137], v[16:17], v[30:31]
	v_pk_fma_f32 v[28:29], v[134:135], v[14:15], v[28:29]
	s_waitcnt vmcnt(0)
	v_pk_fma_f32 v[132:133], v[132:133], v[12:13], v[148:149]
	v_pk_fma_f32 v[130:131], v[130:131], v[10:11], v[146:147]
	global_store_dwordx4 v[186:187], v[20:23], off
	global_store_dwordx4 v[186:187], v[24:27], off offset:64
	global_store_dwordx4 v[186:187], v[28:31], off offset:512
	global_store_dwordx4 v[186:187], v[130:133], off offset:576
	global_load_dwordx4 v[20:23], v[150:151], off
	global_load_dwordx4 v[24:27], v[150:151], off offset:64
	global_load_dwordx4 v[28:31], v[150:151], off offset:512
	global_load_dwordx4 v[130:133], v[150:151], off offset:576
	v_or_b32_e32 v134, 48, v184
	v_ashrrev_i32_e32 v135, 31, v134
	v_lshlrev_b64 v[134:135], 13, v[134:135]
	v_lshl_add_u64 v[134:135], s[76:77], 0, v[134:135]
	v_lshl_add_u64 v[32:33], v[134:135], 0, v[32:33]
	s_waitcnt vmcnt(3)
	v_pk_fma_f32 v[22:23], v[128:129], v[8:9], v[22:23]
	v_pk_fma_f32 v[20:21], v[126:127], v[6:7], v[20:21]
	s_waitcnt vmcnt(2)
	v_pk_fma_f32 v[26:27], v[124:125], v[4:5], v[26:27]
	v_pk_fma_f32 v[24:25], v[122:123], v[2:3], v[24:25]
	s_waitcnt vmcnt(1)
	v_pk_fma_f32 v[30:31], v[120:121], v[16:17], v[30:31]
	v_pk_fma_f32 v[28:29], v[118:119], v[14:15], v[28:29]
	s_waitcnt vmcnt(0)
	v_pk_fma_f32 v[116:117], v[116:117], v[12:13], v[132:133]
	v_pk_fma_f32 v[114:115], v[114:115], v[10:11], v[130:131]
	global_store_dwordx4 v[150:151], v[20:23], off
	global_store_dwordx4 v[150:151], v[24:27], off offset:64
	global_store_dwordx4 v[150:151], v[28:31], off offset:512
	global_store_dwordx4 v[150:151], v[114:117], off offset:576
	global_load_dwordx4 v[20:23], v[32:33], off
	global_load_dwordx4 v[24:27], v[32:33], off offset:64
	global_load_dwordx4 v[28:31], v[32:33], off offset:512
	global_load_dwordx4 v[114:117], v[32:33], off offset:576
	v_add_co_u32_e32 v118, vcc, s18, v18
	s_mov_b64 s[18:19], s[4:5]
	s_nop 0
	v_addc_co_u32_e32 v119, vcc, 0, v19, vcc
	s_waitcnt vmcnt(3)
	v_pk_fma_f32 v[22:23], v[112:113], v[8:9], v[22:23]
	v_pk_fma_f32 v[20:21], v[110:111], v[6:7], v[20:21]
	s_waitcnt vmcnt(2)
	v_pk_fma_f32 v[26:27], v[108:109], v[4:5], v[26:27]
	v_pk_fma_f32 v[24:25], v[106:107], v[2:3], v[24:25]
	s_waitcnt vmcnt(1)
	v_pk_fma_f32 v[30:31], v[104:105], v[16:17], v[30:31]
	v_pk_fma_f32 v[28:29], v[102:103], v[14:15], v[28:29]
	s_waitcnt vmcnt(0)
	v_pk_fma_f32 v[100:101], v[100:101], v[12:13], v[116:117]
	v_pk_fma_f32 v[98:99], v[98:99], v[10:11], v[114:115]
	global_store_dwordx4 v[32:33], v[20:23], off
	global_store_dwordx4 v[32:33], v[24:27], off offset:64
	global_store_dwordx4 v[32:33], v[28:31], off offset:512
	global_store_dwordx4 v[32:33], v[98:101], off offset:576
	global_load_dwordx4 v[20:23], v[118:119], off
	v_lshl_add_u64 v[32:33], v[18:19], 0, s[16:17]
	global_load_dwordx4 v[24:27], v[32:33], off offset:64
	global_load_dwordx4 v[28:31], v[32:33], off offset:512
	global_load_dwordx4 v[98:101], v[32:33], off offset:576
	v_add_co_u32_e32 v102, vcc, s44, v18
	s_mov_b64 s[16:17], 0x120000
	s_nop 0
	v_addc_co_u32_e32 v103, vcc, 0, v19, vcc
	s_waitcnt vmcnt(2)
	v_pk_fma_f32 v[26:27], v[92:93], v[4:5], v[26:27]
	v_pk_fma_f32 v[22:23], v[96:97], v[8:9], v[22:23]
	v_pk_fma_f32 v[20:21], v[94:95], v[6:7], v[20:21]
	v_pk_fma_f32 v[24:25], v[90:91], v[2:3], v[24:25]
	s_waitcnt vmcnt(1)
	v_pk_fma_f32 v[30:31], v[88:89], v[16:17], v[30:31]
	v_pk_fma_f32 v[28:29], v[86:87], v[14:15], v[28:29]
	s_waitcnt vmcnt(0)
	v_pk_fma_f32 v[84:85], v[84:85], v[12:13], v[100:101]
	v_pk_fma_f32 v[82:83], v[82:83], v[10:11], v[98:99]
	global_store_dwordx4 v[118:119], v[20:23], off
	global_store_dwordx4 v[32:33], v[24:27], off offset:64
	global_store_dwordx4 v[32:33], v[28:31], off offset:512
	global_store_dwordx4 v[32:33], v[82:85], off offset:576
	global_load_dwordx4 v[20:23], v[102:103], off
	v_lshl_add_u64 v[32:33], v[18:19], 0, s[16:17]
	global_load_dwordx4 v[24:27], v[32:33], off offset:64
	global_load_dwordx4 v[28:31], v[32:33], off offset:512
	global_load_dwordx4 v[82:85], v[32:33], off offset:576
	v_add_co_u32_e32 v86, vcc, s45, v18
	s_mov_b32 s16, 0x160000
	s_nop 0
	v_addc_co_u32_e32 v87, vcc, 0, v19, vcc
	s_waitcnt vmcnt(2)
	v_pk_fma_f32 v[26:27], v[76:77], v[4:5], v[26:27]
	v_pk_fma_f32 v[22:23], v[80:81], v[8:9], v[22:23]
	v_pk_fma_f32 v[20:21], v[78:79], v[6:7], v[20:21]
	v_pk_fma_f32 v[24:25], v[74:75], v[2:3], v[24:25]
	s_waitcnt vmcnt(1)
	v_pk_fma_f32 v[30:31], v[72:73], v[16:17], v[30:31]
	v_pk_fma_f32 v[28:29], v[70:71], v[14:15], v[28:29]
	s_waitcnt vmcnt(0)
	v_pk_fma_f32 v[68:69], v[68:69], v[12:13], v[84:85]
	v_pk_fma_f32 v[66:67], v[66:67], v[10:11], v[82:83]
	global_store_dwordx4 v[102:103], v[20:23], off
	global_store_dwordx4 v[32:33], v[24:27], off offset:64
	global_store_dwordx4 v[32:33], v[28:31], off offset:512
	global_store_dwordx4 v[32:33], v[66:69], off offset:576
	global_load_dwordx4 v[20:23], v[86:87], off
	v_lshl_add_u64 v[32:33], v[18:19], 0, s[12:13]
	global_load_dwordx4 v[24:27], v[32:33], off offset:64
	global_load_dwordx4 v[28:31], v[32:33], off offset:512
	global_load_dwordx4 v[66:69], v[32:33], off offset:576
	v_add_co_u32_e32 v70, vcc, s16, v18
	s_mov_b64 s[16:17], s[2:3]
	s_nop 0
	v_addc_co_u32_e32 v71, vcc, 0, v19, vcc
	v_lshl_add_u64 v[18:19], v[18:19], 0, s[14:15]
	s_and_b64 vcc, exec, s[0:1]
	s_waitcnt vmcnt(2)
	v_pk_fma_f32 v[26:27], v[60:61], v[4:5], v[26:27]
	v_pk_fma_f32 v[22:23], v[64:65], v[8:9], v[22:23]
	v_pk_fma_f32 v[20:21], v[62:63], v[6:7], v[20:21]
	v_pk_fma_f32 v[24:25], v[58:59], v[2:3], v[24:25]
	s_waitcnt vmcnt(1)
	v_pk_fma_f32 v[30:31], v[56:57], v[16:17], v[30:31]
	v_pk_fma_f32 v[28:29], v[54:55], v[14:15], v[28:29]
	s_waitcnt vmcnt(0)
	v_pk_fma_f32 v[52:53], v[52:53], v[12:13], v[68:69]
	v_pk_fma_f32 v[50:51], v[50:51], v[10:11], v[66:67]
	global_store_dwordx4 v[86:87], v[20:23], off
	global_store_dwordx4 v[32:33], v[24:27], off offset:64
	global_store_dwordx4 v[32:33], v[28:31], off offset:512
	global_store_dwordx4 v[32:33], v[50:53], off offset:576
	global_load_dwordx4 v[20:23], v[70:71], off
	global_load_dwordx4 v[24:27], v[18:19], off offset:64
	global_load_dwordx4 v[28:31], v[18:19], off offset:512
	global_load_dwordx4 v[50:53], v[18:19], off offset:576
	s_waitcnt vmcnt(2)
	v_pk_fma_f32 v[4:5], v[44:45], v[4:5], v[26:27]
	v_pk_fma_f32 v[8:9], v[48:49], v[8:9], v[22:23]
	v_pk_fma_f32 v[6:7], v[46:47], v[6:7], v[20:21]
	v_pk_fma_f32 v[2:3], v[42:43], v[2:3], v[24:25]
	s_waitcnt vmcnt(1)
	v_pk_fma_f32 v[16:17], v[40:41], v[16:17], v[30:31]
	v_pk_fma_f32 v[14:15], v[38:39], v[14:15], v[28:29]
	s_waitcnt vmcnt(0)
	v_pk_fma_f32 v[12:13], v[36:37], v[12:13], v[52:53]
	v_pk_fma_f32 v[10:11], v[34:35], v[10:11], v[50:51]
	global_store_dwordx4 v[70:71], v[6:9], off
	global_store_dwordx4 v[18:19], v[2:5], off offset:64
	global_store_dwordx4 v[18:19], v[14:17], off offset:512
	global_store_dwordx4 v[18:19], v[10:13], off offset:576
	s_cbranch_vccz .LBB0_865
	s_waitcnt vmcnt(0)
	s_mov_b64 s[60:61], s[64:65]
	s_mov_b64 s[62:63], s[66:67]
	s_cmpk_gt_u32 s24, 0xff
	s_cbranch_scc1 .LBB0_880
	s_barrier

.LBB0_1201:
	s_ashr_i32 s19, s18, 31
	s_lshl_b64 s[22:23], s[18:19], 19
	s_add_u32 s22, s72, s22
	s_addc_u32 s23, s73, s23
	s_and_b64 s[24:25], s[0:1], exec
	s_cselect_b32 s19, s23, s27
	s_cselect_b32 s46, s22, s26
	s_ashr_i32 s15, s14, 31
	s_lshl_b64 s[24:25], s[14:15], 19
	s_add_u32 s24, s33, s24
	s_addc_u32 s25, s34, s25
	s_and_b64 s[30:31], s[0:1], exec
	s_cselect_b32 s15, s25, s29
	s_cselect_b32 s47, s24, s28
	s_add_u32 s26, s26, 0x40080
	s_addc_u32 s27, s27, 0
	s_add_u32 s48, s28, 0x100
	v_mov_b32_e32 v34, 0
	s_addc_u32 s49, s29, 0
	s_mov_b32 s50, -2
	ds_read_b128 v[18:21], v194
	ds_read_b128 v[22:25], v194 offset:1024
	ds_read_b128 v[26:29], v194 offset:2048
	ds_read_b128 v[30:33], v194 offset:3072
	ds_read_b128 v[2:5], v196
	ds_read_b128 v[6:9], v196 offset:1024
	ds_read_b128 v[10:13], v196 offset:2048
	ds_read_b128 v[14:17], v196 offset:3072
	s_add_u32 s28, s26, 0xfffc0080
	s_addc_u32 s29, s27, -1
	s_cmp_eq_u32 s50, 12
	s_cselect_b32 s31, s19, s29
	s_cselect_b32 s30, s46, s28
	s_cselect_b32 s29, s15, s49
	s_cselect_b32 s28, s47, s48
	v_lshl_add_u64 v[226:227], s[26:27], 0, v[170:171]
	s_add_i32 m0, s13, 0xc000
	ds_read_b128 v[186:189], v199
	ds_read_b128 v[190:193], v199 offset:1024
	ds_read_b128 v[202:205], v199 offset:2048
	ds_read_b128 v[206:209], v199 offset:3072
	ds_read_b128 v[210:213], v199 offset:4096
	ds_read_b128 v[214:217], v199 offset:5120
	ds_read_b128 v[218:221], v199 offset:6144
	ds_read_b128 v[222:225], v199 offset:7168
	global_load_lds_dwordx4 v[226:227], off
	v_lshl_add_u64 v[226:227], s[26:27], 0, v[172:173]
	s_add_i32 m0, s13, 0xe000
	s_nop 0
	global_load_lds_dwordx4 v[226:227], off
	s_waitcnt vmcnt(8)
	s_waitcnt lgkmcnt(0)
	s_barrier
	s_setprio 1
	s_waitcnt lgkmcnt(0)
	v_mfma_scale_f32_16x16x128_f8f6f4 v[158:161], v[18:25], v[186:193], 0, v200, v201 op_sel_hi:[0,0,0]
	v_mfma_scale_f32_16x16x128_f8f6f4 v[154:157], v[26:33], v[186:193], 0, v200, v201 op_sel_hi:[0,0,0]
	v_mfma_scale_f32_16x16x128_f8f6f4 v[150:153], v[18:25], v[202:209], 0, v200, v201 op_sel_hi:[0,0,0]
	v_mfma_scale_f32_16x16x128_f8f6f4 v[142:145], v[26:33], v[202:209], 0, v200, v201 op_sel_hi:[0,0,0]
	v_mfma_scale_f32_16x16x128_f8f6f4 v[134:137], v[18:25], v[210:217], 0, v200, v201 op_sel_hi:[0,0,0]
	v_mfma_scale_f32_16x16x128_f8f6f4 v[126:129], v[26:33], v[210:217], 0, v200, v201 op_sel_hi:[0,0,0]
	v_mfma_scale_f32_16x16x128_f8f6f4 v[118:121], v[18:25], v[218:225], 0, v200, v201 op_sel_hi:[0,0,0]
	v_mfma_scale_f32_16x16x128_f8f6f4 v[110:113], v[26:33], v[218:225], 0, v200, v201 op_sel_hi:[0,0,0]
	s_setprio 0
	s_setprio 1
	v_mfma_scale_f32_16x16x128_f8f6f4 v[146:149], v[2:9], v[186:193], 0, v200, v201 op_sel_hi:[0,0,0]
	v_mfma_scale_f32_16x16x128_f8f6f4 v[138:141], v[10:17], v[186:193], 0, v200, v201 op_sel_hi:[0,0,0]
	v_mfma_scale_f32_16x16x128_f8f6f4 v[130:133], v[2:9], v[202:209], 0, v200, v201 op_sel_hi:[0,0,0]
	v_mfma_scale_f32_16x16x128_f8f6f4 v[122:125], v[10:17], v[202:209], 0, v200, v201 op_sel_hi:[0,0,0]
	v_mfma_scale_f32_16x16x128_f8f6f4 v[114:117], v[2:9], v[210:217], 0, v200, v201 op_sel_hi:[0,0,0]
	v_mfma_scale_f32_16x16x128_f8f6f4 v[106:109], v[10:17], v[210:217], 0, v200, v201 op_sel_hi:[0,0,0]
	v_mfma_scale_f32_16x16x128_f8f6f4 v[102:105], v[2:9], v[218:225], 0, v200, v201 op_sel_hi:[0,0,0]
	v_mfma_scale_f32_16x16x128_f8f6f4 v[98:101], v[10:17], v[218:225], 0, v200, v201 op_sel_hi:[0,0,0]
	s_setprio 0
	s_barrier
	s_add_i32 s51, s44, s35
	v_lshl_add_u64 v[186:187], s[28:29], 0, v[164:165]
	s_mov_b32 m0, s51
	ds_read_b128 v[202:205], v199 offset:16384
	ds_read_b128 v[206:209], v199 offset:17408
	ds_read_b128 v[210:213], v199 offset:18432
	ds_read_b128 v[214:217], v199 offset:19456
	ds_read_b128 v[218:221], v199 offset:20480
	ds_read_b128 v[222:225], v199 offset:21504
	ds_read_b128 v[226:229], v199 offset:22528
	ds_read_b128 v[230:233], v199 offset:23552
	global_load_lds_dwordx4 v[186:187], off
	s_add_i32 m0, s51, 0x2000
	s_add_u32 s52, s28, 0x40000
	v_lshl_add_u64 v[188:189], s[28:29], 0, v[168:169]
	s_addc_u32 s53, s29, 0
	s_add_i32 s51, s45, s35
	global_load_lds_dwordx4 v[188:189], off
	v_lshl_add_u64 v[190:191], s[52:53], 0, v[164:165]
	s_mov_b32 m0, s51
	v_lshl_add_u64 v[192:193], s[30:31], 0, v[166:167]
	global_load_lds_dwordx4 v[190:191], off
	v_lshl_add_u64 v[190:191], s[52:53], 0, v[168:169]
	s_add_i32 m0, s51, 0x2000
	s_nop 0
	global_load_lds_dwordx4 v[190:191], off
	v_lshl_add_u64 v[190:191], s[30:31], 0, v[162:163]
	s_mov_b32 m0, s13
	s_nop 0
	global_load_lds_dwordx4 v[190:191], off
	s_mov_b32 m0, s17
	s_nop 0
	global_load_lds_dwordx4 v[192:193], off
	s_waitcnt vmcnt(8)
	s_waitcnt lgkmcnt(0)
	s_barrier
	s_setprio 1
	s_waitcnt lgkmcnt(0)
	v_mfma_scale_f32_16x16x128_f8f6f4 v[94:97], v[18:25], v[202:209], 0, v200, v201 op_sel_hi:[0,0,0]
	v_mfma_scale_f32_16x16x128_f8f6f4 v[90:93], v[26:33], v[202:209], 0, v200, v201 op_sel_hi:[0,0,0]
	v_mfma_scale_f32_16x16x128_f8f6f4 v[86:89], v[18:25], v[210:217], 0, v200, v201 op_sel_hi:[0,0,0]
	v_mfma_scale_f32_16x16x128_f8f6f4 v[78:81], v[26:33], v[210:217], 0, v200, v201 op_sel_hi:[0,0,0]
	v_mfma_scale_f32_16x16x128_f8f6f4 v[70:73], v[18:25], v[218:225], 0, v200, v201 op_sel_hi:[0,0,0]
	v_mfma_scale_f32_16x16x128_f8f6f4 v[62:65], v[26:33], v[218:225], 0, v200, v201 op_sel_hi:[0,0,0]
	v_mfma_scale_f32_16x16x128_f8f6f4 v[54:57], v[18:25], v[226:233], 0, v200, v201 op_sel_hi:[0,0,0]
	v_mfma_scale_f32_16x16x128_f8f6f4 v[46:49], v[26:33], v[226:233], 0, v200, v201 op_sel_hi:[0,0,0]
	s_setprio 0
	s_setprio 1
	v_mfma_scale_f32_16x16x128_f8f6f4 v[82:85], v[2:9], v[202:209], 0, v200, v201 op_sel_hi:[0,0,0]
	v_mfma_scale_f32_16x16x128_f8f6f4 v[74:77], v[10:17], v[202:209], 0, v200, v201 op_sel_hi:[0,0,0]
	v_mfma_scale_f32_16x16x128_f8f6f4 v[66:69], v[2:9], v[210:217], 0, v200, v201 op_sel_hi:[0,0,0]
	v_mfma_scale_f32_16x16x128_f8f6f4 v[58:61], v[10:17], v[210:217], 0, v200, v201 op_sel_hi:[0,0,0]
	v_mfma_scale_f32_16x16x128_f8f6f4 v[50:53], v[2:9], v[218:225], 0, v200, v201 op_sel_hi:[0,0,0]
	v_mfma_scale_f32_16x16x128_f8f6f4 v[42:45], v[10:17], v[218:225], 0, v200, v201 op_sel_hi:[0,0,0]
	v_mfma_scale_f32_16x16x128_f8f6f4 v[38:41], v[2:9], v[226:233], 0, v200, v201 op_sel_hi:[0,0,0]
	v_mfma_scale_f32_16x16x128_f8f6f4 v[34:37], v[10:17], v[226:233], 0, v200, v201 op_sel_hi:[0,0,0]
	s_setprio 0
	s_barrier
	s_add_i32 s51, 0, 0x18000
	s_add_i32 s52, 0, 0x1c000
	v_add_u32_e32 v14, s51, v181
	v_add_u32_e32 v30, s52, v181
	ds_read_b128 v[2:5], v14
	ds_read_b128 v[6:9], v14 offset:1024
	ds_read_b128 v[10:13], v14 offset:2048
	ds_read_b128 v[14:17], v14 offset:3072
	ds_read_b128 v[18:21], v30
	ds_read_b128 v[22:25], v30 offset:1024
	ds_read_b128 v[26:29], v30 offset:2048
	ds_read_b128 v[30:33], v30 offset:3072
	s_add_u32 s30, s30, 0x40000
	s_addc_u32 s31, s31, 0
	s_mov_b32 m0, s36
	v_lshl_add_u64 v[234:235], s[30:31], 0, v[162:163]
	ds_read_b128 v[202:205], v199 offset:32768
	ds_read_b128 v[206:209], v199 offset:33792
	ds_read_b128 v[210:213], v199 offset:34816
	ds_read_b128 v[214:217], v199 offset:35840
	ds_read_b128 v[218:221], v199 offset:36864
	ds_read_b128 v[222:225], v199 offset:37888
	ds_read_b128 v[226:229], v199 offset:38912
	ds_read_b128 v[230:233], v199 offset:39936
	global_load_lds_dwordx4 v[234:235], off
	v_lshl_add_u64 v[234:235], s[30:31], 0, v[166:167]
	s_mov_b32 m0, s37
	s_nop 0
	global_load_lds_dwordx4 v[234:235], off
	s_waitcnt vmcnt(8)
	s_waitcnt lgkmcnt(0)
	s_barrier
	s_setprio 1
	s_waitcnt lgkmcnt(0)
	v_mfma_scale_f32_16x16x128_f8f6f4 v[158:161], v[2:9], v[202:209], v[158:161], v200, v201 op_sel_hi:[0,0,0]
	v_mfma_scale_f32_16x16x128_f8f6f4 v[154:157], v[10:17], v[202:209], v[154:157], v200, v201 op_sel_hi:[0,0,0]
	v_mfma_scale_f32_16x16x128_f8f6f4 v[150:153], v[2:9], v[210:217], v[150:153], v200, v201 op_sel_hi:[0,0,0]
	v_mfma_scale_f32_16x16x128_f8f6f4 v[142:145], v[10:17], v[210:217], v[142:145], v200, v201 op_sel_hi:[0,0,0]
	v_mfma_scale_f32_16x16x128_f8f6f4 v[134:137], v[2:9], v[218:225], v[134:137], v200, v201 op_sel_hi:[0,0,0]
	v_mfma_scale_f32_16x16x128_f8f6f4 v[126:129], v[10:17], v[218:225], v[126:129], v200, v201 op_sel_hi:[0,0,0]
	v_mfma_scale_f32_16x16x128_f8f6f4 v[118:121], v[2:9], v[226:233], v[118:121], v200, v201 op_sel_hi:[0,0,0]
	v_mfma_scale_f32_16x16x128_f8f6f4 v[110:113], v[10:17], v[226:233], v[110:113], v200, v201 op_sel_hi:[0,0,0]
	s_setprio 0
	s_setprio 1
	v_mfma_scale_f32_16x16x128_f8f6f4 v[146:149], v[18:25], v[202:209], v[146:149], v200, v201 op_sel_hi:[0,0,0]
	v_mfma_scale_f32_16x16x128_f8f6f4 v[138:141], v[26:33], v[202:209], v[138:141], v200, v201 op_sel_hi:[0,0,0]
	v_mfma_scale_f32_16x16x128_f8f6f4 v[130:133], v[18:25], v[210:217], v[130:133], v200, v201 op_sel_hi:[0,0,0]
	v_mfma_scale_f32_16x16x128_f8f6f4 v[122:125], v[26:33], v[210:217], v[122:125], v200, v201 op_sel_hi:[0,0,0]
	v_mfma_scale_f32_16x16x128_f8f6f4 v[114:117], v[18:25], v[218:225], v[114:117], v200, v201 op_sel_hi:[0,0,0]
	v_mfma_scale_f32_16x16x128_f8f6f4 v[106:109], v[26:33], v[218:225], v[106:109], v200, v201 op_sel_hi:[0,0,0]
	v_mfma_scale_f32_16x16x128_f8f6f4 v[102:105], v[18:25], v[226:233], v[102:105], v200, v201 op_sel_hi:[0,0,0]
	v_mfma_scale_f32_16x16x128_f8f6f4 v[98:101], v[26:33], v[226:233], v[98:101], v200, v201 op_sel_hi:[0,0,0]
	s_setprio 0
	s_barrier
	s_add_i32 s30, s51, s35
	v_lshl_add_u64 v[186:187], v[186:187], 0, s[8:9]
	s_mov_b32 m0, s30
	ds_read_b128 v[202:205], v199 offset:49152
	ds_read_b128 v[206:209], v199 offset:50176
	ds_read_b128 v[210:213], v199 offset:51200
	ds_read_b128 v[214:217], v199 offset:52224
	ds_read_b128 v[218:221], v199 offset:53248
	ds_read_b128 v[222:225], v199 offset:54272
	ds_read_b128 v[226:229], v199 offset:55296
	ds_read_b128 v[230:233], v199 offset:56320
	global_load_lds_dwordx4 v[186:187], off
	s_add_i32 m0, s30, 0x2000
	s_add_u32 s28, s28, 0x40080
	v_lshl_add_u64 v[186:187], v[188:189], 0, s[8:9]
	s_addc_u32 s29, s29, 0
	s_add_i32 s30, s52, s35
	global_load_lds_dwordx4 v[186:187], off
	v_lshl_add_u64 v[186:187], s[28:29], 0, v[164:165]
	s_mov_b32 m0, s30
	s_nop 0
	global_load_lds_dwordx4 v[186:187], off
	v_lshl_add_u64 v[186:187], s[28:29], 0, v[168:169]
	s_add_i32 m0, s30, 0x2000
	s_nop 0
	global_load_lds_dwordx4 v[186:187], off
	v_lshl_add_u64 v[186:187], v[190:191], 0, s[8:9]
	s_mov_b32 m0, s39
	s_nop 0
	global_load_lds_dwordx4 v[186:187], off
	v_lshl_add_u64 v[186:187], v[192:193], 0, s[8:9]
	s_mov_b32 m0, s40
	s_nop 0
	global_load_lds_dwordx4 v[186:187], off
	s_waitcnt vmcnt(8)
	s_waitcnt lgkmcnt(0)
	s_barrier
	s_setprio 1
	s_waitcnt lgkmcnt(0)
	v_mfma_scale_f32_16x16x128_f8f6f4 v[94:97], v[2:9], v[202:209], v[94:97], v200, v201 op_sel_hi:[0,0,0]
	v_mfma_scale_f32_16x16x128_f8f6f4 v[90:93], v[10:17], v[202:209], v[90:93], v200, v201 op_sel_hi:[0,0,0]
	v_mfma_scale_f32_16x16x128_f8f6f4 v[86:89], v[2:9], v[210:217], v[86:89], v200, v201 op_sel_hi:[0,0,0]
	v_mfma_scale_f32_16x16x128_f8f6f4 v[78:81], v[10:17], v[210:217], v[78:81], v200, v201 op_sel_hi:[0,0,0]
	v_mfma_scale_f32_16x16x128_f8f6f4 v[70:73], v[2:9], v[218:225], v[70:73], v200, v201 op_sel_hi:[0,0,0]
	v_mfma_scale_f32_16x16x128_f8f6f4 v[62:65], v[10:17], v[218:225], v[62:65], v200, v201 op_sel_hi:[0,0,0]
	v_mfma_scale_f32_16x16x128_f8f6f4 v[54:57], v[2:9], v[226:233], v[54:57], v200, v201 op_sel_hi:[0,0,0]
	v_mfma_scale_f32_16x16x128_f8f6f4 v[46:49], v[10:17], v[226:233], v[46:49], v200, v201 op_sel_hi:[0,0,0]
	s_setprio 0
	s_setprio 1
	v_mfma_scale_f32_16x16x128_f8f6f4 v[82:85], v[18:25], v[202:209], v[82:85], v200, v201 op_sel_hi:[0,0,0]
	v_mfma_scale_f32_16x16x128_f8f6f4 v[74:77], v[26:33], v[202:209], v[74:77], v200, v201 op_sel_hi:[0,0,0]
	v_mfma_scale_f32_16x16x128_f8f6f4 v[66:69], v[18:25], v[210:217], v[66:69], v200, v201 op_sel_hi:[0,0,0]
	v_mfma_scale_f32_16x16x128_f8f6f4 v[58:61], v[26:33], v[210:217], v[58:61], v200, v201 op_sel_hi:[0,0,0]
	v_mfma_scale_f32_16x16x128_f8f6f4 v[50:53], v[18:25], v[218:225], v[50:53], v200, v201 op_sel_hi:[0,0,0]
	v_mfma_scale_f32_16x16x128_f8f6f4 v[42:45], v[26:33], v[218:225], v[42:45], v200, v201 op_sel_hi:[0,0,0]
	v_mfma_scale_f32_16x16x128_f8f6f4 v[38:41], v[18:25], v[226:233], v[38:41], v200, v201 op_sel_hi:[0,0,0]
	v_mfma_scale_f32_16x16x128_f8f6f4 v[34:37], v[26:33], v[226:233], v[34:37], v200, v201 op_sel_hi:[0,0,0]
	s_setprio 0
	s_barrier
	s_add_i32 s50, s50, 2
	s_add_u32 s26, s26, 0x100
	s_addc_u32 s27, s27, 0
	s_add_u32 s48, s48, 0x100
	s_addc_u32 s49, s49, 0
	s_cmp_gt_u32 s50, 13
	s_cbranch_scc1 .Lpeel_exit_1202

.Lpeel_exit_1202:
	s_and_b64 vcc, exec, s[10:11]
	s_cbranch_vccz .LBB0_1205
	s_barrier

.LBB0_1533:
	s_ashr_i32 s19, s18, 31
	v_cmp_lt_i64_e32 vcc, s[22:23], v[170:171]
	s_lshl_b64 s[22:23], s[18:19], 18
	s_add_u32 s22, s37, s22
	s_addc_u32 s23, s38, s23
	s_and_b64 s[24:25], vcc, exec
	s_cselect_b32 s19, s23, s29
	s_cselect_b32 s58, s22, s28
	s_ashr_i32 s17, s16, 31
	s_lshl_b64 s[24:25], s[16:17], 18
	s_add_u32 s24, s39, s24
	s_addc_u32 s25, s40, s25
	s_and_b64 s[34:35], vcc, exec
	s_cselect_b32 s17, s25, s31
	s_cselect_b32 s59, s24, s30
	s_add_u32 s28, s28, 0x20080
	s_addc_u32 s29, s29, 0
	s_add_u32 s60, s30, 0x100
	v_mov_b32_e32 v34, 0
	s_addc_u32 s61, s31, 0
	s_mov_b32 s62, -2
	ds_read_b128 v[18:21], v188
	ds_read_b128 v[22:25], v188 offset:1024
	ds_read_b128 v[26:29], v188 offset:2048
	ds_read_b128 v[30:33], v188 offset:3072
	ds_read_b128 v[2:5], v189
	ds_read_b128 v[6:9], v189 offset:1024
	ds_read_b128 v[10:13], v189 offset:2048
	ds_read_b128 v[14:17], v189 offset:3072
	s_add_u32 s30, s28, 0xfffe0080
	s_addc_u32 s31, s29, -1
	s_cmp_eq_u32 s62, 4
	s_cselect_b32 s35, s19, s31
	s_cselect_b32 s34, s58, s30
	s_cselect_b32 s31, s17, s61
	s_cselect_b32 s30, s59, s60
	v_lshl_add_u64 v[174:175], s[28:29], 0, v[166:167]
	s_add_i32 m0, s27, 0xc000
	ds_read_b128 v[200:203], v190
	ds_read_b128 v[204:207], v190 offset:1024
	ds_read_b128 v[208:211], v190 offset:2048
	ds_read_b128 v[212:215], v190 offset:3072
	ds_read_b128 v[216:219], v190 offset:4096
	ds_read_b128 v[220:223], v190 offset:5120
	ds_read_b128 v[224:227], v190 offset:6144
	ds_read_b128 v[228:231], v190 offset:7168
	global_load_lds_dwordx4 v[174:175], off
	v_lshl_add_u64 v[174:175], s[28:29], 0, v[168:169]
	s_add_i32 m0, s27, 0xe000
	s_nop 0
	global_load_lds_dwordx4 v[174:175], off
	s_waitcnt vmcnt(8)
	s_waitcnt lgkmcnt(0)
	s_barrier
	s_setprio 1
	s_waitcnt lgkmcnt(0)
	v_mfma_scale_f32_16x16x128_f8f6f4 v[158:161], v[18:25], v[200:207], 0, v191, v192 op_sel_hi:[0,0,0]
	v_mfma_scale_f32_16x16x128_f8f6f4 v[154:157], v[26:33], v[200:207], 0, v191, v192 op_sel_hi:[0,0,0]
	v_mfma_scale_f32_16x16x128_f8f6f4 v[142:145], v[18:25], v[208:215], 0, v191, v192 op_sel_hi:[0,0,0]
	v_mfma_scale_f32_16x16x128_f8f6f4 v[138:141], v[26:33], v[208:215], 0, v191, v192 op_sel_hi:[0,0,0]
	v_mfma_scale_f32_16x16x128_f8f6f4 v[126:129], v[18:25], v[216:223], 0, v191, v192 op_sel_hi:[0,0,0]
	v_mfma_scale_f32_16x16x128_f8f6f4 v[122:125], v[26:33], v[216:223], 0, v191, v192 op_sel_hi:[0,0,0]
	v_mfma_scale_f32_16x16x128_f8f6f4 v[110:113], v[18:25], v[224:231], 0, v191, v192 op_sel_hi:[0,0,0]
	v_mfma_scale_f32_16x16x128_f8f6f4 v[106:109], v[26:33], v[224:231], 0, v191, v192 op_sel_hi:[0,0,0]
	s_setprio 0
	s_setprio 1
	v_mfma_scale_f32_16x16x128_f8f6f4 v[150:153], v[2:9], v[200:207], 0, v191, v192 op_sel_hi:[0,0,0]
	v_mfma_scale_f32_16x16x128_f8f6f4 v[146:149], v[10:17], v[200:207], 0, v191, v192 op_sel_hi:[0,0,0]
	v_mfma_scale_f32_16x16x128_f8f6f4 v[134:137], v[2:9], v[208:215], 0, v191, v192 op_sel_hi:[0,0,0]
	v_mfma_scale_f32_16x16x128_f8f6f4 v[130:133], v[10:17], v[208:215], 0, v191, v192 op_sel_hi:[0,0,0]
	v_mfma_scale_f32_16x16x128_f8f6f4 v[118:121], v[2:9], v[216:223], 0, v191, v192 op_sel_hi:[0,0,0]
	v_mfma_scale_f32_16x16x128_f8f6f4 v[114:117], v[10:17], v[216:223], 0, v191, v192 op_sel_hi:[0,0,0]
	v_mfma_scale_f32_16x16x128_f8f6f4 v[102:105], v[2:9], v[224:231], 0, v191, v192 op_sel_hi:[0,0,0]
	v_mfma_scale_f32_16x16x128_f8f6f4 v[98:101], v[10:17], v[224:231], 0, v191, v192 op_sel_hi:[0,0,0]
	s_setprio 0
	s_barrier
	s_add_i32 s63, s51, s41
	v_lshl_add_u64 v[174:175], s[30:31], 0, v[162:163]
	s_mov_b32 m0, s63
	ds_read_b128 v[200:203], v190 offset:16384
	ds_read_b128 v[204:207], v190 offset:17408
	ds_read_b128 v[208:211], v190 offset:18432
	ds_read_b128 v[212:215], v190 offset:19456
	ds_read_b128 v[216:219], v190 offset:20480
	ds_read_b128 v[220:223], v190 offset:21504
	ds_read_b128 v[224:227], v190 offset:22528
	ds_read_b128 v[228:231], v190 offset:23552
	global_load_lds_dwordx4 v[174:175], off
	s_add_i32 m0, s63, 0x2000
	s_add_u32 s64, s30, 0x20000
	v_lshl_add_u64 v[176:177], s[30:31], 0, v[164:165]
	s_addc_u32 s65, s31, 0
	s_add_i32 s63, s52, s41
	global_load_lds_dwordx4 v[176:177], off
	v_lshl_add_u64 v[184:185], s[64:65], 0, v[162:163]
	s_mov_b32 m0, s63
	v_lshl_add_u64 v[186:187], s[34:35], 0, v[164:165]
	global_load_lds_dwordx4 v[184:185], off
	v_lshl_add_u64 v[184:185], s[64:65], 0, v[164:165]
	s_add_i32 m0, s63, 0x2000
	s_nop 0
	global_load_lds_dwordx4 v[184:185], off
	v_lshl_add_u64 v[184:185], s[34:35], 0, v[162:163]
	s_mov_b32 m0, s27
	s_nop 0
	global_load_lds_dwordx4 v[184:185], off
	s_mov_b32 m0, s42
	s_nop 0
	global_load_lds_dwordx4 v[186:187], off
	s_waitcnt vmcnt(8)
	s_waitcnt lgkmcnt(0)
	s_barrier
	s_setprio 1
	s_waitcnt lgkmcnt(0)
	v_mfma_scale_f32_16x16x128_f8f6f4 v[94:97], v[18:25], v[200:207], 0, v191, v192 op_sel_hi:[0,0,0]
	v_mfma_scale_f32_16x16x128_f8f6f4 v[90:93], v[26:33], v[200:207], 0, v191, v192 op_sel_hi:[0,0,0]
	v_mfma_scale_f32_16x16x128_f8f6f4 v[78:81], v[18:25], v[208:215], 0, v191, v192 op_sel_hi:[0,0,0]
	v_mfma_scale_f32_16x16x128_f8f6f4 v[74:77], v[26:33], v[208:215], 0, v191, v192 op_sel_hi:[0,0,0]
	v_mfma_scale_f32_16x16x128_f8f6f4 v[62:65], v[18:25], v[216:223], 0, v191, v192 op_sel_hi:[0,0,0]
	v_mfma_scale_f32_16x16x128_f8f6f4 v[58:61], v[26:33], v[216:223], 0, v191, v192 op_sel_hi:[0,0,0]
	v_mfma_scale_f32_16x16x128_f8f6f4 v[46:49], v[18:25], v[224:231], 0, v191, v192 op_sel_hi:[0,0,0]
	v_mfma_scale_f32_16x16x128_f8f6f4 v[42:45], v[26:33], v[224:231], 0, v191, v192 op_sel_hi:[0,0,0]
	s_setprio 0
	s_setprio 1
	v_mfma_scale_f32_16x16x128_f8f6f4 v[86:89], v[2:9], v[200:207], 0, v191, v192 op_sel_hi:[0,0,0]
	v_mfma_scale_f32_16x16x128_f8f6f4 v[82:85], v[10:17], v[200:207], 0, v191, v192 op_sel_hi:[0,0,0]
	v_mfma_scale_f32_16x16x128_f8f6f4 v[70:73], v[2:9], v[208:215], 0, v191, v192 op_sel_hi:[0,0,0]
	v_mfma_scale_f32_16x16x128_f8f6f4 v[66:69], v[10:17], v[208:215], 0, v191, v192 op_sel_hi:[0,0,0]
	v_mfma_scale_f32_16x16x128_f8f6f4 v[54:57], v[2:9], v[216:223], 0, v191, v192 op_sel_hi:[0,0,0]
	v_mfma_scale_f32_16x16x128_f8f6f4 v[50:53], v[10:17], v[216:223], 0, v191, v192 op_sel_hi:[0,0,0]
	v_mfma_scale_f32_16x16x128_f8f6f4 v[38:41], v[2:9], v[224:231], 0, v191, v192 op_sel_hi:[0,0,0]
	v_mfma_scale_f32_16x16x128_f8f6f4 v[34:37], v[10:17], v[224:231], 0, v191, v192 op_sel_hi:[0,0,0]
	s_setprio 0
	s_barrier
	s_add_i32 s63, 0, 0x18000
	s_add_i32 s64, 0, 0x1c000
	v_add_u32_e32 v14, s63, v181
	v_add_u32_e32 v30, s64, v181
	ds_read_b128 v[2:5], v14
	ds_read_b128 v[6:9], v14 offset:1024
	ds_read_b128 v[10:13], v14 offset:2048
	ds_read_b128 v[14:17], v14 offset:3072
	ds_read_b128 v[18:21], v30
	ds_read_b128 v[22:25], v30 offset:1024
	ds_read_b128 v[26:29], v30 offset:2048
	ds_read_b128 v[30:33], v30 offset:3072
	s_add_u32 s34, s34, 0x20000
	s_addc_u32 s35, s35, 0
	s_mov_b32 m0, s43
	v_lshl_add_u64 v[232:233], s[34:35], 0, v[162:163]
	ds_read_b128 v[200:203], v190 offset:32768
	ds_read_b128 v[204:207], v190 offset:33792
	ds_read_b128 v[208:211], v190 offset:34816
	ds_read_b128 v[212:215], v190 offset:35840
	ds_read_b128 v[216:219], v190 offset:36864
	ds_read_b128 v[220:223], v190 offset:37888
	ds_read_b128 v[224:227], v190 offset:38912
	ds_read_b128 v[228:231], v190 offset:39936
	global_load_lds_dwordx4 v[232:233], off
	v_lshl_add_u64 v[232:233], s[34:35], 0, v[164:165]
	s_mov_b32 m0, s44
	s_nop 0
	global_load_lds_dwordx4 v[232:233], off
	s_waitcnt vmcnt(8)
	s_waitcnt lgkmcnt(0)
	s_barrier
	s_setprio 1
	s_waitcnt lgkmcnt(0)
	v_mfma_scale_f32_16x16x128_f8f6f4 v[158:161], v[2:9], v[200:207], v[158:161], v191, v192 op_sel_hi:[0,0,0]
	v_mfma_scale_f32_16x16x128_f8f6f4 v[154:157], v[10:17], v[200:207], v[154:157], v191, v192 op_sel_hi:[0,0,0]
	v_mfma_scale_f32_16x16x128_f8f6f4 v[142:145], v[2:9], v[208:215], v[142:145], v191, v192 op_sel_hi:[0,0,0]
	v_mfma_scale_f32_16x16x128_f8f6f4 v[138:141], v[10:17], v[208:215], v[138:141], v191, v192 op_sel_hi:[0,0,0]
	v_mfma_scale_f32_16x16x128_f8f6f4 v[126:129], v[2:9], v[216:223], v[126:129], v191, v192 op_sel_hi:[0,0,0]
	v_mfma_scale_f32_16x16x128_f8f6f4 v[122:125], v[10:17], v[216:223], v[122:125], v191, v192 op_sel_hi:[0,0,0]
	v_mfma_scale_f32_16x16x128_f8f6f4 v[110:113], v[2:9], v[224:231], v[110:113], v191, v192 op_sel_hi:[0,0,0]
	v_mfma_scale_f32_16x16x128_f8f6f4 v[106:109], v[10:17], v[224:231], v[106:109], v191, v192 op_sel_hi:[0,0,0]
	s_setprio 0
	s_setprio 1
	v_mfma_scale_f32_16x16x128_f8f6f4 v[150:153], v[18:25], v[200:207], v[150:153], v191, v192 op_sel_hi:[0,0,0]
	v_mfma_scale_f32_16x16x128_f8f6f4 v[146:149], v[26:33], v[200:207], v[146:149], v191, v192 op_sel_hi:[0,0,0]
	v_mfma_scale_f32_16x16x128_f8f6f4 v[134:137], v[18:25], v[208:215], v[134:137], v191, v192 op_sel_hi:[0,0,0]
	v_mfma_scale_f32_16x16x128_f8f6f4 v[130:133], v[26:33], v[208:215], v[130:133], v191, v192 op_sel_hi:[0,0,0]
	v_mfma_scale_f32_16x16x128_f8f6f4 v[118:121], v[18:25], v[216:223], v[118:121], v191, v192 op_sel_hi:[0,0,0]
	v_mfma_scale_f32_16x16x128_f8f6f4 v[114:117], v[26:33], v[216:223], v[114:117], v191, v192 op_sel_hi:[0,0,0]
	v_mfma_scale_f32_16x16x128_f8f6f4 v[102:105], v[18:25], v[224:231], v[102:105], v191, v192 op_sel_hi:[0,0,0]
	v_mfma_scale_f32_16x16x128_f8f6f4 v[98:101], v[26:33], v[224:231], v[98:101], v191, v192 op_sel_hi:[0,0,0]
	s_setprio 0
	s_barrier
	s_add_i32 s34, s63, s41
	v_lshl_add_u64 v[174:175], v[174:175], 0, s[6:7]
	s_mov_b32 m0, s34
	ds_read_b128 v[200:203], v190 offset:49152
	ds_read_b128 v[204:207], v190 offset:50176
	ds_read_b128 v[208:211], v190 offset:51200
	ds_read_b128 v[212:215], v190 offset:52224
	ds_read_b128 v[216:219], v190 offset:53248
	ds_read_b128 v[220:223], v190 offset:54272
	ds_read_b128 v[224:227], v190 offset:55296
	ds_read_b128 v[228:231], v190 offset:56320
	global_load_lds_dwordx4 v[174:175], off
	s_add_i32 m0, s34, 0x2000
	s_add_u32 s30, s30, 0x20080
	v_lshl_add_u64 v[174:175], v[176:177], 0, s[6:7]
	s_addc_u32 s31, s31, 0
	s_add_i32 s34, s64, s41
	global_load_lds_dwordx4 v[174:175], off
	v_lshl_add_u64 v[174:175], s[30:31], 0, v[162:163]
	s_mov_b32 m0, s34
	s_nop 0
	global_load_lds_dwordx4 v[174:175], off
	v_lshl_add_u64 v[174:175], s[30:31], 0, v[164:165]
	s_add_i32 m0, s34, 0x2000
	s_nop 0
	global_load_lds_dwordx4 v[174:175], off
	v_lshl_add_u64 v[174:175], v[184:185], 0, s[6:7]
	s_mov_b32 m0, s48
	s_nop 0
	global_load_lds_dwordx4 v[174:175], off
	v_lshl_add_u64 v[174:175], v[186:187], 0, s[6:7]
	s_mov_b32 m0, s49
	s_nop 0
	global_load_lds_dwordx4 v[174:175], off
	s_waitcnt vmcnt(8)
	s_waitcnt lgkmcnt(0)
	s_barrier
	s_setprio 1
	s_waitcnt lgkmcnt(0)
	v_mfma_scale_f32_16x16x128_f8f6f4 v[94:97], v[2:9], v[200:207], v[94:97], v191, v192 op_sel_hi:[0,0,0]
	v_mfma_scale_f32_16x16x128_f8f6f4 v[90:93], v[10:17], v[200:207], v[90:93], v191, v192 op_sel_hi:[0,0,0]
	v_mfma_scale_f32_16x16x128_f8f6f4 v[78:81], v[2:9], v[208:215], v[78:81], v191, v192 op_sel_hi:[0,0,0]
	v_mfma_scale_f32_16x16x128_f8f6f4 v[74:77], v[10:17], v[208:215], v[74:77], v191, v192 op_sel_hi:[0,0,0]
	v_mfma_scale_f32_16x16x128_f8f6f4 v[62:65], v[2:9], v[216:223], v[62:65], v191, v192 op_sel_hi:[0,0,0]
	v_mfma_scale_f32_16x16x128_f8f6f4 v[58:61], v[10:17], v[216:223], v[58:61], v191, v192 op_sel_hi:[0,0,0]
	v_mfma_scale_f32_16x16x128_f8f6f4 v[46:49], v[2:9], v[224:231], v[46:49], v191, v192 op_sel_hi:[0,0,0]
	v_mfma_scale_f32_16x16x128_f8f6f4 v[42:45], v[10:17], v[224:231], v[42:45], v191, v192 op_sel_hi:[0,0,0]
	s_setprio 0
	s_setprio 1
	v_mfma_scale_f32_16x16x128_f8f6f4 v[86:89], v[18:25], v[200:207], v[86:89], v191, v192 op_sel_hi:[0,0,0]
	v_mfma_scale_f32_16x16x128_f8f6f4 v[82:85], v[26:33], v[200:207], v[82:85], v191, v192 op_sel_hi:[0,0,0]
	v_mfma_scale_f32_16x16x128_f8f6f4 v[70:73], v[18:25], v[208:215], v[70:73], v191, v192 op_sel_hi:[0,0,0]
	v_mfma_scale_f32_16x16x128_f8f6f4 v[66:69], v[26:33], v[208:215], v[66:69], v191, v192 op_sel_hi:[0,0,0]
	v_mfma_scale_f32_16x16x128_f8f6f4 v[54:57], v[18:25], v[216:223], v[54:57], v191, v192 op_sel_hi:[0,0,0]
	v_mfma_scale_f32_16x16x128_f8f6f4 v[50:53], v[26:33], v[216:223], v[50:53], v191, v192 op_sel_hi:[0,0,0]
	v_mfma_scale_f32_16x16x128_f8f6f4 v[38:41], v[18:25], v[224:231], v[38:41], v191, v192 op_sel_hi:[0,0,0]
	v_mfma_scale_f32_16x16x128_f8f6f4 v[34:37], v[26:33], v[224:231], v[34:37], v191, v192 op_sel_hi:[0,0,0]
	s_setprio 0
	s_barrier
	s_add_i32 s62, s62, 2
	s_add_u32 s28, s28, 0x100
	s_addc_u32 s29, s29, 0
	s_add_u32 s60, s60, 0x100
	s_addc_u32 s61, s61, 0
	s_cmp_gt_u32 s62, 5
	s_cbranch_scc1 .Lpeel_exit_1534

.Lpeel_exit_1534:
	v_lshl_or_b32 v2, s57, 8, v183
	s_ashr_i32 s17, s26, 3
	v_lshl_add_u32 v184, s26, 8, v1
	s_mul_hi_i32 s19, s17, 0x1c000
	s_mul_i32 s17, s17, 0x1c000
	v_ashrrev_i32_e32 v3, 31, v2
	v_ashrrev_i32_e32 v185, 31, v184
	s_add_u32 s28, s46, s17
	v_lshlrev_b64 v[32:33], 2, v[2:3]
	v_lshlrev_b64 v[2:3], 13, v[184:185]
	s_addc_u32 s29, s47, s19
	v_lshl_add_u64 v[2:3], s[76:77], 0, v[2:3]
	s_nop 15
	s_nop 15
	v_lshl_add_u64 v[10:11], s[28:29], 0, v[32:33]
	v_lshl_add_u64 v[18:19], v[2:3], 0, v[32:33]
	global_load_dwordx4 v[20:23], v[18:19], off
	global_load_dwordx4 v[6:9], v[10:11], off
	global_load_dwordx4 v[2:5], v[10:11], off offset:64
	global_load_dwordx4 v[24:27], v[18:19], off offset:64
	global_load_dwordx4 v[28:31], v[18:19], off offset:512
	global_load_dwordx4 v[14:17], v[10:11], off offset:512
	s_nop 0
	global_load_dwordx4 v[10:13], v[10:11], off offset:576
	s_nop 0
	global_load_dwordx4 v[174:177], v[18:19], off offset:576
	v_or_b32_e32 v186, 16, v184
	v_ashrrev_i32_e32 v187, 31, v186
	v_lshlrev_b64 v[186:187], 13, v[186:187]
	v_lshl_add_u64 v[186:187], s[76:77], 0, v[186:187]
	v_lshl_add_u64 v[186:187], v[186:187], 0, v[32:33]
	s_mov_b32 s57, s16
	s_mov_b32 s26, s18
	s_mov_b64 s[30:31], s[24:25]
	s_mov_b64 s[28:29], s[22:23]
	s_waitcnt vmcnt(0)
	v_pk_fma_f32 v[22:23], v[160:161], v[8:9], v[22:23]
	v_pk_fma_f32 v[20:21], v[158:159], v[6:7], v[20:21]
	v_pk_fma_f32 v[26:27], v[156:157], v[4:5], v[26:27]
	v_pk_fma_f32 v[24:25], v[154:155], v[2:3], v[24:25]
	v_pk_fma_f32 v[30:31], v[152:153], v[16:17], v[30:31]
	v_pk_fma_f32 v[28:29], v[150:151], v[14:15], v[28:29]
	v_pk_fma_f32 v[148:149], v[148:149], v[12:13], v[176:177]
	v_pk_fma_f32 v[146:147], v[146:147], v[10:11], v[174:175]
	global_store_dwordx4 v[18:19], v[20:23], off
	global_store_dwordx4 v[18:19], v[24:27], off offset:64
	global_store_dwordx4 v[18:19], v[28:31], off offset:512
	global_store_dwordx4 v[18:19], v[146:149], off offset:576
	global_load_dwordx4 v[20:23], v[186:187], off
	global_load_dwordx4 v[24:27], v[186:187], off offset:64
	global_load_dwordx4 v[28:31], v[186:187], off offset:512
	global_load_dwordx4 v[146:149], v[186:187], off offset:576
	v_or_b32_e32 v150, 32, v184
	v_ashrrev_i32_e32 v151, 31, v150
	v_lshlrev_b64 v[150:151], 13, v[150:151]
	v_lshl_add_u64 v[150:151], s[76:77], 0, v[150:151]
	v_lshl_add_u64 v[150:151], v[150:151], 0, v[32:33]
	s_waitcnt vmcnt(3)
	v_pk_fma_f32 v[22:23], v[144:145], v[8:9], v[22:23]
	v_pk_fma_f32 v[20:21], v[142:143], v[6:7], v[20:21]
	s_waitcnt vmcnt(2)
	v_pk_fma_f32 v[26:27], v[140:141], v[4:5], v[26:27]
	v_pk_fma_f32 v[24:25], v[138:139], v[2:3], v[24:25]
	s_waitcnt vmcnt(1)
	v_pk_fma_f32 v[30:31], v[136:137], v[16:17], v[30:31]
	v_pk_fma_f32 v[28:29], v[134:135], v[14:15], v[28:29]
	s_waitcnt vmcnt(0)
	v_pk_fma_f32 v[132:133], v[132:133], v[12:13], v[148:149]
	v_pk_fma_f32 v[130:131], v[130:131], v[10:11], v[146:147]
	global_store_dwordx4 v[186:187], v[20:23], off
	global_store_dwordx4 v[186:187], v[24:27], off offset:64
	global_store_dwordx4 v[186:187], v[28:31], off offset:512
	global_store_dwordx4 v[186:187], v[130:133], off offset:576
	global_load_dwordx4 v[20:23], v[150:151], off
	global_load_dwordx4 v[24:27], v[150:151], off offset:64
	global_load_dwordx4 v[28:31], v[150:151], off offset:512
	global_load_dwordx4 v[130:133], v[150:151], off offset:576
	v_or_b32_e32 v134, 48, v184
	v_ashrrev_i32_e32 v135, 31, v134
	v_lshlrev_b64 v[134:135], 13, v[134:135]
	v_lshl_add_u64 v[134:135], s[76:77], 0, v[134:135]
	v_lshl_add_u64 v[32:33], v[134:135], 0, v[32:33]
	s_waitcnt vmcnt(3)
	v_pk_fma_f32 v[22:23], v[128:129], v[8:9], v[22:23]
	v_pk_fma_f32 v[20:21], v[126:127], v[6:7], v[20:21]
	s_waitcnt vmcnt(2)
	v_pk_fma_f32 v[26:27], v[124:125], v[4:5], v[26:27]
	v_pk_fma_f32 v[24:25], v[122:123], v[2:3], v[24:25]
	s_waitcnt vmcnt(1)
	v_pk_fma_f32 v[30:31], v[120:121], v[16:17], v[30:31]
	v_pk_fma_f32 v[28:29], v[118:119], v[14:15], v[28:29]
	s_waitcnt vmcnt(0)
	v_pk_fma_f32 v[116:117], v[116:117], v[12:13], v[132:133]
	v_pk_fma_f32 v[114:115], v[114:115], v[10:11], v[130:131]
	global_store_dwordx4 v[150:151], v[20:23], off
	global_store_dwordx4 v[150:151], v[24:27], off offset:64
	global_store_dwordx4 v[150:151], v[28:31], off offset:512
	global_store_dwordx4 v[150:151], v[114:117], off offset:576
	global_load_dwordx4 v[20:23], v[32:33], off
	global_load_dwordx4 v[24:27], v[32:33], off offset:64
	global_load_dwordx4 v[28:31], v[32:33], off offset:512
	global_load_dwordx4 v[114:117], v[32:33], off offset:576
	v_add_co_u32_e32 v118, vcc, s53, v18
	s_waitcnt vmcnt(3)
	v_pk_fma_f32 v[22:23], v[112:113], v[8:9], v[22:23]
	v_pk_fma_f32 v[20:21], v[110:111], v[6:7], v[20:21]
	s_waitcnt vmcnt(2)
	v_pk_fma_f32 v[26:27], v[108:109], v[4:5], v[26:27]
	v_pk_fma_f32 v[24:25], v[106:107], v[2:3], v[24:25]
	s_waitcnt vmcnt(1)
	v_pk_fma_f32 v[30:31], v[104:105], v[16:17], v[30:31]
	v_pk_fma_f32 v[28:29], v[102:103], v[14:15], v[28:29]
	s_waitcnt vmcnt(0)
	v_pk_fma_f32 v[100:101], v[100:101], v[12:13], v[116:117]
	v_pk_fma_f32 v[98:99], v[98:99], v[10:11], v[114:115]
	global_store_dwordx4 v[32:33], v[20:23], off
	global_store_dwordx4 v[32:33], v[24:27], off offset:64
	global_store_dwordx4 v[32:33], v[28:31], off offset:512
	global_store_dwordx4 v[32:33], v[98:101], off offset:576
	v_addc_co_u32_e32 v119, vcc, 0, v19, vcc
	global_load_dwordx4 v[20:23], v[118:119], off
	v_lshl_add_u64 v[32:33], v[18:19], 0, s[8:9]
	global_load_dwordx4 v[24:27], v[32:33], off offset:64
	global_load_dwordx4 v[28:31], v[32:33], off offset:512
	global_load_dwordx4 v[98:101], v[32:33], off offset:576
	v_add_co_u32_e32 v102, vcc, s54, v18
	s_waitcnt vmcnt(2)
	v_pk_fma_f32 v[26:27], v[92:93], v[4:5], v[26:27]
	v_pk_fma_f32 v[22:23], v[96:97], v[8:9], v[22:23]
	v_pk_fma_f32 v[20:21], v[94:95], v[6:7], v[20:21]
	v_pk_fma_f32 v[24:25], v[90:91], v[2:3], v[24:25]
	s_waitcnt vmcnt(1)
	v_pk_fma_f32 v[30:31], v[88:89], v[16:17], v[30:31]
	v_pk_fma_f32 v[28:29], v[86:87], v[14:15], v[28:29]
	s_waitcnt vmcnt(0)
	v_pk_fma_f32 v[84:85], v[84:85], v[12:13], v[100:101]
	v_pk_fma_f32 v[82:83], v[82:83], v[10:11], v[98:99]
	global_store_dwordx4 v[118:119], v[20:23], off
	global_store_dwordx4 v[32:33], v[24:27], off offset:64
	global_store_dwordx4 v[32:33], v[28:31], off offset:512
	global_store_dwordx4 v[32:33], v[82:85], off offset:576
	v_addc_co_u32_e32 v103, vcc, 0, v19, vcc
	global_load_dwordx4 v[20:23], v[102:103], off
	v_lshl_add_u64 v[32:33], v[18:19], 0, s[10:11]
	global_load_dwordx4 v[24:27], v[32:33], off offset:64
	global_load_dwordx4 v[28:31], v[32:33], off offset:512
	global_load_dwordx4 v[82:85], v[32:33], off offset:576
	v_add_co_u32_e32 v86, vcc, s55, v18
	s_waitcnt vmcnt(2)
	v_pk_fma_f32 v[26:27], v[76:77], v[4:5], v[26:27]
	v_pk_fma_f32 v[22:23], v[80:81], v[8:9], v[22:23]
	v_pk_fma_f32 v[20:21], v[78:79], v[6:7], v[20:21]
	v_pk_fma_f32 v[24:25], v[74:75], v[2:3], v[24:25]
	s_waitcnt vmcnt(1)
	v_pk_fma_f32 v[30:31], v[72:73], v[16:17], v[30:31]
	v_pk_fma_f32 v[28:29], v[70:71], v[14:15], v[28:29]
	s_waitcnt vmcnt(0)
	v_pk_fma_f32 v[68:69], v[68:69], v[12:13], v[84:85]
	v_pk_fma_f32 v[66:67], v[66:67], v[10:11], v[82:83]
	global_store_dwordx4 v[102:103], v[20:23], off
	global_store_dwordx4 v[32:33], v[24:27], off offset:64
	global_store_dwordx4 v[32:33], v[28:31], off offset:512
	global_store_dwordx4 v[32:33], v[66:69], off offset:576
	v_addc_co_u32_e32 v87, vcc, 0, v19, vcc
	global_load_dwordx4 v[20:23], v[86:87], off
	v_lshl_add_u64 v[32:33], v[18:19], 0, s[12:13]
	global_load_dwordx4 v[24:27], v[32:33], off offset:64
	global_load_dwordx4 v[28:31], v[32:33], off offset:512
	global_load_dwordx4 v[66:69], v[32:33], off offset:576
	v_add_co_u32_e32 v70, vcc, s56, v18
	s_waitcnt vmcnt(2)
	v_pk_fma_f32 v[26:27], v[60:61], v[4:5], v[26:27]
	v_pk_fma_f32 v[22:23], v[64:65], v[8:9], v[22:23]
	v_pk_fma_f32 v[20:21], v[62:63], v[6:7], v[20:21]
	v_pk_fma_f32 v[24:25], v[58:59], v[2:3], v[24:25]
	s_waitcnt vmcnt(1)
	v_pk_fma_f32 v[30:31], v[56:57], v[16:17], v[30:31]
	v_pk_fma_f32 v[28:29], v[54:55], v[14:15], v[28:29]
	s_waitcnt vmcnt(0)
	v_pk_fma_f32 v[52:53], v[52:53], v[12:13], v[68:69]
	v_pk_fma_f32 v[50:51], v[50:51], v[10:11], v[66:67]
	global_store_dwordx4 v[86:87], v[20:23], off
	global_store_dwordx4 v[32:33], v[24:27], off offset:64
	global_store_dwordx4 v[32:33], v[28:31], off offset:512
	global_store_dwordx4 v[32:33], v[50:53], off offset:576
	v_addc_co_u32_e32 v71, vcc, 0, v19, vcc
	global_load_dwordx4 v[20:23], v[70:71], off
	v_lshl_add_u64 v[18:19], v[18:19], 0, s[14:15]
	global_load_dwordx4 v[24:27], v[18:19], off offset:64
	global_load_dwordx4 v[28:31], v[18:19], off offset:512
	global_load_dwordx4 v[50:53], v[18:19], off offset:576
	s_and_b64 vcc, exec, s[2:3]
	s_waitcnt vmcnt(2)
	v_pk_fma_f32 v[4:5], v[44:45], v[4:5], v[26:27]
	v_pk_fma_f32 v[8:9], v[48:49], v[8:9], v[22:23]
	v_pk_fma_f32 v[6:7], v[46:47], v[6:7], v[20:21]
	v_pk_fma_f32 v[2:3], v[42:43], v[2:3], v[24:25]
	s_waitcnt vmcnt(1)
	v_pk_fma_f32 v[16:17], v[40:41], v[16:17], v[30:31]
	v_pk_fma_f32 v[14:15], v[38:39], v[14:15], v[28:29]
	s_waitcnt vmcnt(0)
	v_pk_fma_f32 v[12:13], v[36:37], v[12:13], v[52:53]
	v_pk_fma_f32 v[10:11], v[34:35], v[10:11], v[50:51]
	global_store_dwordx4 v[70:71], v[6:9], off
	global_store_dwordx4 v[18:19], v[2:5], off offset:64
	global_store_dwordx4 v[18:19], v[14:17], off offset:512
	global_store_dwordx4 v[18:19], v[10:13], off offset:576
	s_cbranch_vccz .LBB0_1527
	s_waitcnt vmcnt(0)
	s_cmpk_gt_u32 s33, 0xff
	s_cbranch_scc1 .LBB0_1538
	s_barrier

.LBB0_1722:
	s_ashr_i32 s37, s36, 31
	s_lshl_b64 s[40:41], s[36:37], 19
	s_add_u32 s40, s63, s40
	s_addc_u32 s41, s64, s41
	s_and_b64 s[44:45], s[42:43], exec
	s_cselect_b32 s37, s41, s51
	s_cselect_b32 s84, s40, s50
	s_ashr_i32 s39, s38, 31
	s_lshl_b64 s[44:45], s[38:39], 19
	s_add_u32 s44, s65, s44
	s_addc_u32 s45, s66, s45
	s_and_b64 s[54:55], s[42:43], exec
	s_cselect_b32 s39, s45, s53
	s_cselect_b32 s85, s44, s52
	s_add_u32 s50, s50, 0x40080
	s_addc_u32 s51, s51, 0
	s_add_u32 s86, s52, 0x100
	v_mov_b32_e32 v2, 0
	s_addc_u32 s87, s53, 0
	s_mov_b32 s88, -2
	ds_read_b128 v[158:161], v187
	ds_read_b128 v[154:157], v187 offset:1024
	ds_read_b128 v[150:153], v187 offset:2048
	ds_read_b128 v[146:149], v187 offset:3072
	ds_read_b128 v[142:145], v188
	ds_read_b128 v[138:141], v188 offset:1024
	ds_read_b128 v[134:137], v188 offset:2048
	ds_read_b128 v[130:133], v188 offset:3072
	s_add_u32 s52, s50, 0xfffc0080
	s_addc_u32 s53, s51, -1
	s_cmp_eq_u32 s88, 12
	s_cselect_b32 s55, s37, s53
	s_cselect_b32 s54, s84, s52
	s_cselect_b32 s53, s39, s87
	s_cselect_b32 s52, s85, s86
	v_lshl_add_u64 v[214:215], s[50:51], 0, v[170:171]
	s_add_i32 m0, s47, 0xc000
	ds_read_b128 v[174:177], v189
	ds_read_b128 v[182:185], v189 offset:1024
	ds_read_b128 v[190:193], v189 offset:2048
	ds_read_b128 v[194:197], v189 offset:3072
	ds_read_b128 v[198:201], v189 offset:4096
	ds_read_b128 v[202:205], v189 offset:5120
	ds_read_b128 v[206:209], v189 offset:6144
	ds_read_b128 v[210:213], v189 offset:7168
	global_load_lds_dwordx4 v[214:215], off
	v_lshl_add_u64 v[214:215], s[50:51], 0, v[172:173]
	s_add_i32 m0, s47, 0xe000
	s_nop 0
	global_load_lds_dwordx4 v[214:215], off
	s_waitcnt vmcnt(8)
	s_waitcnt lgkmcnt(0)
	s_barrier
	s_setprio 1
	s_waitcnt lgkmcnt(0)
	v_mfma_i32_16x16x64_i8 v[126:129], v[158:161], v[174:177], 0
	s_nop 0
	v_mfma_i32_16x16x64_i8 v[126:129], v[154:157], v[182:185], v[126:129]
	v_mfma_i32_16x16x64_i8 v[118:121], v[150:153], v[174:177], 0
	s_nop 0
	v_mfma_i32_16x16x64_i8 v[118:121], v[146:149], v[182:185], v[118:121]
	v_mfma_i32_16x16x64_i8 v[114:117], v[158:161], v[190:193], 0
	s_nop 0
	v_mfma_i32_16x16x64_i8 v[114:117], v[154:157], v[194:197], v[114:117]
	v_mfma_i32_16x16x64_i8 v[110:113], v[150:153], v[190:193], 0
	s_nop 0
	v_mfma_i32_16x16x64_i8 v[110:113], v[146:149], v[194:197], v[110:113]
	v_mfma_i32_16x16x64_i8 v[94:97], v[158:161], v[198:201], 0
	s_nop 0
	v_mfma_i32_16x16x64_i8 v[94:97], v[154:157], v[202:205], v[94:97]
	v_mfma_i32_16x16x64_i8 v[86:89], v[150:153], v[198:201], 0
	s_nop 0
	v_mfma_i32_16x16x64_i8 v[86:89], v[146:149], v[202:205], v[86:89]
	v_mfma_i32_16x16x64_i8 v[82:85], v[158:161], v[206:209], 0
	s_nop 0
	v_mfma_i32_16x16x64_i8 v[82:85], v[154:157], v[210:213], v[82:85]
	v_mfma_i32_16x16x64_i8 v[74:77], v[150:153], v[206:209], 0
	s_nop 0
	v_mfma_i32_16x16x64_i8 v[74:77], v[146:149], v[210:213], v[74:77]
	s_setprio 0
	s_setprio 1
	v_mfma_i32_16x16x64_i8 v[122:125], v[142:145], v[174:177], 0
	s_nop 0
	v_mfma_i32_16x16x64_i8 v[122:125], v[138:141], v[182:185], v[122:125]
	v_mfma_i32_16x16x64_i8 v[106:109], v[134:137], v[174:177], 0
	s_nop 0
	v_mfma_i32_16x16x64_i8 v[106:109], v[130:133], v[182:185], v[106:109]
	v_mfma_i32_16x16x64_i8 v[102:105], v[142:145], v[190:193], 0
	s_nop 0
	v_mfma_i32_16x16x64_i8 v[102:105], v[138:141], v[194:197], v[102:105]
	v_mfma_i32_16x16x64_i8 v[98:101], v[134:137], v[190:193], 0
	s_nop 0
	v_mfma_i32_16x16x64_i8 v[98:101], v[130:133], v[194:197], v[98:101]
	v_mfma_i32_16x16x64_i8 v[90:93], v[142:145], v[198:201], 0
	s_nop 0
	v_mfma_i32_16x16x64_i8 v[90:93], v[138:141], v[202:205], v[90:93]
	v_mfma_i32_16x16x64_i8 v[78:81], v[134:137], v[198:201], 0
	s_nop 0
	v_mfma_i32_16x16x64_i8 v[78:81], v[130:133], v[202:205], v[78:81]
	v_mfma_i32_16x16x64_i8 v[70:73], v[142:145], v[206:209], 0
	s_nop 0
	v_mfma_i32_16x16x64_i8 v[70:73], v[138:141], v[210:213], v[70:73]
	v_mfma_i32_16x16x64_i8 v[66:69], v[134:137], v[206:209], 0
	s_nop 0
	v_mfma_i32_16x16x64_i8 v[66:69], v[130:133], v[210:213], v[66:69]
	s_setprio 0
	s_barrier
	s_add_i32 s89, s79, s67
	v_lshl_add_u64 v[174:175], s[52:53], 0, v[164:165]
	s_mov_b32 m0, s89
	ds_read_b128 v[190:193], v189 offset:16384
	ds_read_b128 v[194:197], v189 offset:17408
	ds_read_b128 v[198:201], v189 offset:18432
	ds_read_b128 v[202:205], v189 offset:19456
	ds_read_b128 v[206:209], v189 offset:20480
	ds_read_b128 v[210:213], v189 offset:21504
	ds_read_b128 v[214:217], v189 offset:22528
	ds_read_b128 v[218:221], v189 offset:23552
	global_load_lds_dwordx4 v[174:175], off
	s_add_i32 m0, s89, 0x2000
	s_add_u32 s90, s52, 0x40000
	v_lshl_add_u64 v[176:177], s[52:53], 0, v[168:169]
	s_addc_u32 s91, s53, 0
	s_add_i32 s89, s80, s67
	global_load_lds_dwordx4 v[176:177], off
	v_lshl_add_u64 v[182:183], s[90:91], 0, v[164:165]
	s_mov_b32 m0, s89
	v_lshl_add_u64 v[184:185], s[54:55], 0, v[166:167]
	global_load_lds_dwordx4 v[182:183], off
	v_lshl_add_u64 v[182:183], s[90:91], 0, v[168:169]
	s_add_i32 m0, s89, 0x2000
	s_nop 0
	global_load_lds_dwordx4 v[182:183], off
	v_lshl_add_u64 v[182:183], s[54:55], 0, v[162:163]
	s_mov_b32 m0, s47
	s_nop 0
	global_load_lds_dwordx4 v[182:183], off
	s_mov_b32 m0, s49
	s_nop 0
	global_load_lds_dwordx4 v[184:185], off
	s_waitcnt vmcnt(8)
	s_waitcnt lgkmcnt(0)
	s_barrier
	s_setprio 1
	s_waitcnt lgkmcnt(0)
	v_mfma_i32_16x16x64_i8 v[62:65], v[158:161], v[190:193], 0
	s_nop 0
	v_mfma_i32_16x16x64_i8 v[62:65], v[154:157], v[194:197], v[62:65]
	v_mfma_i32_16x16x64_i8 v[58:61], v[150:153], v[190:193], 0
	s_nop 0
	v_mfma_i32_16x16x64_i8 v[58:61], v[146:149], v[194:197], v[58:61]
	v_mfma_i32_16x16x64_i8 v[50:53], v[158:161], v[198:201], 0
	s_nop 0
	v_mfma_i32_16x16x64_i8 v[50:53], v[154:157], v[202:205], v[50:53]
	v_mfma_i32_16x16x64_i8 v[42:45], v[150:153], v[198:201], 0
	s_nop 0
	v_mfma_i32_16x16x64_i8 v[42:45], v[146:149], v[202:205], v[42:45]
	v_mfma_i32_16x16x64_i8 v[34:37], v[158:161], v[206:209], 0
	s_nop 0
	v_mfma_i32_16x16x64_i8 v[34:37], v[154:157], v[210:213], v[34:37]
	v_mfma_i32_16x16x64_i8 v[26:29], v[150:153], v[206:209], 0
	s_nop 0
	v_mfma_i32_16x16x64_i8 v[26:29], v[146:149], v[210:213], v[26:29]
	v_mfma_i32_16x16x64_i8 v[18:21], v[158:161], v[214:217], 0
	s_nop 0
	v_mfma_i32_16x16x64_i8 v[18:21], v[154:157], v[218:221], v[18:21]
	v_mfma_i32_16x16x64_i8 v[10:13], v[150:153], v[214:217], 0
	s_nop 0
	v_mfma_i32_16x16x64_i8 v[10:13], v[146:149], v[218:221], v[10:13]
	s_setprio 0
	s_setprio 1
	v_mfma_i32_16x16x64_i8 v[54:57], v[142:145], v[190:193], 0
	s_nop 0
	v_mfma_i32_16x16x64_i8 v[54:57], v[138:141], v[194:197], v[54:57]
	v_mfma_i32_16x16x64_i8 v[46:49], v[134:137], v[190:193], 0
	s_nop 0
	v_mfma_i32_16x16x64_i8 v[46:49], v[130:133], v[194:197], v[46:49]
	v_mfma_i32_16x16x64_i8 v[38:41], v[142:145], v[198:201], 0
	s_nop 0
	v_mfma_i32_16x16x64_i8 v[38:41], v[138:141], v[202:205], v[38:41]
	v_mfma_i32_16x16x64_i8 v[30:33], v[134:137], v[198:201], 0
	s_nop 0
	v_mfma_i32_16x16x64_i8 v[30:33], v[130:133], v[202:205], v[30:33]
	v_mfma_i32_16x16x64_i8 v[22:25], v[142:145], v[206:209], 0
	s_nop 0
	v_mfma_i32_16x16x64_i8 v[22:25], v[138:141], v[210:213], v[22:25]
	v_mfma_i32_16x16x64_i8 v[14:17], v[134:137], v[206:209], 0
	s_nop 0
	v_mfma_i32_16x16x64_i8 v[14:17], v[130:133], v[210:213], v[14:17]
	v_mfma_i32_16x16x64_i8 v[6:9], v[142:145], v[214:217], 0
	s_nop 0
	v_mfma_i32_16x16x64_i8 v[6:9], v[138:141], v[218:221], v[6:9]
	v_mfma_i32_16x16x64_i8 v[2:5], v[134:137], v[214:217], 0
	s_nop 0
	v_mfma_i32_16x16x64_i8 v[2:5], v[130:133], v[218:221], v[2:5]
	s_setprio 0
	s_barrier
	s_add_i32 s89, 0, 0x18000
	s_add_i32 s90, 0, 0x1c000
	v_add_u32_e32 v142, s89, v181
	v_add_u32_e32 v158, s90, v181
	ds_read_b128 v[130:133], v142
	ds_read_b128 v[134:137], v142 offset:1024
	ds_read_b128 v[138:141], v142 offset:2048
	ds_read_b128 v[142:145], v142 offset:3072
	ds_read_b128 v[146:149], v158
	ds_read_b128 v[150:153], v158 offset:1024
	ds_read_b128 v[154:157], v158 offset:2048
	ds_read_b128 v[158:161], v158 offset:3072
	s_add_u32 s54, s54, 0x40000
	s_addc_u32 s55, s55, 0
	s_mov_b32 m0, s68
	v_lshl_add_u64 v[222:223], s[54:55], 0, v[162:163]
	ds_read_b128 v[190:193], v189 offset:32768
	ds_read_b128 v[194:197], v189 offset:33792
	ds_read_b128 v[198:201], v189 offset:34816
	ds_read_b128 v[202:205], v189 offset:35840
	ds_read_b128 v[206:209], v189 offset:36864
	ds_read_b128 v[210:213], v189 offset:37888
	ds_read_b128 v[214:217], v189 offset:38912
	ds_read_b128 v[218:221], v189 offset:39936
	global_load_lds_dwordx4 v[222:223], off
	v_lshl_add_u64 v[222:223], s[54:55], 0, v[166:167]
	s_mov_b32 m0, s69
	s_nop 0
	global_load_lds_dwordx4 v[222:223], off
	s_waitcnt vmcnt(8)
	s_waitcnt lgkmcnt(0)
	s_barrier
	s_setprio 1
	s_waitcnt lgkmcnt(0)
	v_mfma_i32_16x16x64_i8 v[126:129], v[130:133], v[190:193], v[126:129]
	s_nop 0
	v_mfma_i32_16x16x64_i8 v[126:129], v[134:137], v[194:197], v[126:129]
	v_mfma_i32_16x16x64_i8 v[118:121], v[138:141], v[190:193], v[118:121]
	s_nop 0
	v_mfma_i32_16x16x64_i8 v[118:121], v[142:145], v[194:197], v[118:121]
	v_mfma_i32_16x16x64_i8 v[114:117], v[130:133], v[198:201], v[114:117]
	s_nop 0
	v_mfma_i32_16x16x64_i8 v[114:117], v[134:137], v[202:205], v[114:117]
	v_mfma_i32_16x16x64_i8 v[110:113], v[138:141], v[198:201], v[110:113]
	s_nop 0
	v_mfma_i32_16x16x64_i8 v[110:113], v[142:145], v[202:205], v[110:113]
	v_mfma_i32_16x16x64_i8 v[94:97], v[130:133], v[206:209], v[94:97]
	s_nop 0
	v_mfma_i32_16x16x64_i8 v[94:97], v[134:137], v[210:213], v[94:97]
	v_mfma_i32_16x16x64_i8 v[86:89], v[138:141], v[206:209], v[86:89]
	s_nop 0
	v_mfma_i32_16x16x64_i8 v[86:89], v[142:145], v[210:213], v[86:89]
	v_mfma_i32_16x16x64_i8 v[82:85], v[130:133], v[214:217], v[82:85]
	s_nop 0
	v_mfma_i32_16x16x64_i8 v[82:85], v[134:137], v[218:221], v[82:85]
	v_mfma_i32_16x16x64_i8 v[74:77], v[138:141], v[214:217], v[74:77]
	s_nop 0
	v_mfma_i32_16x16x64_i8 v[74:77], v[142:145], v[218:221], v[74:77]
	s_setprio 0
	s_setprio 1
	v_mfma_i32_16x16x64_i8 v[122:125], v[146:149], v[190:193], v[122:125]
	s_nop 0
	v_mfma_i32_16x16x64_i8 v[122:125], v[150:153], v[194:197], v[122:125]
	v_mfma_i32_16x16x64_i8 v[106:109], v[154:157], v[190:193], v[106:109]
	s_nop 0
	v_mfma_i32_16x16x64_i8 v[106:109], v[158:161], v[194:197], v[106:109]
	v_mfma_i32_16x16x64_i8 v[102:105], v[146:149], v[198:201], v[102:105]
	s_nop 0
	v_mfma_i32_16x16x64_i8 v[102:105], v[150:153], v[202:205], v[102:105]
	v_mfma_i32_16x16x64_i8 v[98:101], v[154:157], v[198:201], v[98:101]
	s_nop 0
	v_mfma_i32_16x16x64_i8 v[98:101], v[158:161], v[202:205], v[98:101]
	v_mfma_i32_16x16x64_i8 v[90:93], v[146:149], v[206:209], v[90:93]
	s_nop 0
	v_mfma_i32_16x16x64_i8 v[90:93], v[150:153], v[210:213], v[90:93]
	v_mfma_i32_16x16x64_i8 v[78:81], v[154:157], v[206:209], v[78:81]
	s_nop 0
	v_mfma_i32_16x16x64_i8 v[78:81], v[158:161], v[210:213], v[78:81]
	v_mfma_i32_16x16x64_i8 v[70:73], v[146:149], v[214:217], v[70:73]
	s_nop 0
	v_mfma_i32_16x16x64_i8 v[70:73], v[150:153], v[218:221], v[70:73]
	v_mfma_i32_16x16x64_i8 v[66:69], v[154:157], v[214:217], v[66:69]
	s_nop 0
	v_mfma_i32_16x16x64_i8 v[66:69], v[158:161], v[218:221], v[66:69]
	s_setprio 0
	s_barrier
	s_add_i32 s54, s89, s67
	v_lshl_add_u64 v[174:175], v[174:175], 0, s[28:29]
	s_mov_b32 m0, s54
	ds_read_b128 v[190:193], v189 offset:49152
	ds_read_b128 v[194:197], v189 offset:50176
	ds_read_b128 v[198:201], v189 offset:51200
	ds_read_b128 v[202:205], v189 offset:52224
	ds_read_b128 v[206:209], v189 offset:53248
	ds_read_b128 v[210:213], v189 offset:54272
	ds_read_b128 v[214:217], v189 offset:55296
	ds_read_b128 v[218:221], v189 offset:56320
	global_load_lds_dwordx4 v[174:175], off
	s_add_i32 m0, s54, 0x2000
	s_add_u32 s52, s52, 0x40080
	v_lshl_add_u64 v[174:175], v[176:177], 0, s[28:29]
	s_addc_u32 s53, s53, 0
	s_add_i32 s54, s90, s67
	global_load_lds_dwordx4 v[174:175], off
	v_lshl_add_u64 v[174:175], s[52:53], 0, v[164:165]
	s_mov_b32 m0, s54
	s_nop 0
	global_load_lds_dwordx4 v[174:175], off
	v_lshl_add_u64 v[174:175], s[52:53], 0, v[168:169]
	s_add_i32 m0, s54, 0x2000
	s_nop 0
	global_load_lds_dwordx4 v[174:175], off
	v_lshl_add_u64 v[174:175], v[182:183], 0, s[28:29]
	s_mov_b32 m0, s71
	s_nop 0
	global_load_lds_dwordx4 v[174:175], off
	v_lshl_add_u64 v[174:175], v[184:185], 0, s[28:29]
	s_mov_b32 m0, s72
	s_nop 0
	global_load_lds_dwordx4 v[174:175], off
	s_waitcnt vmcnt(8)
	s_waitcnt lgkmcnt(0)
	s_barrier
	s_setprio 1
	s_waitcnt lgkmcnt(0)
	v_mfma_i32_16x16x64_i8 v[62:65], v[130:133], v[190:193], v[62:65]
	s_nop 0
	v_mfma_i32_16x16x64_i8 v[62:65], v[134:137], v[194:197], v[62:65]
	v_mfma_i32_16x16x64_i8 v[58:61], v[138:141], v[190:193], v[58:61]
	s_nop 0
	v_mfma_i32_16x16x64_i8 v[58:61], v[142:145], v[194:197], v[58:61]
	v_mfma_i32_16x16x64_i8 v[50:53], v[130:133], v[198:201], v[50:53]
	s_nop 0
	v_mfma_i32_16x16x64_i8 v[50:53], v[134:137], v[202:205], v[50:53]
	v_mfma_i32_16x16x64_i8 v[42:45], v[138:141], v[198:201], v[42:45]
	s_nop 0
	v_mfma_i32_16x16x64_i8 v[42:45], v[142:145], v[202:205], v[42:45]
	v_mfma_i32_16x16x64_i8 v[34:37], v[130:133], v[206:209], v[34:37]
	s_nop 0
	v_mfma_i32_16x16x64_i8 v[34:37], v[134:137], v[210:213], v[34:37]
	v_mfma_i32_16x16x64_i8 v[26:29], v[138:141], v[206:209], v[26:29]
	s_nop 0
	v_mfma_i32_16x16x64_i8 v[26:29], v[142:145], v[210:213], v[26:29]
	v_mfma_i32_16x16x64_i8 v[18:21], v[130:133], v[214:217], v[18:21]
	s_nop 0
	v_mfma_i32_16x16x64_i8 v[18:21], v[134:137], v[218:221], v[18:21]
	v_mfma_i32_16x16x64_i8 v[10:13], v[138:141], v[214:217], v[10:13]
	s_nop 0
	v_mfma_i32_16x16x64_i8 v[10:13], v[142:145], v[218:221], v[10:13]
	s_setprio 0
	s_setprio 1
	v_mfma_i32_16x16x64_i8 v[54:57], v[146:149], v[190:193], v[54:57]
	s_nop 0
	v_mfma_i32_16x16x64_i8 v[54:57], v[150:153], v[194:197], v[54:57]
	v_mfma_i32_16x16x64_i8 v[46:49], v[154:157], v[190:193], v[46:49]
	s_nop 0
	v_mfma_i32_16x16x64_i8 v[46:49], v[158:161], v[194:197], v[46:49]
	v_mfma_i32_16x16x64_i8 v[38:41], v[146:149], v[198:201], v[38:41]
	s_nop 0
	v_mfma_i32_16x16x64_i8 v[38:41], v[150:153], v[202:205], v[38:41]
	v_mfma_i32_16x16x64_i8 v[30:33], v[154:157], v[198:201], v[30:33]
	s_nop 0
	v_mfma_i32_16x16x64_i8 v[30:33], v[158:161], v[202:205], v[30:33]
	v_mfma_i32_16x16x64_i8 v[22:25], v[146:149], v[206:209], v[22:25]
	s_nop 0
	v_mfma_i32_16x16x64_i8 v[22:25], v[150:153], v[210:213], v[22:25]
	v_mfma_i32_16x16x64_i8 v[14:17], v[154:157], v[206:209], v[14:17]
	s_nop 0
	v_mfma_i32_16x16x64_i8 v[14:17], v[158:161], v[210:213], v[14:17]
	v_mfma_i32_16x16x64_i8 v[6:9], v[146:149], v[214:217], v[6:9]
	s_nop 0
	v_mfma_i32_16x16x64_i8 v[6:9], v[150:153], v[218:221], v[6:9]
	v_mfma_i32_16x16x64_i8 v[2:5], v[154:157], v[214:217], v[2:5]
	s_nop 0
	v_mfma_i32_16x16x64_i8 v[2:5], v[158:161], v[218:221], v[2:5]
	s_setprio 0
	s_barrier
	s_add_i32 s88, s88, 2
	s_add_u32 s50, s50, 0x100
	s_addc_u32 s51, s51, 0
	s_add_u32 s86, s86, 0x100
	s_addc_u32 s87, s87, 0
	s_cmp_gt_u32 s88, 13
	s_cbranch_scc1 .Lpeel_exit_1723

.Lpeel_exit_1723:
	s_and_b64 vcc, exec, s[30:31]
	s_cbranch_vccz .LBB0_1726
	s_barrier

.LBB0_1802:
	s_add_i32 s13, s93, -2
	s_add_u32 s6, s64, 0xe0080
	s_addc_u32 s7, s65, 0
	s_add_u32 s47, s62, 0x100
	v_mov_b32_e32 v34, 0
	s_addc_u32 s51, s63, 0
	s_mov_b32 s8, 0
	ds_read_b128 v[18:21], v187
	ds_read_b128 v[22:25], v187 offset:1024
	ds_read_b128 v[26:29], v187 offset:2048
	ds_read_b128 v[30:33], v187 offset:3072
	ds_read_b128 v[2:5], v188
	ds_read_b128 v[6:9], v188 offset:1024
	ds_read_b128 v[10:13], v188 offset:2048
	ds_read_b128 v[14:17], v188 offset:3072
	s_add_i32 s55, s8, 2
	s_add_u32 s9, s6, 0xfff20080
	s_addc_u32 s10, s7, -1
	s_cmp_eq_u32 s13, s8
	s_cselect_b32 s8, s4, s47
	s_cselect_b32 s11, s3, s10
	s_cselect_b32 s10, s2, s9
	s_cselect_b32 s9, s5, s51
	v_lshl_add_u64 v[176:177], s[6:7], 0, v[170:171]
	s_add_i32 m0, s80, 0xc000
	ds_read_b128 v[192:195], v189
	ds_read_b128 v[196:199], v189 offset:1024
	ds_read_b128 v[200:203], v189 offset:2048
	ds_read_b128 v[204:207], v189 offset:3072
	ds_read_b128 v[208:211], v189 offset:4096
	ds_read_b128 v[212:215], v189 offset:5120
	ds_read_b128 v[216:219], v189 offset:6144
	ds_read_b128 v[220:223], v189 offset:7168
	global_load_lds_dwordx4 v[176:177], off
	v_lshl_add_u64 v[176:177], s[6:7], 0, v[172:173]
	s_add_i32 m0, s80, 0xe000
	s_nop 0
	global_load_lds_dwordx4 v[176:177], off
	s_waitcnt vmcnt(8)
	s_waitcnt lgkmcnt(0)
	s_barrier
	s_setprio 1
	s_waitcnt lgkmcnt(0)
	v_mfma_scale_f32_16x16x128_f8f6f4 v[158:161], v[18:25], v[192:199], 0, v190, v191 op_sel_hi:[0,0,0]
	v_mfma_scale_f32_16x16x128_f8f6f4 v[154:157], v[26:33], v[192:199], 0, v190, v191 op_sel_hi:[0,0,0]
	v_mfma_scale_f32_16x16x128_f8f6f4 v[150:153], v[18:25], v[200:207], 0, v190, v191 op_sel_hi:[0,0,0]
	v_mfma_scale_f32_16x16x128_f8f6f4 v[142:145], v[26:33], v[200:207], 0, v190, v191 op_sel_hi:[0,0,0]
	v_mfma_scale_f32_16x16x128_f8f6f4 v[134:137], v[18:25], v[208:215], 0, v190, v191 op_sel_hi:[0,0,0]
	v_mfma_scale_f32_16x16x128_f8f6f4 v[126:129], v[26:33], v[208:215], 0, v190, v191 op_sel_hi:[0,0,0]
	v_mfma_scale_f32_16x16x128_f8f6f4 v[118:121], v[18:25], v[216:223], 0, v190, v191 op_sel_hi:[0,0,0]
	v_mfma_scale_f32_16x16x128_f8f6f4 v[110:113], v[26:33], v[216:223], 0, v190, v191 op_sel_hi:[0,0,0]
	s_setprio 0
	s_setprio 1
	v_mfma_scale_f32_16x16x128_f8f6f4 v[146:149], v[2:9], v[192:199], 0, v190, v191 op_sel_hi:[0,0,0]
	v_mfma_scale_f32_16x16x128_f8f6f4 v[138:141], v[10:17], v[192:199], 0, v190, v191 op_sel_hi:[0,0,0]
	v_mfma_scale_f32_16x16x128_f8f6f4 v[130:133], v[2:9], v[200:207], 0, v190, v191 op_sel_hi:[0,0,0]
	v_mfma_scale_f32_16x16x128_f8f6f4 v[122:125], v[10:17], v[200:207], 0, v190, v191 op_sel_hi:[0,0,0]
	v_mfma_scale_f32_16x16x128_f8f6f4 v[114:117], v[2:9], v[208:215], 0, v190, v191 op_sel_hi:[0,0,0]
	v_mfma_scale_f32_16x16x128_f8f6f4 v[106:109], v[10:17], v[208:215], 0, v190, v191 op_sel_hi:[0,0,0]
	v_mfma_scale_f32_16x16x128_f8f6f4 v[102:105], v[2:9], v[216:223], 0, v190, v191 op_sel_hi:[0,0,0]
	v_mfma_scale_f32_16x16x128_f8f6f4 v[98:101], v[10:17], v[216:223], 0, v190, v191 op_sel_hi:[0,0,0]
	s_setprio 0
	s_barrier
	s_add_i32 s61, s31, s79
	v_lshl_add_u64 v[176:177], s[8:9], 0, v[164:165]
	s_mov_b32 m0, s61
	ds_read_b128 v[192:195], v189 offset:16384
	ds_read_b128 v[196:199], v189 offset:17408
	ds_read_b128 v[200:203], v189 offset:18432
	ds_read_b128 v[204:207], v189 offset:19456
	ds_read_b128 v[208:211], v189 offset:20480
	ds_read_b128 v[212:215], v189 offset:21504
	ds_read_b128 v[216:219], v189 offset:22528
	ds_read_b128 v[220:223], v189 offset:23552
	global_load_lds_dwordx4 v[176:177], off
	s_add_i32 m0, s61, 0x2000
	s_add_u32 s62, s8, 0xe0000
	v_lshl_add_u64 v[180:181], s[8:9], 0, v[168:169]
	s_addc_u32 s63, s9, 0
	s_add_i32 s61, s35, s79
	global_load_lds_dwordx4 v[180:181], off
	v_lshl_add_u64 v[182:183], s[62:63], 0, v[164:165]
	s_mov_b32 m0, s61
	v_lshl_add_u64 v[184:185], s[10:11], 0, v[166:167]
	global_load_lds_dwordx4 v[182:183], off
	v_lshl_add_u64 v[182:183], s[62:63], 0, v[168:169]
	s_add_i32 m0, s61, 0x2000
	s_nop 0
	global_load_lds_dwordx4 v[182:183], off
	v_lshl_add_u64 v[182:183], s[10:11], 0, v[162:163]
	s_mov_b32 m0, s80
	s_nop 0
	global_load_lds_dwordx4 v[182:183], off
	s_mov_b32 m0, s81
	s_nop 0
	global_load_lds_dwordx4 v[184:185], off
	s_waitcnt vmcnt(8)
	s_waitcnt lgkmcnt(0)
	s_barrier
	s_setprio 1
	s_waitcnt lgkmcnt(0)
	v_mfma_scale_f32_16x16x128_f8f6f4 v[94:97], v[18:25], v[192:199], 0, v190, v191 op_sel_hi:[0,0,0]
	v_mfma_scale_f32_16x16x128_f8f6f4 v[90:93], v[26:33], v[192:199], 0, v190, v191 op_sel_hi:[0,0,0]
	v_mfma_scale_f32_16x16x128_f8f6f4 v[86:89], v[18:25], v[200:207], 0, v190, v191 op_sel_hi:[0,0,0]
	v_mfma_scale_f32_16x16x128_f8f6f4 v[78:81], v[26:33], v[200:207], 0, v190, v191 op_sel_hi:[0,0,0]
	v_mfma_scale_f32_16x16x128_f8f6f4 v[70:73], v[18:25], v[208:215], 0, v190, v191 op_sel_hi:[0,0,0]
	v_mfma_scale_f32_16x16x128_f8f6f4 v[62:65], v[26:33], v[208:215], 0, v190, v191 op_sel_hi:[0,0,0]
	v_mfma_scale_f32_16x16x128_f8f6f4 v[54:57], v[18:25], v[216:223], 0, v190, v191 op_sel_hi:[0,0,0]
	v_mfma_scale_f32_16x16x128_f8f6f4 v[46:49], v[26:33], v[216:223], 0, v190, v191 op_sel_hi:[0,0,0]
	s_setprio 0
	s_setprio 1
	v_mfma_scale_f32_16x16x128_f8f6f4 v[82:85], v[2:9], v[192:199], 0, v190, v191 op_sel_hi:[0,0,0]
	v_mfma_scale_f32_16x16x128_f8f6f4 v[74:77], v[10:17], v[192:199], 0, v190, v191 op_sel_hi:[0,0,0]
	v_mfma_scale_f32_16x16x128_f8f6f4 v[66:69], v[2:9], v[200:207], 0, v190, v191 op_sel_hi:[0,0,0]
	v_mfma_scale_f32_16x16x128_f8f6f4 v[58:61], v[10:17], v[200:207], 0, v190, v191 op_sel_hi:[0,0,0]
	v_mfma_scale_f32_16x16x128_f8f6f4 v[50:53], v[2:9], v[208:215], 0, v190, v191 op_sel_hi:[0,0,0]
	v_mfma_scale_f32_16x16x128_f8f6f4 v[42:45], v[10:17], v[208:215], 0, v190, v191 op_sel_hi:[0,0,0]
	v_mfma_scale_f32_16x16x128_f8f6f4 v[38:41], v[2:9], v[216:223], 0, v190, v191 op_sel_hi:[0,0,0]
	v_mfma_scale_f32_16x16x128_f8f6f4 v[34:37], v[10:17], v[216:223], 0, v190, v191 op_sel_hi:[0,0,0]
	s_setprio 0
	s_barrier
	s_add_i32 s61, 0, 0x18000
	s_add_i32 s62, 0, 0x1c000
	v_add_u32_e32 v14, s61, v179
	v_add_u32_e32 v30, s62, v179
	ds_read_b128 v[2:5], v14
	ds_read_b128 v[6:9], v14 offset:1024
	ds_read_b128 v[10:13], v14 offset:2048
	ds_read_b128 v[14:17], v14 offset:3072
	ds_read_b128 v[18:21], v30
	ds_read_b128 v[22:25], v30 offset:1024
	ds_read_b128 v[26:29], v30 offset:2048
	ds_read_b128 v[30:33], v30 offset:3072
	s_add_u32 s10, s10, 0xe0000
	s_addc_u32 s11, s11, 0
	s_mov_b32 m0, s82
	v_lshl_add_u64 v[224:225], s[10:11], 0, v[162:163]
	ds_read_b128 v[192:195], v189 offset:32768
	ds_read_b128 v[196:199], v189 offset:33792
	ds_read_b128 v[200:203], v189 offset:34816
	ds_read_b128 v[204:207], v189 offset:35840
	ds_read_b128 v[208:211], v189 offset:36864
	ds_read_b128 v[212:215], v189 offset:37888
	ds_read_b128 v[216:219], v189 offset:38912
	ds_read_b128 v[220:223], v189 offset:39936
	global_load_lds_dwordx4 v[224:225], off
	v_lshl_add_u64 v[224:225], s[10:11], 0, v[166:167]
	s_mov_b32 m0, s83
	s_nop 0
	global_load_lds_dwordx4 v[224:225], off
	s_waitcnt vmcnt(8)
	s_waitcnt lgkmcnt(0)
	s_barrier
	s_setprio 1
	s_waitcnt lgkmcnt(0)
	v_mfma_scale_f32_16x16x128_f8f6f4 v[158:161], v[2:9], v[192:199], v[158:161], v190, v191 op_sel_hi:[0,0,0]
	v_mfma_scale_f32_16x16x128_f8f6f4 v[154:157], v[10:17], v[192:199], v[154:157], v190, v191 op_sel_hi:[0,0,0]
	v_mfma_scale_f32_16x16x128_f8f6f4 v[150:153], v[2:9], v[200:207], v[150:153], v190, v191 op_sel_hi:[0,0,0]
	v_mfma_scale_f32_16x16x128_f8f6f4 v[142:145], v[10:17], v[200:207], v[142:145], v190, v191 op_sel_hi:[0,0,0]
	v_mfma_scale_f32_16x16x128_f8f6f4 v[134:137], v[2:9], v[208:215], v[134:137], v190, v191 op_sel_hi:[0,0,0]
	v_mfma_scale_f32_16x16x128_f8f6f4 v[126:129], v[10:17], v[208:215], v[126:129], v190, v191 op_sel_hi:[0,0,0]
	v_mfma_scale_f32_16x16x128_f8f6f4 v[118:121], v[2:9], v[216:223], v[118:121], v190, v191 op_sel_hi:[0,0,0]
	v_mfma_scale_f32_16x16x128_f8f6f4 v[110:113], v[10:17], v[216:223], v[110:113], v190, v191 op_sel_hi:[0,0,0]
	s_setprio 0
	s_setprio 1
	v_mfma_scale_f32_16x16x128_f8f6f4 v[146:149], v[18:25], v[192:199], v[146:149], v190, v191 op_sel_hi:[0,0,0]
	v_mfma_scale_f32_16x16x128_f8f6f4 v[138:141], v[26:33], v[192:199], v[138:141], v190, v191 op_sel_hi:[0,0,0]
	v_mfma_scale_f32_16x16x128_f8f6f4 v[130:133], v[18:25], v[200:207], v[130:133], v190, v191 op_sel_hi:[0,0,0]
	v_mfma_scale_f32_16x16x128_f8f6f4 v[122:125], v[26:33], v[200:207], v[122:125], v190, v191 op_sel_hi:[0,0,0]
	v_mfma_scale_f32_16x16x128_f8f6f4 v[114:117], v[18:25], v[208:215], v[114:117], v190, v191 op_sel_hi:[0,0,0]
	v_mfma_scale_f32_16x16x128_f8f6f4 v[106:109], v[26:33], v[208:215], v[106:109], v190, v191 op_sel_hi:[0,0,0]
	v_mfma_scale_f32_16x16x128_f8f6f4 v[102:105], v[18:25], v[216:223], v[102:105], v190, v191 op_sel_hi:[0,0,0]
	v_mfma_scale_f32_16x16x128_f8f6f4 v[98:101], v[26:33], v[216:223], v[98:101], v190, v191 op_sel_hi:[0,0,0]
	s_setprio 0
	s_barrier
	s_add_i32 s10, s61, s79
	v_lshl_add_u64 v[176:177], v[176:177], 0, s[26:27]
	s_mov_b32 m0, s10
	ds_read_b128 v[192:195], v189 offset:49152
	ds_read_b128 v[196:199], v189 offset:50176
	ds_read_b128 v[200:203], v189 offset:51200
	ds_read_b128 v[204:207], v189 offset:52224
	ds_read_b128 v[208:211], v189 offset:53248
	ds_read_b128 v[212:215], v189 offset:54272
	ds_read_b128 v[216:219], v189 offset:55296
	ds_read_b128 v[220:223], v189 offset:56320
	global_load_lds_dwordx4 v[176:177], off
	s_add_i32 m0, s10, 0x2000
	s_add_u32 s8, s8, 0xe0080
	v_lshl_add_u64 v[176:177], v[180:181], 0, s[26:27]
	s_addc_u32 s9, s9, 0
	s_add_i32 s10, s62, s79
	global_load_lds_dwordx4 v[176:177], off
	v_lshl_add_u64 v[176:177], s[8:9], 0, v[164:165]
	s_mov_b32 m0, s10
	s_nop 0
	global_load_lds_dwordx4 v[176:177], off
	v_lshl_add_u64 v[176:177], s[8:9], 0, v[168:169]
	s_add_i32 m0, s10, 0x2000
	s_nop 0
	global_load_lds_dwordx4 v[176:177], off
	v_lshl_add_u64 v[176:177], v[182:183], 0, s[26:27]
	s_mov_b32 m0, s85
	s_nop 0
	global_load_lds_dwordx4 v[176:177], off
	v_lshl_add_u64 v[176:177], v[184:185], 0, s[26:27]
	s_mov_b32 m0, s86
	s_nop 0
	global_load_lds_dwordx4 v[176:177], off
	s_waitcnt vmcnt(8)
	s_waitcnt lgkmcnt(0)
	s_barrier
	s_setprio 1
	s_waitcnt lgkmcnt(0)
	v_mfma_scale_f32_16x16x128_f8f6f4 v[94:97], v[2:9], v[192:199], v[94:97], v190, v191 op_sel_hi:[0,0,0]
	v_mfma_scale_f32_16x16x128_f8f6f4 v[90:93], v[10:17], v[192:199], v[90:93], v190, v191 op_sel_hi:[0,0,0]
	v_mfma_scale_f32_16x16x128_f8f6f4 v[86:89], v[2:9], v[200:207], v[86:89], v190, v191 op_sel_hi:[0,0,0]
	v_mfma_scale_f32_16x16x128_f8f6f4 v[78:81], v[10:17], v[200:207], v[78:81], v190, v191 op_sel_hi:[0,0,0]
	v_mfma_scale_f32_16x16x128_f8f6f4 v[70:73], v[2:9], v[208:215], v[70:73], v190, v191 op_sel_hi:[0,0,0]
	v_mfma_scale_f32_16x16x128_f8f6f4 v[62:65], v[10:17], v[208:215], v[62:65], v190, v191 op_sel_hi:[0,0,0]
	v_mfma_scale_f32_16x16x128_f8f6f4 v[54:57], v[2:9], v[216:223], v[54:57], v190, v191 op_sel_hi:[0,0,0]
	v_mfma_scale_f32_16x16x128_f8f6f4 v[46:49], v[10:17], v[216:223], v[46:49], v190, v191 op_sel_hi:[0,0,0]
	s_setprio 0
	s_setprio 1
	v_mfma_scale_f32_16x16x128_f8f6f4 v[82:85], v[18:25], v[192:199], v[82:85], v190, v191 op_sel_hi:[0,0,0]
	v_mfma_scale_f32_16x16x128_f8f6f4 v[74:77], v[26:33], v[192:199], v[74:77], v190, v191 op_sel_hi:[0,0,0]
	v_mfma_scale_f32_16x16x128_f8f6f4 v[66:69], v[18:25], v[200:207], v[66:69], v190, v191 op_sel_hi:[0,0,0]
	v_mfma_scale_f32_16x16x128_f8f6f4 v[58:61], v[26:33], v[200:207], v[58:61], v190, v191 op_sel_hi:[0,0,0]
	v_mfma_scale_f32_16x16x128_f8f6f4 v[50:53], v[18:25], v[208:215], v[50:53], v190, v191 op_sel_hi:[0,0,0]
	v_mfma_scale_f32_16x16x128_f8f6f4 v[42:45], v[26:33], v[208:215], v[42:45], v190, v191 op_sel_hi:[0,0,0]
	v_mfma_scale_f32_16x16x128_f8f6f4 v[38:41], v[18:25], v[216:223], v[38:41], v190, v191 op_sel_hi:[0,0,0]
	v_mfma_scale_f32_16x16x128_f8f6f4 v[34:37], v[26:33], v[216:223], v[34:37], v190, v191 op_sel_hi:[0,0,0]
	s_setprio 0
	s_barrier
	s_add_u32 s6, s6, 0x100
	s_addc_u32 s7, s7, 0
	s_add_u32 s47, s47, 0x100
	s_addc_u32 s51, s51, 0
	s_cmp_ge_i32 s55, s93
	s_mov_b32 s8, s55
	s_cbranch_scc1 .Lpeel_exit_1803

.Lpeel_exit_1803:
	s_and_b64 vcc, exec, s[28:29]
	s_cbranch_vccz .LBB0_1806
	s_barrier
